# GEMM K-loops: back-edge rotation - loop counter update, exit test and loop-carried s_mov moved in front of the loop-back barrier
# baseline (speedup 1.0000x reference)
; #define PG8_STAGE(bufoff, gbase, voff) do { _Pragma("unroll") for (int _i = 0; _i < 2; ++_i) \
;         __builtin_amdgcn_global_load_lds((const unsigned*)((const char*)(gbase) + (voff)[_i]), (LAS unsigned*)(lds + (bufoff) + ldsw + _i * 8192), 16, 0, 0); } while (0)
; #define PG8_LDA(dst, b, h) do { _Pragma("unroll") for (int m = 0; m < 4; ++m) dst[m] = PG8_LD32(lds + PG8_SA(b, h) + aoff + m * 2048); } while (0)
; #define PG8_LDB(dst, b, h) do { _Pragma("unroll") for (int n = 0; n < 2; ++n) dst[n] = PG8_LD32(lds + PG8_SB(b, h) + boff + n * 2048); } while (0)
; #define PG8_WAIT_V(n) asm volatile("s_waitcnt vmcnt(" #n ")" ::: "memory")
; #define PG8_WAIT_L(n) asm volatile("s_waitcnt lgkmcnt(" #n ")" ::: "memory")
; #define PG8_BAR __builtin_amdgcn_s_barrier()
; #define PG8_SCHED __builtin_amdgcn_sched_barrier(0)
; #define PG8_STA(bufoff, nextflag, h, koff) do { if constexpr (Sched::GATHER) { unsigned _o[2]; _o[0] = (nextflag) ? nxtA[h][0] : curA[h][0]; _o[1] = (nextflag) ? nxtA[h][1] : curA[h][1]; PG8_STAGE(bufoff, Ab + (koff), _o); } \
;         else { PG8_STAGE(bufoff, ((nextflag) ? nA : cA) + (size_t)(h) * hstep + (koff), voffA); } } while (0)
; template <class Epi, class Sched, bool ALIGN_EPI, int DT>
; __device__ __forceinline__ void gemm_phase(LAS unsigned char* lds, const int KB, const Sched& S, const Epi& E) {
;     ...
;             const size_t k1 = (size_t)(t + 1) * kstep, k2 = last ? 0 : (size_t)(t + 2) * kstep, k3 = k2 + kstep;
;             const char* b2 = last ? nB : cB + (size_t)(t + 2) * kstep; const char* b3 = b2 + kstep;
;             PG8_LDB(B0, 0, 0); PG8_LDB(B1, 0, 1); PG8_SCHED; PG8_LDA(At, 0, 0); PG8_STA(PG8_SA(1, 1), false, 1, k1);
;             PG8_WAIT_V(8); PG8_WAIT_L(0); PG8_BAR; PG8_MMA(0, 0, At, B0); PG8_MMA(0, 1, At, B1); PG8_BAR; PG8_SCHED;
;             PG8_LDA(At, 0, 1); PG8_STAGE(PG8_SB(0, 0), b2, voffB); PG8_STAGE(PG8_SB(0, 1), b2 + hstep, voffB); PG8_STA(PG8_SA(0, 0), last, 0, k2);
;             PG8_WAIT_V(8); PG8_WAIT_L(0); PG8_BAR; PG8_MMA(1, 0, At, B0); PG8_MMA(1, 1, At, B1); PG8_BAR; PG8_SCHED;
.LBB0_193:
	ds_read_b128 v[152:155], v175
	ds_read_b128 v[156:159], v175 offset:1024
	ds_read_b128 v[160:163], v175 offset:2048
	ds_read_b128 v[164:167], v175 offset:3072
	ds_read_b128 v[168:171], v176
	ds_read_b128 v[182:185], v176 offset:1024
	ds_read_b128 v[186:189], v176 offset:2048
	ds_read_b128 v[190:193], v176 offset:3072
	s_add_u32 s38, s36, 0x100
	s_addc_u32 s39, s37, 0
	s_add_u32 s68, s25, s36
	s_addc_u32 s69, s66, s37
	s_cmp_eq_u32 s67, 12
	s_cselect_b64 s[42:43], -1, 0
	s_and_b64 s[40:41], s[42:43], exec
	s_cselect_b32 s70, 0, s38
	s_cselect_b32 s41, s0, s69
	s_cselect_b32 s40, s23, s68
	v_lshl_add_u64 v[228:229], v[148:149], 0, s[36:37]
	s_add_i32 m0, s45, 0xc000
	ds_read_b128 v[196:199], v177
	ds_read_b128 v[200:203], v177 offset:1024
	ds_read_b128 v[204:207], v177 offset:2048
	ds_read_b128 v[208:211], v177 offset:3072
	ds_read_b128 v[212:215], v177 offset:4096
	ds_read_b128 v[216:219], v177 offset:5120
	ds_read_b128 v[220:223], v177 offset:6144
	ds_read_b128 v[224:227], v177 offset:7168
	global_load_lds_dwordx4 v[228:229], off
	v_lshl_add_u64 v[228:229], v[150:151], 0, s[36:37]
	s_add_i32 m0, s45, 0xe000
	s_nop 0
	global_load_lds_dwordx4 v[228:229], off
	s_waitcnt vmcnt(8)
	s_waitcnt lgkmcnt(0)
	s_barrier
	s_setprio 1
	s_waitcnt lgkmcnt(0)
	v_mfma_i32_16x16x64_i8 v[126:129], v[152:155], v[196:199], v[126:129]
	v_mfma_i32_16x16x64_i8 v[122:125], v[160:163], v[196:199], v[122:125]
	v_mfma_i32_16x16x64_i8 v[110:113], v[152:155], v[204:207], v[110:113]
	v_mfma_i32_16x16x64_i8 v[106:109], v[160:163], v[204:207], v[106:109]
	v_mfma_i32_16x16x64_i8 v[94:97], v[152:155], v[212:215], v[94:97]
	v_mfma_i32_16x16x64_i8 v[90:93], v[160:163], v[212:215], v[90:93]
	v_mfma_i32_16x16x64_i8 v[78:81], v[152:155], v[220:223], v[78:81]
	v_mfma_i32_16x16x64_i8 v[74:77], v[160:163], v[220:223], v[74:77]
	v_mfma_i32_16x16x64_i8 v[126:129], v[156:159], v[200:203], v[126:129]
	v_mfma_i32_16x16x64_i8 v[122:125], v[164:167], v[200:203], v[122:125]
	v_mfma_i32_16x16x64_i8 v[110:113], v[156:159], v[208:211], v[110:113]
	v_mfma_i32_16x16x64_i8 v[106:109], v[164:167], v[208:211], v[106:109]
	v_mfma_i32_16x16x64_i8 v[94:97], v[156:159], v[216:219], v[94:97]
	v_mfma_i32_16x16x64_i8 v[90:93], v[164:167], v[216:219], v[90:93]
	v_mfma_i32_16x16x64_i8 v[78:81], v[156:159], v[224:227], v[78:81]
	v_mfma_i32_16x16x64_i8 v[74:77], v[164:167], v[224:227], v[74:77]
	s_setprio 0
	s_setprio 1
	v_mfma_i32_16x16x64_i8 v[118:121], v[168:171], v[196:199], v[118:121]
	v_mfma_i32_16x16x64_i8 v[114:117], v[186:189], v[196:199], v[114:117]
	v_mfma_i32_16x16x64_i8 v[102:105], v[168:171], v[204:207], v[102:105]
	v_mfma_i32_16x16x64_i8 v[98:101], v[186:189], v[204:207], v[98:101]
	v_mfma_i32_16x16x64_i8 v[86:89], v[168:171], v[212:215], v[86:89]
	v_mfma_i32_16x16x64_i8 v[82:85], v[186:189], v[212:215], v[82:85]
	v_mfma_i32_16x16x64_i8 v[70:73], v[168:171], v[220:223], v[70:73]
	v_mfma_i32_16x16x64_i8 v[66:69], v[186:189], v[220:223], v[66:69]
	v_mfma_i32_16x16x64_i8 v[118:121], v[182:185], v[200:203], v[118:121]
	v_mfma_i32_16x16x64_i8 v[114:117], v[190:193], v[200:203], v[114:117]
	v_mfma_i32_16x16x64_i8 v[102:105], v[182:185], v[208:211], v[102:105]
	v_mfma_i32_16x16x64_i8 v[98:101], v[190:193], v[208:211], v[98:101]
	v_mfma_i32_16x16x64_i8 v[86:89], v[182:185], v[216:219], v[86:89]
	v_mfma_i32_16x16x64_i8 v[82:85], v[190:193], v[216:219], v[82:85]
	v_mfma_i32_16x16x64_i8 v[70:73], v[182:185], v[224:227], v[70:73]
	v_mfma_i32_16x16x64_i8 v[66:69], v[190:193], v[224:227], v[66:69]
	s_setprio 0
	s_barrier
	s_add_i32 s36, s62, s5
	v_lshl_add_u64 v[228:229], s[40:41], 0, v[134:135]
	s_mov_b32 m0, s36
	ds_read_b128 v[196:199], v177 offset:16384
	ds_read_b128 v[200:203], v177 offset:17408
	ds_read_b128 v[204:207], v177 offset:18432
	ds_read_b128 v[208:211], v177 offset:19456
	ds_read_b128 v[212:215], v177 offset:20480
	ds_read_b128 v[216:219], v177 offset:21504
	ds_read_b128 v[220:223], v177 offset:22528
	ds_read_b128 v[224:227], v177 offset:23552
	global_load_lds_dwordx4 v[228:229], off
	s_add_i32 m0, s36, 0x2000
	s_add_u32 s36, s40, 0x40000
	v_lshl_add_u64 v[230:231], s[40:41], 0, v[132:133]
	s_addc_u32 s37, s41, 0
	s_add_i32 s68, s63, s5
	global_load_lds_dwordx4 v[230:231], off
	v_lshl_add_u64 v[232:233], s[36:37], 0, v[134:135]
	s_mov_b32 m0, s68
	s_nop 0
	global_load_lds_dwordx4 v[232:233], off
	v_lshl_add_u64 v[232:233], s[36:37], 0, v[132:133]
	s_add_i32 m0, s68, 0x2000
	s_and_b64 s[36:37], s[8:9], s[42:43]
	s_and_b64 s[36:37], s[36:37], exec
	s_cselect_b32 s36, s26, s34
	s_cselect_b32 s37, s27, s35
	s_add_u32 s36, s36, s70
	s_addc_u32 s37, s37, 0
	global_load_lds_dwordx4 v[232:233], off
	v_lshl_add_u64 v[232:233], s[36:37], 0, v[136:137]
	s_mov_b32 m0, s45
	v_lshl_add_u64 v[234:235], s[36:37], 0, v[138:139]
	global_load_lds_dwordx4 v[232:233], off
	s_mov_b32 m0, s46
	s_nop 0
	global_load_lds_dwordx4 v[234:235], off
	s_waitcnt vmcnt(8)
	s_waitcnt lgkmcnt(0)
	s_barrier
; #define PG8_LDA(dst, b, h) do { _Pragma("unroll") for (int m = 0; m < 4; ++m) dst[m] = PG8_LD32(lds + PG8_SA(b, h) + aoff + m * 2048); } while (0)
; #define PG8_LDB(dst, b, h) do { _Pragma("unroll") for (int n = 0; n < 2; ++n) dst[n] = PG8_LD32(lds + PG8_SB(b, h) + boff + n * 2048); } while (0)
; #define PG8_WAIT_V(n) asm volatile("s_waitcnt vmcnt(" #n ")" ::: "memory")
; #define PG8_WAIT_L(n) asm volatile("s_waitcnt lgkmcnt(" #n ")" ::: "memory")
; #define PG8_BAR __builtin_amdgcn_s_barrier()
; #define PG8_SCHED __builtin_amdgcn_sched_barrier(0)
; #define PG8_STA(bufoff, nextflag, h, koff) do { if constexpr (Sched::GATHER) { unsigned _o[2]; _o[0] = (nextflag) ? nxtA[h][0] : curA[h][0]; _o[1] = (nextflag) ? nxtA[h][1] : curA[h][1]; PG8_STAGE(bufoff, Ab + (koff), _o); } \
;         else { PG8_STAGE(bufoff, ((nextflag) ? nA : cA) + (size_t)(h) * hstep + (koff), voffA); } } while (0)
; template <class Epi, class Sched, bool ALIGN_EPI, int DT>
; __device__ __forceinline__ void gemm_phase(LAS unsigned char* lds, const int KB, const Sched& S, const Epi& E) {
;     ...
;             PG8_WAIT_V(8); PG8_WAIT_L(0); PG8_BAR; PG8_MMA(1, 0, At, B0); PG8_MMA(1, 1, At, B1); PG8_BAR; PG8_SCHED;
;             PG8_LDB(B0, 1, 0); PG8_LDB(B1, 1, 1); PG8_SCHED; PG8_LDA(At, 1, 0); PG8_STA(PG8_SA(0, 1), last, 1, k2);
;             PG8_WAIT_V(8); PG8_WAIT_L(0); PG8_BAR; PG8_MMA(0, 0, At, B0); PG8_MMA(0, 1, At, B1); PG8_BAR; PG8_SCHED;
	s_setprio 1
	s_waitcnt lgkmcnt(0)
	v_mfma_i32_16x16x64_i8 v[62:65], v[152:155], v[196:199], v[62:65]
	v_mfma_i32_16x16x64_i8 v[58:61], v[160:163], v[196:199], v[58:61]
	v_mfma_i32_16x16x64_i8 v[46:49], v[152:155], v[204:207], v[46:49]
	v_mfma_i32_16x16x64_i8 v[42:45], v[160:163], v[204:207], v[42:45]
	v_mfma_i32_16x16x64_i8 v[30:33], v[152:155], v[212:215], v[30:33]
	v_mfma_i32_16x16x64_i8 v[26:29], v[160:163], v[212:215], v[26:29]
	v_mfma_i32_16x16x64_i8 v[6:9], v[152:155], v[220:223], v[6:9]
	v_mfma_i32_16x16x64_i8 v[2:5], v[160:163], v[220:223], v[2:5]
	v_mfma_i32_16x16x64_i8 v[62:65], v[156:159], v[200:203], v[62:65]
	v_mfma_i32_16x16x64_i8 v[58:61], v[164:167], v[200:203], v[58:61]
	v_mfma_i32_16x16x64_i8 v[46:49], v[156:159], v[208:211], v[46:49]
	v_mfma_i32_16x16x64_i8 v[42:45], v[164:167], v[208:211], v[42:45]
	v_mfma_i32_16x16x64_i8 v[30:33], v[156:159], v[216:219], v[30:33]
	v_mfma_i32_16x16x64_i8 v[26:29], v[164:167], v[216:219], v[26:29]
	v_mfma_i32_16x16x64_i8 v[6:9], v[156:159], v[224:227], v[6:9]
	v_mfma_i32_16x16x64_i8 v[2:5], v[164:167], v[224:227], v[2:5]
	s_setprio 0
	s_setprio 1
	v_mfma_i32_16x16x64_i8 v[54:57], v[168:171], v[196:199], v[54:57]
	v_mfma_i32_16x16x64_i8 v[50:53], v[186:189], v[196:199], v[50:53]
	v_mfma_i32_16x16x64_i8 v[38:41], v[168:171], v[204:207], v[38:41]
	v_mfma_i32_16x16x64_i8 v[34:37], v[186:189], v[204:207], v[34:37]
	v_mfma_i32_16x16x64_i8 v[14:17], v[168:171], v[212:215], v[14:17]
	v_mfma_i32_16x16x64_i8 v[10:13], v[186:189], v[212:215], v[10:13]
	v_mfma_i32_16x16x64_i8 v[22:25], v[168:171], v[220:223], v[22:25]
	v_mfma_i32_16x16x64_i8 v[18:21], v[186:189], v[220:223], v[18:21]
	v_mfma_i32_16x16x64_i8 v[54:57], v[182:185], v[200:203], v[54:57]
	v_mfma_i32_16x16x64_i8 v[50:53], v[190:193], v[200:203], v[50:53]
	v_mfma_i32_16x16x64_i8 v[38:41], v[182:185], v[208:211], v[38:41]
	v_mfma_i32_16x16x64_i8 v[34:37], v[190:193], v[208:211], v[34:37]
	v_mfma_i32_16x16x64_i8 v[14:17], v[182:185], v[216:219], v[14:17]
	v_mfma_i32_16x16x64_i8 v[10:13], v[190:193], v[216:219], v[10:13]
	v_mfma_i32_16x16x64_i8 v[22:25], v[182:185], v[224:227], v[22:25]
	v_mfma_i32_16x16x64_i8 v[18:21], v[190:193], v[224:227], v[18:21]
	s_setprio 0
	s_barrier
	s_add_i32 s42, 0, 0x18000
	v_add_u32_e32 v1, s42, v173
	s_add_i32 s43, 0, 0x1c000
	ds_read_b128 v[152:155], v1
	ds_read_b128 v[156:159], v1 offset:1024
	ds_read_b128 v[160:163], v1 offset:2048
	ds_read_b128 v[164:167], v1 offset:3072
	v_add_u32_e32 v1, s43, v173
	ds_read_b128 v[168:171], v1
	ds_read_b128 v[182:185], v1 offset:1024
	ds_read_b128 v[186:189], v1 offset:2048
	ds_read_b128 v[190:193], v1 offset:3072
	s_add_u32 s36, s36, 0x40000
	s_addc_u32 s37, s37, 0
	s_mov_b32 m0, s47
	v_lshl_add_u64 v[236:237], s[36:37], 0, v[136:137]
	ds_read_b128 v[196:199], v177 offset:32768
	ds_read_b128 v[200:203], v177 offset:33792
	ds_read_b128 v[204:207], v177 offset:34816
	ds_read_b128 v[208:211], v177 offset:35840
	ds_read_b128 v[212:215], v177 offset:36864
	ds_read_b128 v[216:219], v177 offset:37888
	ds_read_b128 v[220:223], v177 offset:38912
	ds_read_b128 v[224:227], v177 offset:39936
	global_load_lds_dwordx4 v[236:237], off
	v_lshl_add_u64 v[236:237], s[36:37], 0, v[138:139]
	s_mov_b32 m0, s49
	s_nop 0
	global_load_lds_dwordx4 v[236:237], off
	s_waitcnt vmcnt(8)
	s_waitcnt lgkmcnt(0)
	s_barrier
	s_setprio 1
	s_waitcnt lgkmcnt(0)
	v_mfma_i32_16x16x64_i8 v[126:129], v[152:155], v[196:199], v[126:129]
	v_mfma_i32_16x16x64_i8 v[122:125], v[160:163], v[196:199], v[122:125]
	v_mfma_i32_16x16x64_i8 v[110:113], v[152:155], v[204:207], v[110:113]
	v_mfma_i32_16x16x64_i8 v[106:109], v[160:163], v[204:207], v[106:109]
	v_mfma_i32_16x16x64_i8 v[94:97], v[152:155], v[212:215], v[94:97]
	v_mfma_i32_16x16x64_i8 v[90:93], v[160:163], v[212:215], v[90:93]
	v_mfma_i32_16x16x64_i8 v[78:81], v[152:155], v[220:223], v[78:81]
	v_mfma_i32_16x16x64_i8 v[74:77], v[160:163], v[220:223], v[74:77]
	v_mfma_i32_16x16x64_i8 v[126:129], v[156:159], v[200:203], v[126:129]
	v_mfma_i32_16x16x64_i8 v[122:125], v[164:167], v[200:203], v[122:125]
	v_mfma_i32_16x16x64_i8 v[110:113], v[156:159], v[208:211], v[110:113]
	v_mfma_i32_16x16x64_i8 v[106:109], v[164:167], v[208:211], v[106:109]
	v_mfma_i32_16x16x64_i8 v[94:97], v[156:159], v[216:219], v[94:97]
	v_mfma_i32_16x16x64_i8 v[90:93], v[164:167], v[216:219], v[90:93]
	v_mfma_i32_16x16x64_i8 v[78:81], v[156:159], v[224:227], v[78:81]
	v_mfma_i32_16x16x64_i8 v[74:77], v[164:167], v[224:227], v[74:77]
	s_setprio 0
	s_setprio 1
	v_mfma_i32_16x16x64_i8 v[118:121], v[168:171], v[196:199], v[118:121]
	v_mfma_i32_16x16x64_i8 v[114:117], v[186:189], v[196:199], v[114:117]
	v_mfma_i32_16x16x64_i8 v[102:105], v[168:171], v[204:207], v[102:105]
	v_mfma_i32_16x16x64_i8 v[98:101], v[186:189], v[204:207], v[98:101]
	v_mfma_i32_16x16x64_i8 v[86:89], v[168:171], v[212:215], v[86:89]
	v_mfma_i32_16x16x64_i8 v[82:85], v[186:189], v[212:215], v[82:85]
	v_mfma_i32_16x16x64_i8 v[70:73], v[168:171], v[220:223], v[70:73]
	v_mfma_i32_16x16x64_i8 v[66:69], v[186:189], v[220:223], v[66:69]
	v_mfma_i32_16x16x64_i8 v[118:121], v[182:185], v[200:203], v[118:121]
	v_mfma_i32_16x16x64_i8 v[114:117], v[190:193], v[200:203], v[114:117]
	v_mfma_i32_16x16x64_i8 v[102:105], v[182:185], v[208:211], v[102:105]
	v_mfma_i32_16x16x64_i8 v[98:101], v[190:193], v[208:211], v[98:101]
	v_mfma_i32_16x16x64_i8 v[86:89], v[182:185], v[216:219], v[86:89]
	v_mfma_i32_16x16x64_i8 v[82:85], v[190:193], v[216:219], v[82:85]
	v_mfma_i32_16x16x64_i8 v[70:73], v[182:185], v[224:227], v[70:73]
	v_mfma_i32_16x16x64_i8 v[66:69], v[190:193], v[224:227], v[66:69]
	s_setprio 0
	s_barrier
; #define PG8_STAGE(bufoff, gbase, voff) do { _Pragma("unroll") for (int _i = 0; _i < 2; ++_i) \
;         __builtin_amdgcn_global_load_lds((const unsigned*)((const char*)(gbase) + (voff)[_i]), (LAS unsigned*)(lds + (bufoff) + ldsw + _i * 8192), 16, 0, 0); } while (0)
; #define PG8_LDA(dst, b, h) do { _Pragma("unroll") for (int m = 0; m < 4; ++m) dst[m] = PG8_LD32(lds + PG8_SA(b, h) + aoff + m * 2048); } while (0)
; #define PG8_WAIT_V(n) asm volatile("s_waitcnt vmcnt(" #n ")" ::: "memory")
; #define PG8_WAIT_L(n) asm volatile("s_waitcnt lgkmcnt(" #n ")" ::: "memory")
; #define PG8_BAR __builtin_amdgcn_s_barrier()
; #define PG8_SCHED __builtin_amdgcn_sched_barrier(0)
; #define PG8_STA(bufoff, nextflag, h, koff) do { if constexpr (Sched::GATHER) { unsigned _o[2]; _o[0] = (nextflag) ? nxtA[h][0] : curA[h][0]; _o[1] = (nextflag) ? nxtA[h][1] : curA[h][1]; PG8_STAGE(bufoff, Ab + (koff), _o); } \
;         else { PG8_STAGE(bufoff, ((nextflag) ? nA : cA) + (size_t)(h) * hstep + (koff), voffA); } } while (0)
; template <class Epi, class Sched, bool ALIGN_EPI, int DT>
; __device__ __forceinline__ void gemm_phase(LAS unsigned char* lds, const int KB, const Sched& S, const Epi& E) {
;     ...
;         for (int t = 0; t < nt; t += 2) {
;             const bool last = (t == nt - 2);
;             const size_t k1 = (size_t)(t + 1) * kstep, k2 = last ? 0 : (size_t)(t + 2) * kstep, k3 = k2 + kstep;
;     ...
;             PG8_LDA(At, 1, 1); PG8_STAGE(PG8_SB(1, 0), b3, voffB); PG8_STAGE(PG8_SB(1, 1), b3 + hstep, voffB); PG8_STA(PG8_SA(1, 0), last, 0, k3);
;             PG8_WAIT_V(8); PG8_WAIT_L(0); PG8_BAR; PG8_MMA(1, 0, At, B0); PG8_MMA(1, 1, At, B1); PG8_BAR; PG8_SCHED;
	s_add_i32 s36, s42, s5
	v_lshl_add_u64 v[228:229], v[228:229], 0, s[18:19]
	s_mov_b32 m0, s36
	ds_read_b128 v[196:199], v177 offset:49152
	ds_read_b128 v[200:203], v177 offset:50176
	ds_read_b128 v[204:207], v177 offset:51200
	ds_read_b128 v[208:211], v177 offset:52224
	ds_read_b128 v[212:215], v177 offset:53248
	ds_read_b128 v[216:219], v177 offset:54272
	ds_read_b128 v[220:223], v177 offset:55296
	ds_read_b128 v[224:227], v177 offset:56320
	global_load_lds_dwordx4 v[228:229], off
	s_add_i32 m0, s36, 0x2000
	s_add_u32 s36, s40, 0x40080
	v_lshl_add_u64 v[228:229], v[230:231], 0, s[18:19]
	s_addc_u32 s37, s41, 0
	s_add_i32 s40, s43, s5
	global_load_lds_dwordx4 v[228:229], off
	v_lshl_add_u64 v[228:229], s[36:37], 0, v[134:135]
	s_mov_b32 m0, s40
	s_nop 0
	global_load_lds_dwordx4 v[228:229], off
	v_lshl_add_u64 v[228:229], s[36:37], 0, v[132:133]
	s_add_i32 m0, s40, 0x2000
	s_nop 0
	global_load_lds_dwordx4 v[228:229], off
	v_lshl_add_u64 v[228:229], v[232:233], 0, s[18:19]
	s_mov_b32 m0, s55
	s_nop 0
	global_load_lds_dwordx4 v[228:229], off
	v_lshl_add_u64 v[228:229], v[234:235], 0, s[18:19]
	s_mov_b32 m0, s56
	s_nop 0
	global_load_lds_dwordx4 v[228:229], off
	s_waitcnt vmcnt(8)
	s_waitcnt lgkmcnt(0)
	s_barrier
	s_setprio 1
	s_waitcnt lgkmcnt(0)
	v_mfma_i32_16x16x64_i8 v[62:65], v[152:155], v[196:199], v[62:65]
	v_mfma_i32_16x16x64_i8 v[58:61], v[160:163], v[196:199], v[58:61]
	v_mfma_i32_16x16x64_i8 v[46:49], v[152:155], v[204:207], v[46:49]
	v_mfma_i32_16x16x64_i8 v[42:45], v[160:163], v[204:207], v[42:45]
	v_mfma_i32_16x16x64_i8 v[30:33], v[152:155], v[212:215], v[30:33]
	v_mfma_i32_16x16x64_i8 v[26:29], v[160:163], v[212:215], v[26:29]
	v_mfma_i32_16x16x64_i8 v[6:9], v[152:155], v[220:223], v[6:9]
	v_mfma_i32_16x16x64_i8 v[2:5], v[160:163], v[220:223], v[2:5]
	v_mfma_i32_16x16x64_i8 v[62:65], v[156:159], v[200:203], v[62:65]
	v_mfma_i32_16x16x64_i8 v[58:61], v[164:167], v[200:203], v[58:61]
	v_mfma_i32_16x16x64_i8 v[46:49], v[156:159], v[208:211], v[46:49]
	v_mfma_i32_16x16x64_i8 v[42:45], v[164:167], v[208:211], v[42:45]
	v_mfma_i32_16x16x64_i8 v[30:33], v[156:159], v[216:219], v[30:33]
	v_mfma_i32_16x16x64_i8 v[26:29], v[164:167], v[216:219], v[26:29]
	v_mfma_i32_16x16x64_i8 v[6:9], v[156:159], v[224:227], v[6:9]
	v_mfma_i32_16x16x64_i8 v[2:5], v[164:167], v[224:227], v[2:5]
	s_setprio 0
	s_setprio 1
	v_mfma_i32_16x16x64_i8 v[54:57], v[168:171], v[196:199], v[54:57]
	v_mfma_i32_16x16x64_i8 v[50:53], v[186:189], v[196:199], v[50:53]
	v_mfma_i32_16x16x64_i8 v[38:41], v[168:171], v[204:207], v[38:41]
	v_mfma_i32_16x16x64_i8 v[34:37], v[186:189], v[204:207], v[34:37]
	v_mfma_i32_16x16x64_i8 v[14:17], v[168:171], v[212:215], v[14:17]
	v_mfma_i32_16x16x64_i8 v[10:13], v[186:189], v[212:215], v[10:13]
	v_mfma_i32_16x16x64_i8 v[22:25], v[168:171], v[220:223], v[22:25]
	v_mfma_i32_16x16x64_i8 v[18:21], v[186:189], v[220:223], v[18:21]
	v_mfma_i32_16x16x64_i8 v[54:57], v[182:185], v[200:203], v[54:57]
	v_mfma_i32_16x16x64_i8 v[50:53], v[190:193], v[200:203], v[50:53]
	v_mfma_i32_16x16x64_i8 v[38:41], v[182:185], v[208:211], v[38:41]
	v_mfma_i32_16x16x64_i8 v[34:37], v[190:193], v[208:211], v[34:37]
	v_mfma_i32_16x16x64_i8 v[14:17], v[182:185], v[216:219], v[14:17]
	v_mfma_i32_16x16x64_i8 v[10:13], v[190:193], v[216:219], v[10:13]
	v_mfma_i32_16x16x64_i8 v[22:25], v[182:185], v[224:227], v[22:25]
	v_mfma_i32_16x16x64_i8 v[18:21], v[190:193], v[224:227], v[18:21]
	s_setprio 0
	s_add_i32 s67, s67, 2
	s_cmp_gt_u32 s67, 13
	s_mov_b64 s[36:37], s[38:39]
	s_barrier
	s_cbranch_scc0 .LBB0_193
	s_and_b64 vcc, exec, s[20:21]
	s_cbranch_vccz .LBB0_196
	s_barrier

; #define PG8_STAGE(bufoff, gbase, voff) do { _Pragma("unroll") for (int _i = 0; _i < 2; ++_i) \
;         __builtin_amdgcn_global_load_lds((const unsigned*)((const char*)(gbase) + (voff)[_i]), (LAS unsigned*)(lds + (bufoff) + ldsw + _i * 8192), 16, 0, 0); } while (0)
; #define PG8_LDA(dst, b, h) do { _Pragma("unroll") for (int m = 0; m < 4; ++m) dst[m] = PG8_LD32(lds + PG8_SA(b, h) + aoff + m * 2048); } while (0)
; #define PG8_LDB(dst, b, h) do { _Pragma("unroll") for (int n = 0; n < 2; ++n) dst[n] = PG8_LD32(lds + PG8_SB(b, h) + boff + n * 2048); } while (0)
; #define PG8_WAIT_V(n) asm volatile("s_waitcnt vmcnt(" #n ")" ::: "memory")
; #define PG8_WAIT_L(n) asm volatile("s_waitcnt lgkmcnt(" #n ")" ::: "memory")
; #define PG8_BAR __builtin_amdgcn_s_barrier()
; #define PG8_SCHED __builtin_amdgcn_sched_barrier(0)
; #define PG8_STA(bufoff, nextflag, h, koff) do { if constexpr (Sched::GATHER) { unsigned _o[2]; _o[0] = (nextflag) ? nxtA[h][0] : curA[h][0]; _o[1] = (nextflag) ? nxtA[h][1] : curA[h][1]; PG8_STAGE(bufoff, Ab + (koff), _o); } \
;         else { PG8_STAGE(bufoff, ((nextflag) ? nA : cA) + (size_t)(h) * hstep + (koff), voffA); } } while (0)
; template <class Epi, class Sched, bool ALIGN_EPI, int DT>
; __device__ __forceinline__ void gemm_phase(LAS unsigned char* lds, const int KB, const Sched& S, const Epi& E) {
;     ...
;             const size_t k1 = (size_t)(t + 1) * kstep, k2 = last ? 0 : (size_t)(t + 2) * kstep, k3 = k2 + kstep;
;             const char* b2 = last ? nB : cB + (size_t)(t + 2) * kstep; const char* b3 = b2 + kstep;
;             PG8_LDB(B0, 0, 0); PG8_LDB(B1, 0, 1); PG8_SCHED; PG8_LDA(At, 0, 0); PG8_STA(PG8_SA(1, 1), false, 1, k1);
;             PG8_WAIT_V(8); PG8_WAIT_L(0); PG8_BAR; PG8_MMA(0, 0, At, B0); PG8_MMA(0, 1, At, B1); PG8_BAR; PG8_SCHED;
;             PG8_LDA(At, 0, 1); PG8_STAGE(PG8_SB(0, 0), b2, voffB); PG8_STAGE(PG8_SB(0, 1), b2 + hstep, voffB); PG8_STA(PG8_SA(0, 0), last, 0, k2);
;             PG8_WAIT_V(8); PG8_WAIT_L(0); PG8_BAR; PG8_MMA(1, 0, At, B0); PG8_MMA(1, 1, At, B1); PG8_BAR; PG8_SCHED;
.LBB0_1018:
	ds_read_b128 v[18:21], v193
	ds_read_b128 v[22:25], v193 offset:1024
	ds_read_b128 v[26:29], v193 offset:2048
	ds_read_b128 v[30:33], v193 offset:3072
	ds_read_b128 v[2:5], v195
	ds_read_b128 v[6:9], v195 offset:1024
	ds_read_b128 v[10:13], v195 offset:2048
	ds_read_b128 v[14:17], v195 offset:3072
	s_add_u32 s34, s38, 0x100
	s_addc_u32 s35, s39, 0
	s_add_u32 s68, s63, s38
	s_addc_u32 s69, s66, s39
	s_cmp_eq_u32 s67, 12
	s_cselect_b64 s[40:41], -1, 0
	s_and_b64 s[36:37], s[40:41], exec
	s_cselect_b32 s37, s21, s69
	s_cselect_b32 s36, s23, s68
	s_cselect_b32 s68, 0, s35
	s_cselect_b32 s69, 0, s34
	v_lshl_add_u64 v[222:223], v[178:179], 0, s[38:39]
	s_add_i32 m0, s29, 0xc000
	ds_read_b128 v[182:185], v196
	ds_read_b128 v[186:189], v196 offset:1024
	ds_read_b128 v[198:201], v196 offset:2048
	ds_read_b128 v[202:205], v196 offset:3072
	ds_read_b128 v[206:209], v196 offset:4096
	ds_read_b128 v[210:213], v196 offset:5120
	ds_read_b128 v[214:217], v196 offset:6144
	ds_read_b128 v[218:221], v196 offset:7168
	global_load_lds_dwordx4 v[222:223], off
	v_lshl_add_u64 v[222:223], v[180:181], 0, s[38:39]
	s_add_i32 m0, s29, 0xe000
	s_nop 0
	global_load_lds_dwordx4 v[222:223], off
	s_waitcnt vmcnt(8)
	s_waitcnt lgkmcnt(0)
	s_barrier
	s_setprio 1
	s_waitcnt lgkmcnt(0)
	v_mfma_scale_f32_16x16x128_f8f6f4 v[158:161], v[18:25], v[182:189], v[158:161], v190, v190 op_sel_hi:[0,0,0]
	v_mfma_scale_f32_16x16x128_f8f6f4 v[154:157], v[26:33], v[182:189], v[154:157], v190, v190 op_sel_hi:[0,0,0]
	v_mfma_scale_f32_16x16x128_f8f6f4 v[150:153], v[18:25], v[198:205], v[150:153], v190, v190 op_sel_hi:[0,0,0]
	v_mfma_scale_f32_16x16x128_f8f6f4 v[142:145], v[26:33], v[198:205], v[142:145], v190, v190 op_sel_hi:[0,0,0]
	v_mfma_scale_f32_16x16x128_f8f6f4 v[134:137], v[18:25], v[206:213], v[134:137], v190, v190 op_sel_hi:[0,0,0]
	v_mfma_scale_f32_16x16x128_f8f6f4 v[126:129], v[26:33], v[206:213], v[126:129], v190, v190 op_sel_hi:[0,0,0]
	v_mfma_scale_f32_16x16x128_f8f6f4 v[118:121], v[18:25], v[214:221], v[118:121], v190, v190 op_sel_hi:[0,0,0]
	v_mfma_scale_f32_16x16x128_f8f6f4 v[110:113], v[26:33], v[214:221], v[110:113], v190, v190 op_sel_hi:[0,0,0]
	s_setprio 0
	s_setprio 1
	v_mfma_scale_f32_16x16x128_f8f6f4 v[146:149], v[2:9], v[182:189], v[146:149], v190, v190 op_sel_hi:[0,0,0]
	v_mfma_scale_f32_16x16x128_f8f6f4 v[138:141], v[10:17], v[182:189], v[138:141], v190, v190 op_sel_hi:[0,0,0]
	v_mfma_scale_f32_16x16x128_f8f6f4 v[130:133], v[2:9], v[198:205], v[130:133], v190, v190 op_sel_hi:[0,0,0]
	v_mfma_scale_f32_16x16x128_f8f6f4 v[122:125], v[10:17], v[198:205], v[122:125], v190, v190 op_sel_hi:[0,0,0]
	v_mfma_scale_f32_16x16x128_f8f6f4 v[114:117], v[2:9], v[206:213], v[114:117], v190, v190 op_sel_hi:[0,0,0]
	v_mfma_scale_f32_16x16x128_f8f6f4 v[106:109], v[10:17], v[206:213], v[106:109], v190, v190 op_sel_hi:[0,0,0]
	v_mfma_scale_f32_16x16x128_f8f6f4 v[102:105], v[2:9], v[214:221], v[102:105], v190, v190 op_sel_hi:[0,0,0]
	v_mfma_scale_f32_16x16x128_f8f6f4 v[98:101], v[10:17], v[214:221], v[98:101], v190, v190 op_sel_hi:[0,0,0]
	s_setprio 0
	s_barrier
	s_add_i32 s38, s53, s42
	v_lshl_add_u64 v[182:183], s[36:37], 0, v[162:163]
	s_mov_b32 m0, s38
	ds_read_b128 v[198:201], v196 offset:16384
	ds_read_b128 v[202:205], v196 offset:17408
	ds_read_b128 v[206:209], v196 offset:18432
	ds_read_b128 v[210:213], v196 offset:19456
	ds_read_b128 v[214:217], v196 offset:20480
	ds_read_b128 v[218:221], v196 offset:21504
	ds_read_b128 v[222:225], v196 offset:22528
	ds_read_b128 v[226:229], v196 offset:23552
	global_load_lds_dwordx4 v[182:183], off
	s_add_i32 m0, s38, 0x2000
	s_add_u32 s38, s36, 0x40000
	v_lshl_add_u64 v[184:185], s[36:37], 0, v[164:165]
	s_addc_u32 s39, s37, 0
	s_add_i32 s70, s54, s42
	global_load_lds_dwordx4 v[184:185], off
	v_lshl_add_u64 v[186:187], s[38:39], 0, v[162:163]
	s_mov_b32 m0, s70
	s_nop 0
	global_load_lds_dwordx4 v[186:187], off
	v_lshl_add_u64 v[186:187], s[38:39], 0, v[164:165]
	s_add_i32 m0, s70, 0x2000
	s_and_b64 s[38:39], s[6:7], s[40:41]
	s_and_b64 s[38:39], s[38:39], exec
	s_cselect_b32 s38, s24, s30
	s_cselect_b32 s39, s25, s31
	s_add_u32 s38, s38, s69
	s_addc_u32 s39, s39, s68
	global_load_lds_dwordx4 v[186:187], off
	v_lshl_add_u64 v[186:187], s[38:39], 0, v[166:167]
	s_mov_b32 m0, s29
	v_lshl_add_u64 v[188:189], s[38:39], 0, v[168:169]
	global_load_lds_dwordx4 v[186:187], off
	s_mov_b32 m0, s43
	s_nop 0
	global_load_lds_dwordx4 v[188:189], off
	s_waitcnt vmcnt(8)
	s_waitcnt lgkmcnt(0)
	s_barrier
	s_setprio 1
	s_waitcnt lgkmcnt(0)
	v_mfma_scale_f32_16x16x128_f8f6f4 v[94:97], v[18:25], v[198:205], v[94:97], v190, v190 op_sel_hi:[0,0,0]
	v_mfma_scale_f32_16x16x128_f8f6f4 v[90:93], v[26:33], v[198:205], v[90:93], v190, v190 op_sel_hi:[0,0,0]
	v_mfma_scale_f32_16x16x128_f8f6f4 v[86:89], v[18:25], v[206:213], v[86:89], v190, v190 op_sel_hi:[0,0,0]
	v_mfma_scale_f32_16x16x128_f8f6f4 v[78:81], v[26:33], v[206:213], v[78:81], v190, v190 op_sel_hi:[0,0,0]
	v_mfma_scale_f32_16x16x128_f8f6f4 v[62:65], v[18:25], v[214:221], v[62:65], v190, v190 op_sel_hi:[0,0,0]
	v_mfma_scale_f32_16x16x128_f8f6f4 v[54:57], v[26:33], v[214:221], v[54:57], v190, v190 op_sel_hi:[0,0,0]
	v_mfma_scale_f32_16x16x128_f8f6f4 v[46:49], v[18:25], v[222:229], v[46:49], v190, v190 op_sel_hi:[0,0,0]
	v_mfma_scale_f32_16x16x128_f8f6f4 v[38:41], v[26:33], v[222:229], v[38:41], v190, v190 op_sel_hi:[0,0,0]
	s_setprio 0
	s_setprio 1
	v_mfma_scale_f32_16x16x128_f8f6f4 v[82:85], v[2:9], v[198:205], v[82:85], v190, v190 op_sel_hi:[0,0,0]
	v_mfma_scale_f32_16x16x128_f8f6f4 v[74:77], v[10:17], v[198:205], v[74:77], v190, v190 op_sel_hi:[0,0,0]
	v_mfma_scale_f32_16x16x128_f8f6f4 v[58:61], v[2:9], v[206:213], v[58:61], v190, v190 op_sel_hi:[0,0,0]
	v_mfma_scale_f32_16x16x128_f8f6f4 v[50:53], v[10:17], v[206:213], v[50:53], v190, v190 op_sel_hi:[0,0,0]
	v_mfma_scale_f32_16x16x128_f8f6f4 v[42:45], v[2:9], v[214:221], v[42:45], v190, v190 op_sel_hi:[0,0,0]
	v_mfma_scale_f32_16x16x128_f8f6f4 v[34:37], v[10:17], v[214:221], v[34:37], v190, v190 op_sel_hi:[0,0,0]
	v_mfma_scale_f32_16x16x128_f8f6f4 v[70:73], v[2:9], v[222:229], v[70:73], v190, v190 op_sel_hi:[0,0,0]
	v_mfma_scale_f32_16x16x128_f8f6f4 v[66:69], v[10:17], v[222:229], v[66:69], v190, v190 op_sel_hi:[0,0,0]
	s_setprio 0
	s_barrier
; #define PG8_STAGE(bufoff, gbase, voff) do { _Pragma("unroll") for (int _i = 0; _i < 2; ++_i) \
;         __builtin_amdgcn_global_load_lds((const unsigned*)((const char*)(gbase) + (voff)[_i]), (LAS unsigned*)(lds + (bufoff) + ldsw + _i * 8192), 16, 0, 0); } while (0)
; #define PG8_LDA(dst, b, h) do { _Pragma("unroll") for (int m = 0; m < 4; ++m) dst[m] = PG8_LD32(lds + PG8_SA(b, h) + aoff + m * 2048); } while (0)
; #define PG8_LDB(dst, b, h) do { _Pragma("unroll") for (int n = 0; n < 2; ++n) dst[n] = PG8_LD32(lds + PG8_SB(b, h) + boff + n * 2048); } while (0)
; #define PG8_WAIT_V(n) asm volatile("s_waitcnt vmcnt(" #n ")" ::: "memory")
; #define PG8_WAIT_L(n) asm volatile("s_waitcnt lgkmcnt(" #n ")" ::: "memory")
; #define PG8_BAR __builtin_amdgcn_s_barrier()
; #define PG8_SCHED __builtin_amdgcn_sched_barrier(0)
; #define PG8_STA(bufoff, nextflag, h, koff) do { if constexpr (Sched::GATHER) { unsigned _o[2]; _o[0] = (nextflag) ? nxtA[h][0] : curA[h][0]; _o[1] = (nextflag) ? nxtA[h][1] : curA[h][1]; PG8_STAGE(bufoff, Ab + (koff), _o); } \
;         else { PG8_STAGE(bufoff, ((nextflag) ? nA : cA) + (size_t)(h) * hstep + (koff), voffA); } } while (0)
; template <class Epi, class Sched, bool ALIGN_EPI, int DT>
; __device__ __forceinline__ void gemm_phase(LAS unsigned char* lds, const int KB, const Sched& S, const Epi& E) {
;     ...
;         for (int t = 0; t < nt; t += 2) {
;             const bool last = (t == nt - 2);
;             const size_t k1 = (size_t)(t + 1) * kstep, k2 = last ? 0 : (size_t)(t + 2) * kstep, k3 = k2 + kstep;
;     ...
;             PG8_LDB(B0, 1, 0); PG8_LDB(B1, 1, 1); PG8_SCHED; PG8_LDA(At, 1, 0); PG8_STA(PG8_SA(0, 1), last, 1, k2);
;             PG8_WAIT_V(8); PG8_WAIT_L(0); PG8_BAR; PG8_MMA(0, 0, At, B0); PG8_MMA(0, 1, At, B1); PG8_BAR; PG8_SCHED;
;             PG8_LDA(At, 1, 1); PG8_STAGE(PG8_SB(1, 0), b3, voffB); PG8_STAGE(PG8_SB(1, 1), b3 + hstep, voffB); PG8_STA(PG8_SA(1, 0), last, 0, k3);
;             PG8_WAIT_V(8); PG8_WAIT_L(0); PG8_BAR; PG8_MMA(1, 0, At, B0); PG8_MMA(1, 1, At, B1); PG8_BAR; PG8_SCHED;
	s_add_i32 s40, 0, 0x18000
	s_add_i32 s41, 0, 0x1c000
	v_add_u32_e32 v14, s40, v191
	v_add_u32_e32 v30, s41, v191
	ds_read_b128 v[2:5], v14
	ds_read_b128 v[6:9], v14 offset:1024
	ds_read_b128 v[10:13], v14 offset:2048
	ds_read_b128 v[14:17], v14 offset:3072
	ds_read_b128 v[18:21], v30
	ds_read_b128 v[22:25], v30 offset:1024
	ds_read_b128 v[26:29], v30 offset:2048
	ds_read_b128 v[30:33], v30 offset:3072
	s_add_u32 s38, s38, 0x40000
	s_addc_u32 s39, s39, 0
	s_mov_b32 m0, s44
	v_lshl_add_u64 v[230:231], s[38:39], 0, v[166:167]
	ds_read_b128 v[198:201], v196 offset:32768
	ds_read_b128 v[202:205], v196 offset:33792
	ds_read_b128 v[206:209], v196 offset:34816
	ds_read_b128 v[210:213], v196 offset:35840
	ds_read_b128 v[214:217], v196 offset:36864
	ds_read_b128 v[218:221], v196 offset:37888
	ds_read_b128 v[222:225], v196 offset:38912
	ds_read_b128 v[226:229], v196 offset:39936
	global_load_lds_dwordx4 v[230:231], off
	v_lshl_add_u64 v[230:231], s[38:39], 0, v[168:169]
	s_mov_b32 m0, s45
	s_nop 0
	global_load_lds_dwordx4 v[230:231], off
	s_waitcnt vmcnt(8)
	s_waitcnt lgkmcnt(0)
	s_barrier
	s_setprio 1
	s_waitcnt lgkmcnt(0)
	v_mfma_scale_f32_16x16x128_f8f6f4 v[158:161], v[2:9], v[198:205], v[158:161], v190, v190 op_sel_hi:[0,0,0]
	v_mfma_scale_f32_16x16x128_f8f6f4 v[154:157], v[10:17], v[198:205], v[154:157], v190, v190 op_sel_hi:[0,0,0]
	v_mfma_scale_f32_16x16x128_f8f6f4 v[150:153], v[2:9], v[206:213], v[150:153], v190, v190 op_sel_hi:[0,0,0]
	v_mfma_scale_f32_16x16x128_f8f6f4 v[142:145], v[10:17], v[206:213], v[142:145], v190, v190 op_sel_hi:[0,0,0]
	v_mfma_scale_f32_16x16x128_f8f6f4 v[134:137], v[2:9], v[214:221], v[134:137], v190, v190 op_sel_hi:[0,0,0]
	v_mfma_scale_f32_16x16x128_f8f6f4 v[126:129], v[10:17], v[214:221], v[126:129], v190, v190 op_sel_hi:[0,0,0]
	v_mfma_scale_f32_16x16x128_f8f6f4 v[118:121], v[2:9], v[222:229], v[118:121], v190, v190 op_sel_hi:[0,0,0]
	v_mfma_scale_f32_16x16x128_f8f6f4 v[110:113], v[10:17], v[222:229], v[110:113], v190, v190 op_sel_hi:[0,0,0]
	s_setprio 0
	s_setprio 1
	v_mfma_scale_f32_16x16x128_f8f6f4 v[146:149], v[18:25], v[198:205], v[146:149], v190, v190 op_sel_hi:[0,0,0]
	v_mfma_scale_f32_16x16x128_f8f6f4 v[138:141], v[26:33], v[198:205], v[138:141], v190, v190 op_sel_hi:[0,0,0]
	v_mfma_scale_f32_16x16x128_f8f6f4 v[130:133], v[18:25], v[206:213], v[130:133], v190, v190 op_sel_hi:[0,0,0]
	v_mfma_scale_f32_16x16x128_f8f6f4 v[122:125], v[26:33], v[206:213], v[122:125], v190, v190 op_sel_hi:[0,0,0]
	v_mfma_scale_f32_16x16x128_f8f6f4 v[114:117], v[18:25], v[214:221], v[114:117], v190, v190 op_sel_hi:[0,0,0]
	v_mfma_scale_f32_16x16x128_f8f6f4 v[106:109], v[26:33], v[214:221], v[106:109], v190, v190 op_sel_hi:[0,0,0]
	v_mfma_scale_f32_16x16x128_f8f6f4 v[102:105], v[18:25], v[222:229], v[102:105], v190, v190 op_sel_hi:[0,0,0]
	v_mfma_scale_f32_16x16x128_f8f6f4 v[98:101], v[26:33], v[222:229], v[98:101], v190, v190 op_sel_hi:[0,0,0]
	s_setprio 0
	s_barrier
	s_add_i32 s38, s40, s42
	v_lshl_add_u64 v[182:183], v[182:183], 0, s[10:11]
	s_mov_b32 m0, s38
	ds_read_b128 v[198:201], v196 offset:49152
	ds_read_b128 v[202:205], v196 offset:50176
	ds_read_b128 v[206:209], v196 offset:51200
	ds_read_b128 v[210:213], v196 offset:52224
	ds_read_b128 v[214:217], v196 offset:53248
	ds_read_b128 v[218:221], v196 offset:54272
	ds_read_b128 v[222:225], v196 offset:55296
	ds_read_b128 v[226:229], v196 offset:56320
	global_load_lds_dwordx4 v[182:183], off
	s_add_i32 m0, s38, 0x2000
	s_add_u32 s36, s36, 0x40080
	v_lshl_add_u64 v[182:183], v[184:185], 0, s[10:11]
	s_addc_u32 s37, s37, 0
	s_add_i32 s38, s41, s42
	global_load_lds_dwordx4 v[182:183], off
	v_lshl_add_u64 v[182:183], s[36:37], 0, v[162:163]
	s_mov_b32 m0, s38
	s_nop 0
	global_load_lds_dwordx4 v[182:183], off
	v_lshl_add_u64 v[182:183], s[36:37], 0, v[164:165]
	s_add_i32 m0, s38, 0x2000
	s_nop 0
	global_load_lds_dwordx4 v[182:183], off
	v_lshl_add_u64 v[182:183], v[186:187], 0, s[10:11]
	s_mov_b32 m0, s47
	s_nop 0
	global_load_lds_dwordx4 v[182:183], off
	v_lshl_add_u64 v[182:183], v[188:189], 0, s[10:11]
	s_mov_b32 m0, s49
	s_nop 0
	global_load_lds_dwordx4 v[182:183], off
	s_waitcnt vmcnt(8)
	s_waitcnt lgkmcnt(0)
	s_barrier
	s_setprio 1
	s_waitcnt lgkmcnt(0)
	v_mfma_scale_f32_16x16x128_f8f6f4 v[94:97], v[2:9], v[198:205], v[94:97], v190, v190 op_sel_hi:[0,0,0]
	v_mfma_scale_f32_16x16x128_f8f6f4 v[90:93], v[10:17], v[198:205], v[90:93], v190, v190 op_sel_hi:[0,0,0]
	v_mfma_scale_f32_16x16x128_f8f6f4 v[86:89], v[2:9], v[206:213], v[86:89], v190, v190 op_sel_hi:[0,0,0]
	v_mfma_scale_f32_16x16x128_f8f6f4 v[78:81], v[10:17], v[206:213], v[78:81], v190, v190 op_sel_hi:[0,0,0]
	v_mfma_scale_f32_16x16x128_f8f6f4 v[62:65], v[2:9], v[214:221], v[62:65], v190, v190 op_sel_hi:[0,0,0]
	v_mfma_scale_f32_16x16x128_f8f6f4 v[54:57], v[10:17], v[214:221], v[54:57], v190, v190 op_sel_hi:[0,0,0]
	v_mfma_scale_f32_16x16x128_f8f6f4 v[46:49], v[2:9], v[222:229], v[46:49], v190, v190 op_sel_hi:[0,0,0]
	v_mfma_scale_f32_16x16x128_f8f6f4 v[38:41], v[10:17], v[222:229], v[38:41], v190, v190 op_sel_hi:[0,0,0]
	s_setprio 0
	s_setprio 1
	v_mfma_scale_f32_16x16x128_f8f6f4 v[82:85], v[18:25], v[198:205], v[82:85], v190, v190 op_sel_hi:[0,0,0]
	v_mfma_scale_f32_16x16x128_f8f6f4 v[74:77], v[26:33], v[198:205], v[74:77], v190, v190 op_sel_hi:[0,0,0]
	v_mfma_scale_f32_16x16x128_f8f6f4 v[58:61], v[18:25], v[206:213], v[58:61], v190, v190 op_sel_hi:[0,0,0]
	v_mfma_scale_f32_16x16x128_f8f6f4 v[50:53], v[26:33], v[206:213], v[50:53], v190, v190 op_sel_hi:[0,0,0]
	v_mfma_scale_f32_16x16x128_f8f6f4 v[42:45], v[18:25], v[214:221], v[42:45], v190, v190 op_sel_hi:[0,0,0]
	v_mfma_scale_f32_16x16x128_f8f6f4 v[34:37], v[26:33], v[214:221], v[34:37], v190, v190 op_sel_hi:[0,0,0]
	v_mfma_scale_f32_16x16x128_f8f6f4 v[70:73], v[18:25], v[222:229], v[70:73], v190, v190 op_sel_hi:[0,0,0]
	v_mfma_scale_f32_16x16x128_f8f6f4 v[66:69], v[26:33], v[222:229], v[66:69], v190, v190 op_sel_hi:[0,0,0]
	s_setprio 0
	s_add_i32 s67, s67, 2
	s_cmp_gt_u32 s67, 13
	s_mov_b64 s[38:39], s[34:35]
	s_barrier
	s_cbranch_scc0 .LBB0_1018
	s_and_b64 vcc, exec, s[12:13]
	s_cbranch_vccz .LBB0_1021
	s_barrier

; #define PG8_STAGE(bufoff, gbase, voff) do { _Pragma("unroll") for (int _i = 0; _i < 2; ++_i) \
;         __builtin_amdgcn_global_load_lds((const unsigned*)((const char*)(gbase) + (voff)[_i]), (LAS unsigned*)(lds + (bufoff) + ldsw + _i * 8192), 16, 0, 0); } while (0)
; #define PG8_LDA(dst, b, h) do { _Pragma("unroll") for (int m = 0; m < 4; ++m) dst[m] = PG8_LD32(lds + PG8_SA(b, h) + aoff + m * 2048); } while (0)
; #define PG8_LDB(dst, b, h) do { _Pragma("unroll") for (int n = 0; n < 2; ++n) dst[n] = PG8_LD32(lds + PG8_SB(b, h) + boff + n * 2048); } while (0)
; #define PG8_WAIT_V(n) asm volatile("s_waitcnt vmcnt(" #n ")" ::: "memory")
; #define PG8_WAIT_L(n) asm volatile("s_waitcnt lgkmcnt(" #n ")" ::: "memory")
; #define PG8_BAR __builtin_amdgcn_s_barrier()
; #define PG8_SCHED __builtin_amdgcn_sched_barrier(0)
; #define PG8_STA(bufoff, nextflag, h, koff) do { if constexpr (Sched::GATHER) { unsigned _o[2]; _o[0] = (nextflag) ? nxtA[h][0] : curA[h][0]; _o[1] = (nextflag) ? nxtA[h][1] : curA[h][1]; PG8_STAGE(bufoff, Ab + (koff), _o); } \
;         else { PG8_STAGE(bufoff, ((nextflag) ? nA : cA) + (size_t)(h) * hstep + (koff), voffA); } } while (0)
; template <class Epi, class Sched, bool ALIGN_EPI, int DT>
; __device__ __forceinline__ void gemm_phase(LAS unsigned char* lds, const int KB, const Sched& S, const Epi& E) {
;     ...
;             const size_t k1 = (size_t)(t + 1) * kstep, k2 = last ? 0 : (size_t)(t + 2) * kstep, k3 = k2 + kstep;
;             const char* b2 = last ? nB : cB + (size_t)(t + 2) * kstep; const char* b3 = b2 + kstep;
;             PG8_LDB(B0, 0, 0); PG8_LDB(B1, 0, 1); PG8_SCHED; PG8_LDA(At, 0, 0); PG8_STA(PG8_SA(1, 1), false, 1, k1);
;             PG8_WAIT_V(8); PG8_WAIT_L(0); PG8_BAR; PG8_MMA(0, 0, At, B0); PG8_MMA(0, 1, At, B1); PG8_BAR; PG8_SCHED;
;             PG8_LDA(At, 0, 1); PG8_STAGE(PG8_SB(0, 0), b2, voffB); PG8_STAGE(PG8_SB(0, 1), b2 + hstep, voffB); PG8_STA(PG8_SA(0, 0), last, 0, k2);
;             PG8_WAIT_V(8); PG8_WAIT_L(0); PG8_BAR; PG8_MMA(1, 0, At, B0); PG8_MMA(1, 1, At, B1); PG8_BAR; PG8_SCHED;
.LBB0_1154:
	ds_read_b128 v[70:73], v167
	ds_read_b128 v[156:159], v167 offset:1024
	ds_read_b128 v[160:163], v167 offset:2048
	ds_read_b128 v[172:175], v167 offset:3072
	ds_read_b128 v[176:179], v168
	ds_read_b128 v[180:183], v168 offset:1024
	ds_read_b128 v[184:187], v168 offset:2048
	ds_read_b128 v[188:191], v168 offset:3072
	s_add_u32 s30, s28, 0x100
	s_addc_u32 s31, s29, 0
	s_add_u32 s63, s56, s28
	s_addc_u32 s66, s57, s29
	s_cmp_eq_u32 s62, 12
	s_cselect_b64 s[36:37], -1, 0
	s_and_b64 s[34:35], s[36:37], exec
	s_cselect_b32 s67, 0, s30
	s_cselect_b32 s35, s17, s66
	s_cselect_b32 s34, s19, s63
	v_lshl_add_u64 v[192:193], v[66:67], 0, s[28:29]
	s_add_i32 m0, s25, 0xc000
	ds_read_b128 v[196:199], v169
	ds_read_b128 v[200:203], v169 offset:1024
	ds_read_b128 v[204:207], v169 offset:2048
	ds_read_b128 v[208:211], v169 offset:3072
	ds_read_b128 v[212:215], v169 offset:4096
	ds_read_b128 v[216:219], v169 offset:5120
	ds_read_b128 v[220:223], v169 offset:6144
	ds_read_b128 v[224:227], v169 offset:7168
	global_load_lds_dwordx4 v[192:193], off
	v_lshl_add_u64 v[192:193], v[68:69], 0, s[28:29]
	s_add_i32 m0, s25, 0xe000
	s_nop 0
	global_load_lds_dwordx4 v[192:193], off
	s_waitcnt vmcnt(8)
	s_waitcnt lgkmcnt(0)
	s_barrier
	s_setprio 1
	s_waitcnt lgkmcnt(0)
	v_mfma_i32_16x16x64_i8 v[134:137], v[70:73], v[196:199], v[134:137]
	v_mfma_i32_16x16x64_i8 v[126:129], v[160:163], v[196:199], v[126:129]
	v_mfma_i32_16x16x64_i8 v[118:121], v[70:73], v[204:207], v[118:121]
	v_mfma_i32_16x16x64_i8 v[110:113], v[160:163], v[204:207], v[110:113]
	v_mfma_i32_16x16x64_i8 v[102:105], v[70:73], v[212:215], v[102:105]
	v_mfma_i32_16x16x64_i8 v[94:97], v[160:163], v[212:215], v[94:97]
	v_mfma_i32_16x16x64_i8 v[86:89], v[70:73], v[220:223], v[86:89]
	v_mfma_i32_16x16x64_i8 v[78:81], v[160:163], v[220:223], v[78:81]
	v_mfma_i32_16x16x64_i8 v[134:137], v[156:159], v[200:203], v[134:137]
	v_mfma_i32_16x16x64_i8 v[126:129], v[172:175], v[200:203], v[126:129]
	v_mfma_i32_16x16x64_i8 v[118:121], v[156:159], v[208:211], v[118:121]
	v_mfma_i32_16x16x64_i8 v[110:113], v[172:175], v[208:211], v[110:113]
	v_mfma_i32_16x16x64_i8 v[102:105], v[156:159], v[216:219], v[102:105]
	v_mfma_i32_16x16x64_i8 v[94:97], v[172:175], v[216:219], v[94:97]
	v_mfma_i32_16x16x64_i8 v[86:89], v[156:159], v[224:227], v[86:89]
	v_mfma_i32_16x16x64_i8 v[78:81], v[172:175], v[224:227], v[78:81]
	s_setprio 0
	s_setprio 1
	v_mfma_i32_16x16x64_i8 v[130:133], v[176:179], v[196:199], v[130:133]
	v_mfma_i32_16x16x64_i8 v[122:125], v[184:187], v[196:199], v[122:125]
	v_mfma_i32_16x16x64_i8 v[114:117], v[176:179], v[204:207], v[114:117]
	v_mfma_i32_16x16x64_i8 v[106:109], v[184:187], v[204:207], v[106:109]
	v_mfma_i32_16x16x64_i8 v[98:101], v[176:179], v[212:215], v[98:101]
	v_mfma_i32_16x16x64_i8 v[90:93], v[184:187], v[212:215], v[90:93]
	v_mfma_i32_16x16x64_i8 v[82:85], v[176:179], v[220:223], v[82:85]
	v_mfma_i32_16x16x64_i8 v[74:77], v[184:187], v[220:223], v[74:77]
	v_mfma_i32_16x16x64_i8 v[130:133], v[180:183], v[200:203], v[130:133]
	v_mfma_i32_16x16x64_i8 v[122:125], v[188:191], v[200:203], v[122:125]
	v_mfma_i32_16x16x64_i8 v[114:117], v[180:183], v[208:211], v[114:117]
	v_mfma_i32_16x16x64_i8 v[106:109], v[188:191], v[208:211], v[106:109]
	v_mfma_i32_16x16x64_i8 v[98:101], v[180:183], v[216:219], v[98:101]
	v_mfma_i32_16x16x64_i8 v[90:93], v[188:191], v[216:219], v[90:93]
	v_mfma_i32_16x16x64_i8 v[82:85], v[180:183], v[224:227], v[82:85]
	v_mfma_i32_16x16x64_i8 v[74:77], v[188:191], v[224:227], v[74:77]
	s_setprio 0
	s_barrier
	s_add_i32 s28, s49, s38
	v_lshl_add_u64 v[192:193], s[34:35], 0, v[140:141]
	s_mov_b32 m0, s28
	ds_read_b128 v[196:199], v169 offset:16384
	ds_read_b128 v[200:203], v169 offset:17408
	ds_read_b128 v[204:207], v169 offset:18432
	ds_read_b128 v[208:211], v169 offset:19456
	ds_read_b128 v[212:215], v169 offset:20480
	ds_read_b128 v[216:219], v169 offset:21504
	ds_read_b128 v[220:223], v169 offset:22528
	ds_read_b128 v[224:227], v169 offset:23552
	global_load_lds_dwordx4 v[192:193], off
	s_add_i32 m0, s28, 0x2000
	s_add_u32 s28, s34, 0x40000
	v_lshl_add_u64 v[228:229], s[34:35], 0, v[138:139]
	s_addc_u32 s29, s35, 0
	s_add_i32 s63, s52, s38
	global_load_lds_dwordx4 v[228:229], off
	v_lshl_add_u64 v[230:231], s[28:29], 0, v[140:141]
	s_mov_b32 m0, s63
	s_nop 0
	global_load_lds_dwordx4 v[230:231], off
	v_lshl_add_u64 v[230:231], s[28:29], 0, v[138:139]
	s_add_i32 m0, s63, 0x2000
	s_and_b64 s[28:29], s[6:7], s[36:37]
	s_and_b64 s[28:29], s[28:29], exec
	s_cselect_b32 s28, s20, s26
	s_cselect_b32 s29, s21, s27
	s_add_u32 s28, s28, s67
	s_addc_u32 s29, s29, 0
	global_load_lds_dwordx4 v[230:231], off
	v_lshl_add_u64 v[230:231], s[28:29], 0, v[142:143]
	s_mov_b32 m0, s25
	v_lshl_add_u64 v[232:233], s[28:29], 0, v[144:145]
	global_load_lds_dwordx4 v[230:231], off
	s_mov_b32 m0, s41
	s_nop 0
	global_load_lds_dwordx4 v[232:233], off
	s_waitcnt vmcnt(8)
	s_waitcnt lgkmcnt(0)
	s_barrier
; #define PG8_LDA(dst, b, h) do { _Pragma("unroll") for (int m = 0; m < 4; ++m) dst[m] = PG8_LD32(lds + PG8_SA(b, h) + aoff + m * 2048); } while (0)
; #define PG8_LDB(dst, b, h) do { _Pragma("unroll") for (int n = 0; n < 2; ++n) dst[n] = PG8_LD32(lds + PG8_SB(b, h) + boff + n * 2048); } while (0)
; #define PG8_WAIT_V(n) asm volatile("s_waitcnt vmcnt(" #n ")" ::: "memory")
; #define PG8_WAIT_L(n) asm volatile("s_waitcnt lgkmcnt(" #n ")" ::: "memory")
; #define PG8_BAR __builtin_amdgcn_s_barrier()
; #define PG8_SCHED __builtin_amdgcn_sched_barrier(0)
; #define PG8_STA(bufoff, nextflag, h, koff) do { if constexpr (Sched::GATHER) { unsigned _o[2]; _o[0] = (nextflag) ? nxtA[h][0] : curA[h][0]; _o[1] = (nextflag) ? nxtA[h][1] : curA[h][1]; PG8_STAGE(bufoff, Ab + (koff), _o); } \
;         else { PG8_STAGE(bufoff, ((nextflag) ? nA : cA) + (size_t)(h) * hstep + (koff), voffA); } } while (0)
; template <class Epi, class Sched, bool ALIGN_EPI, int DT>
; __device__ __forceinline__ void gemm_phase(LAS unsigned char* lds, const int KB, const Sched& S, const Epi& E) {
;     ...
;             PG8_WAIT_V(8); PG8_WAIT_L(0); PG8_BAR; PG8_MMA(1, 0, At, B0); PG8_MMA(1, 1, At, B1); PG8_BAR; PG8_SCHED;
;             PG8_LDB(B0, 1, 0); PG8_LDB(B1, 1, 1); PG8_SCHED; PG8_LDA(At, 1, 0); PG8_STA(PG8_SA(0, 1), last, 1, k2);
;             PG8_WAIT_V(8); PG8_WAIT_L(0); PG8_BAR; PG8_MMA(0, 0, At, B0); PG8_MMA(0, 1, At, B1); PG8_BAR; PG8_SCHED;
	s_setprio 1
	s_waitcnt lgkmcnt(0)
	v_mfma_i32_16x16x64_i8 v[62:65], v[70:73], v[196:199], v[62:65]
	v_mfma_i32_16x16x64_i8 v[54:57], v[160:163], v[196:199], v[54:57]
	v_mfma_i32_16x16x64_i8 v[46:49], v[70:73], v[204:207], v[46:49]
	v_mfma_i32_16x16x64_i8 v[38:41], v[160:163], v[204:207], v[38:41]
	v_mfma_i32_16x16x64_i8 v[30:33], v[70:73], v[212:215], v[30:33]
	v_mfma_i32_16x16x64_i8 v[22:25], v[160:163], v[212:215], v[22:25]
	v_mfma_i32_16x16x64_i8 v[6:9], v[70:73], v[220:223], v[6:9]
	v_mfma_i32_16x16x64_i8 v[2:5], v[160:163], v[220:223], v[2:5]
	v_mfma_i32_16x16x64_i8 v[62:65], v[156:159], v[200:203], v[62:65]
	v_mfma_i32_16x16x64_i8 v[54:57], v[172:175], v[200:203], v[54:57]
	v_mfma_i32_16x16x64_i8 v[46:49], v[156:159], v[208:211], v[46:49]
	v_mfma_i32_16x16x64_i8 v[38:41], v[172:175], v[208:211], v[38:41]
	v_mfma_i32_16x16x64_i8 v[30:33], v[156:159], v[216:219], v[30:33]
	v_mfma_i32_16x16x64_i8 v[22:25], v[172:175], v[216:219], v[22:25]
	v_mfma_i32_16x16x64_i8 v[6:9], v[156:159], v[224:227], v[6:9]
	v_mfma_i32_16x16x64_i8 v[2:5], v[172:175], v[224:227], v[2:5]
	s_setprio 0
	s_setprio 1
	v_mfma_i32_16x16x64_i8 v[58:61], v[176:179], v[196:199], v[58:61]
	v_mfma_i32_16x16x64_i8 v[50:53], v[184:187], v[196:199], v[50:53]
	v_mfma_i32_16x16x64_i8 v[42:45], v[176:179], v[204:207], v[42:45]
	v_mfma_i32_16x16x64_i8 v[34:37], v[184:187], v[204:207], v[34:37]
	v_mfma_i32_16x16x64_i8 v[26:29], v[176:179], v[212:215], v[26:29]
	v_mfma_i32_16x16x64_i8 v[18:21], v[184:187], v[212:215], v[18:21]
	v_mfma_i32_16x16x64_i8 v[14:17], v[176:179], v[220:223], v[14:17]
	v_mfma_i32_16x16x64_i8 v[10:13], v[184:187], v[220:223], v[10:13]
	v_mfma_i32_16x16x64_i8 v[58:61], v[180:183], v[200:203], v[58:61]
	v_mfma_i32_16x16x64_i8 v[50:53], v[188:191], v[200:203], v[50:53]
	v_mfma_i32_16x16x64_i8 v[42:45], v[180:183], v[208:211], v[42:45]
	v_mfma_i32_16x16x64_i8 v[34:37], v[188:191], v[208:211], v[34:37]
	v_mfma_i32_16x16x64_i8 v[26:29], v[180:183], v[216:219], v[26:29]
	v_mfma_i32_16x16x64_i8 v[18:21], v[188:191], v[216:219], v[18:21]
	v_mfma_i32_16x16x64_i8 v[14:17], v[180:183], v[224:227], v[14:17]
	v_mfma_i32_16x16x64_i8 v[10:13], v[188:191], v[224:227], v[10:13]
	s_setprio 0
	s_barrier
	s_add_i32 s36, 0, 0x18000
	v_add_u32_e32 v1, s36, v165
	s_add_i32 s37, 0, 0x1c000
	ds_read_b128 v[70:73], v1
	ds_read_b128 v[156:159], v1 offset:1024
	ds_read_b128 v[160:163], v1 offset:2048
	ds_read_b128 v[172:175], v1 offset:3072
	v_add_u32_e32 v1, s37, v165
	ds_read_b128 v[176:179], v1
	ds_read_b128 v[180:183], v1 offset:1024
	ds_read_b128 v[184:187], v1 offset:2048
	ds_read_b128 v[188:191], v1 offset:3072
	s_add_u32 s28, s28, 0x40000
	s_addc_u32 s29, s29, 0
	s_mov_b32 m0, s42
	v_lshl_add_u64 v[234:235], s[28:29], 0, v[142:143]
	ds_read_b128 v[196:199], v169 offset:32768
	ds_read_b128 v[200:203], v169 offset:33792
	ds_read_b128 v[204:207], v169 offset:34816
	ds_read_b128 v[208:211], v169 offset:35840
	ds_read_b128 v[212:215], v169 offset:36864
	ds_read_b128 v[216:219], v169 offset:37888
	ds_read_b128 v[220:223], v169 offset:38912
	ds_read_b128 v[224:227], v169 offset:39936
	global_load_lds_dwordx4 v[234:235], off
	v_lshl_add_u64 v[234:235], s[28:29], 0, v[144:145]
	s_mov_b32 m0, s43
	s_nop 0
	global_load_lds_dwordx4 v[234:235], off
	s_waitcnt vmcnt(8)
	s_waitcnt lgkmcnt(0)
	s_barrier
	s_setprio 1
	s_waitcnt lgkmcnt(0)
	v_mfma_i32_16x16x64_i8 v[134:137], v[70:73], v[196:199], v[134:137]
	v_mfma_i32_16x16x64_i8 v[126:129], v[160:163], v[196:199], v[126:129]
	v_mfma_i32_16x16x64_i8 v[118:121], v[70:73], v[204:207], v[118:121]
	v_mfma_i32_16x16x64_i8 v[110:113], v[160:163], v[204:207], v[110:113]
	v_mfma_i32_16x16x64_i8 v[102:105], v[70:73], v[212:215], v[102:105]
	v_mfma_i32_16x16x64_i8 v[94:97], v[160:163], v[212:215], v[94:97]
	v_mfma_i32_16x16x64_i8 v[86:89], v[70:73], v[220:223], v[86:89]
	v_mfma_i32_16x16x64_i8 v[78:81], v[160:163], v[220:223], v[78:81]
	v_mfma_i32_16x16x64_i8 v[134:137], v[156:159], v[200:203], v[134:137]
	v_mfma_i32_16x16x64_i8 v[126:129], v[172:175], v[200:203], v[126:129]
	v_mfma_i32_16x16x64_i8 v[118:121], v[156:159], v[208:211], v[118:121]
	v_mfma_i32_16x16x64_i8 v[110:113], v[172:175], v[208:211], v[110:113]
	v_mfma_i32_16x16x64_i8 v[102:105], v[156:159], v[216:219], v[102:105]
	v_mfma_i32_16x16x64_i8 v[94:97], v[172:175], v[216:219], v[94:97]
	v_mfma_i32_16x16x64_i8 v[86:89], v[156:159], v[224:227], v[86:89]
	v_mfma_i32_16x16x64_i8 v[78:81], v[172:175], v[224:227], v[78:81]
	s_setprio 0
	s_setprio 1
	v_mfma_i32_16x16x64_i8 v[130:133], v[176:179], v[196:199], v[130:133]
	v_mfma_i32_16x16x64_i8 v[122:125], v[184:187], v[196:199], v[122:125]
	v_mfma_i32_16x16x64_i8 v[114:117], v[176:179], v[204:207], v[114:117]
	v_mfma_i32_16x16x64_i8 v[106:109], v[184:187], v[204:207], v[106:109]
	v_mfma_i32_16x16x64_i8 v[98:101], v[176:179], v[212:215], v[98:101]
	v_mfma_i32_16x16x64_i8 v[90:93], v[184:187], v[212:215], v[90:93]
	v_mfma_i32_16x16x64_i8 v[82:85], v[176:179], v[220:223], v[82:85]
	v_mfma_i32_16x16x64_i8 v[74:77], v[184:187], v[220:223], v[74:77]
	v_mfma_i32_16x16x64_i8 v[130:133], v[180:183], v[200:203], v[130:133]
	v_mfma_i32_16x16x64_i8 v[122:125], v[188:191], v[200:203], v[122:125]
	v_mfma_i32_16x16x64_i8 v[114:117], v[180:183], v[208:211], v[114:117]
	v_mfma_i32_16x16x64_i8 v[106:109], v[188:191], v[208:211], v[106:109]
	v_mfma_i32_16x16x64_i8 v[98:101], v[180:183], v[216:219], v[98:101]
	v_mfma_i32_16x16x64_i8 v[90:93], v[188:191], v[216:219], v[90:93]
	v_mfma_i32_16x16x64_i8 v[82:85], v[180:183], v[224:227], v[82:85]
	v_mfma_i32_16x16x64_i8 v[74:77], v[188:191], v[224:227], v[74:77]
	s_setprio 0
	s_barrier
; #define PG8_STAGE(bufoff, gbase, voff) do { _Pragma("unroll") for (int _i = 0; _i < 2; ++_i) \
;         __builtin_amdgcn_global_load_lds((const unsigned*)((const char*)(gbase) + (voff)[_i]), (LAS unsigned*)(lds + (bufoff) + ldsw + _i * 8192), 16, 0, 0); } while (0)
; #define PG8_LDA(dst, b, h) do { _Pragma("unroll") for (int m = 0; m < 4; ++m) dst[m] = PG8_LD32(lds + PG8_SA(b, h) + aoff + m * 2048); } while (0)
; #define PG8_WAIT_V(n) asm volatile("s_waitcnt vmcnt(" #n ")" ::: "memory")
; #define PG8_WAIT_L(n) asm volatile("s_waitcnt lgkmcnt(" #n ")" ::: "memory")
; #define PG8_BAR __builtin_amdgcn_s_barrier()
; #define PG8_SCHED __builtin_amdgcn_sched_barrier(0)
; #define PG8_STA(bufoff, nextflag, h, koff) do { if constexpr (Sched::GATHER) { unsigned _o[2]; _o[0] = (nextflag) ? nxtA[h][0] : curA[h][0]; _o[1] = (nextflag) ? nxtA[h][1] : curA[h][1]; PG8_STAGE(bufoff, Ab + (koff), _o); } \
;         else { PG8_STAGE(bufoff, ((nextflag) ? nA : cA) + (size_t)(h) * hstep + (koff), voffA); } } while (0)
; template <class Epi, class Sched, bool ALIGN_EPI, int DT>
; __device__ __forceinline__ void gemm_phase(LAS unsigned char* lds, const int KB, const Sched& S, const Epi& E) {
;     ...
;         for (int t = 0; t < nt; t += 2) {
;             const bool last = (t == nt - 2);
;             const size_t k1 = (size_t)(t + 1) * kstep, k2 = last ? 0 : (size_t)(t + 2) * kstep, k3 = k2 + kstep;
;     ...
;             PG8_LDA(At, 1, 1); PG8_STAGE(PG8_SB(1, 0), b3, voffB); PG8_STAGE(PG8_SB(1, 1), b3 + hstep, voffB); PG8_STA(PG8_SA(1, 0), last, 0, k3);
;             PG8_WAIT_V(8); PG8_WAIT_L(0); PG8_BAR; PG8_MMA(1, 0, At, B0); PG8_MMA(1, 1, At, B1); PG8_BAR; PG8_SCHED;
	s_add_i32 s28, s36, s38
	v_lshl_add_u64 v[192:193], v[192:193], 0, s[12:13]
	s_mov_b32 m0, s28
	ds_read_b128 v[196:199], v169 offset:49152
	ds_read_b128 v[200:203], v169 offset:50176
	ds_read_b128 v[204:207], v169 offset:51200
	ds_read_b128 v[208:211], v169 offset:52224
	ds_read_b128 v[212:215], v169 offset:53248
	ds_read_b128 v[216:219], v169 offset:54272
	ds_read_b128 v[220:223], v169 offset:55296
	ds_read_b128 v[224:227], v169 offset:56320
	global_load_lds_dwordx4 v[192:193], off
	s_add_i32 m0, s28, 0x2000
	s_add_u32 s28, s34, 0x40080
	v_lshl_add_u64 v[192:193], v[228:229], 0, s[12:13]
	s_addc_u32 s29, s35, 0
	s_add_i32 s34, s37, s38
	global_load_lds_dwordx4 v[192:193], off
	v_lshl_add_u64 v[192:193], s[28:29], 0, v[140:141]
	s_mov_b32 m0, s34
	s_nop 0
	global_load_lds_dwordx4 v[192:193], off
	v_lshl_add_u64 v[192:193], s[28:29], 0, v[138:139]
	s_add_i32 m0, s34, 0x2000
	s_nop 0
	global_load_lds_dwordx4 v[192:193], off
	v_lshl_add_u64 v[192:193], v[230:231], 0, s[12:13]
	s_mov_b32 m0, s45
	s_nop 0
	global_load_lds_dwordx4 v[192:193], off
	v_lshl_add_u64 v[192:193], v[232:233], 0, s[12:13]
	s_mov_b32 m0, s46
	s_nop 0
	global_load_lds_dwordx4 v[192:193], off
	s_waitcnt vmcnt(8)
	s_waitcnt lgkmcnt(0)
	s_barrier
	s_setprio 1
	s_waitcnt lgkmcnt(0)
	v_mfma_i32_16x16x64_i8 v[62:65], v[70:73], v[196:199], v[62:65]
	v_mfma_i32_16x16x64_i8 v[54:57], v[160:163], v[196:199], v[54:57]
	v_mfma_i32_16x16x64_i8 v[46:49], v[70:73], v[204:207], v[46:49]
	v_mfma_i32_16x16x64_i8 v[38:41], v[160:163], v[204:207], v[38:41]
	v_mfma_i32_16x16x64_i8 v[30:33], v[70:73], v[212:215], v[30:33]
	v_mfma_i32_16x16x64_i8 v[22:25], v[160:163], v[212:215], v[22:25]
	v_mfma_i32_16x16x64_i8 v[6:9], v[70:73], v[220:223], v[6:9]
	v_mfma_i32_16x16x64_i8 v[2:5], v[160:163], v[220:223], v[2:5]
	v_mfma_i32_16x16x64_i8 v[62:65], v[156:159], v[200:203], v[62:65]
	v_mfma_i32_16x16x64_i8 v[54:57], v[172:175], v[200:203], v[54:57]
	v_mfma_i32_16x16x64_i8 v[46:49], v[156:159], v[208:211], v[46:49]
	v_mfma_i32_16x16x64_i8 v[38:41], v[172:175], v[208:211], v[38:41]
	v_mfma_i32_16x16x64_i8 v[30:33], v[156:159], v[216:219], v[30:33]
	v_mfma_i32_16x16x64_i8 v[22:25], v[172:175], v[216:219], v[22:25]
	v_mfma_i32_16x16x64_i8 v[6:9], v[156:159], v[224:227], v[6:9]
	v_mfma_i32_16x16x64_i8 v[2:5], v[172:175], v[224:227], v[2:5]
	s_setprio 0
	s_setprio 1
	v_mfma_i32_16x16x64_i8 v[58:61], v[176:179], v[196:199], v[58:61]
	v_mfma_i32_16x16x64_i8 v[50:53], v[184:187], v[196:199], v[50:53]
	v_mfma_i32_16x16x64_i8 v[42:45], v[176:179], v[204:207], v[42:45]
	v_mfma_i32_16x16x64_i8 v[34:37], v[184:187], v[204:207], v[34:37]
	v_mfma_i32_16x16x64_i8 v[26:29], v[176:179], v[212:215], v[26:29]
	v_mfma_i32_16x16x64_i8 v[18:21], v[184:187], v[212:215], v[18:21]
	v_mfma_i32_16x16x64_i8 v[14:17], v[176:179], v[220:223], v[14:17]
	v_mfma_i32_16x16x64_i8 v[10:13], v[184:187], v[220:223], v[10:13]
	v_mfma_i32_16x16x64_i8 v[58:61], v[180:183], v[200:203], v[58:61]
	v_mfma_i32_16x16x64_i8 v[50:53], v[188:191], v[200:203], v[50:53]
	v_mfma_i32_16x16x64_i8 v[42:45], v[180:183], v[208:211], v[42:45]
	v_mfma_i32_16x16x64_i8 v[34:37], v[188:191], v[208:211], v[34:37]
	v_mfma_i32_16x16x64_i8 v[26:29], v[180:183], v[216:219], v[26:29]
	v_mfma_i32_16x16x64_i8 v[18:21], v[188:191], v[216:219], v[18:21]
	v_mfma_i32_16x16x64_i8 v[14:17], v[180:183], v[224:227], v[14:17]
	v_mfma_i32_16x16x64_i8 v[10:13], v[188:191], v[224:227], v[10:13]
	s_setprio 0
	s_add_i32 s62, s62, 2
	s_cmp_gt_u32 s62, 13
	s_mov_b64 s[28:29], s[30:31]
	s_barrier
	s_cbranch_scc0 .LBB0_1154
	s_and_b64 vcc, exec, s[14:15]
	s_cbranch_vccz .LBB0_1157
	s_barrier

; #define PG8_STAGE(bufoff, gbase, voff) do { _Pragma("unroll") for (int _i = 0; _i < 2; ++_i) \
;         __builtin_amdgcn_global_load_lds((const unsigned*)((const char*)(gbase) + (voff)[_i]), (LAS unsigned*)(lds + (bufoff) + ldsw + _i * 8192), 16, 0, 0); } while (0)
; #define PG8_LDA(dst, b, h) do { _Pragma("unroll") for (int m = 0; m < 4; ++m) dst[m] = PG8_LD32(lds + PG8_SA(b, h) + aoff + m * 2048); } while (0)
; #define PG8_LDB(dst, b, h) do { _Pragma("unroll") for (int n = 0; n < 2; ++n) dst[n] = PG8_LD32(lds + PG8_SB(b, h) + boff + n * 2048); } while (0)
; #define PG8_WAIT_V(n) asm volatile("s_waitcnt vmcnt(" #n ")" ::: "memory")
; #define PG8_WAIT_L(n) asm volatile("s_waitcnt lgkmcnt(" #n ")" ::: "memory")
; #define PG8_BAR __builtin_amdgcn_s_barrier()
; #define PG8_SCHED __builtin_amdgcn_sched_barrier(0)
; #define PG8_STA(bufoff, nextflag, h, koff) do { if constexpr (Sched::GATHER) { unsigned _o[2]; _o[0] = (nextflag) ? nxtA[h][0] : curA[h][0]; _o[1] = (nextflag) ? nxtA[h][1] : curA[h][1]; PG8_STAGE(bufoff, Ab + (koff), _o); } \
;         else { PG8_STAGE(bufoff, ((nextflag) ? nA : cA) + (size_t)(h) * hstep + (koff), voffA); } } while (0)
; template <class Epi, class Sched, bool ALIGN_EPI, int DT>
; __device__ __forceinline__ void gemm_phase(LAS unsigned char* lds, const int KB, const Sched& S, const Epi& E) {
;     ...
;             const size_t k1 = (size_t)(t + 1) * kstep, k2 = last ? 0 : (size_t)(t + 2) * kstep, k3 = k2 + kstep;
;             const char* b2 = last ? nB : cB + (size_t)(t + 2) * kstep; const char* b3 = b2 + kstep;
;             PG8_LDB(B0, 0, 0); PG8_LDB(B1, 0, 1); PG8_SCHED; PG8_LDA(At, 0, 0); PG8_STA(PG8_SA(1, 1), false, 1, k1);
;             PG8_WAIT_V(8); PG8_WAIT_L(0); PG8_BAR; PG8_MMA(0, 0, At, B0); PG8_MMA(0, 1, At, B1); PG8_BAR; PG8_SCHED;
;             PG8_LDA(At, 0, 1); PG8_STAGE(PG8_SB(0, 0), b2, voffB); PG8_STAGE(PG8_SB(0, 1), b2 + hstep, voffB); PG8_STA(PG8_SA(0, 0), last, 0, k2);
;             PG8_WAIT_V(8); PG8_WAIT_L(0); PG8_BAR; PG8_MMA(1, 0, At, B0); PG8_MMA(1, 1, At, B1); PG8_BAR; PG8_SCHED;
.LBB0_1237:
	ds_read_b128 v[18:21], v193
	ds_read_b128 v[22:25], v193 offset:1024
	ds_read_b128 v[26:29], v193 offset:2048
	ds_read_b128 v[30:33], v193 offset:3072
	ds_read_b128 v[2:5], v195
	ds_read_b128 v[6:9], v195 offset:1024
	ds_read_b128 v[10:13], v195 offset:2048
	ds_read_b128 v[14:17], v195 offset:3072
	s_add_u32 s26, s30, 0x100
	s_addc_u32 s27, s31, 0
	s_add_u32 s28, s56, s30
	s_addc_u32 s29, s57, s31
	s_add_i32 s68, s43, s34
	s_add_i32 m0, s35, 0xc000
	s_add_i32 s69, s35, 0xe000
	s_add_i32 s63, s68, 0x2000
	s_cmp_eq_u32 s62, 40
	s_cselect_b32 s29, s23, s29
	s_cselect_b32 s28, s22, s28
	s_cselect_b32 s66, 0, s27
	s_cselect_b32 s67, 0, s26
	v_lshl_add_u64 v[222:223], v[178:179], 0, s[30:31]
	ds_read_b128 v[182:185], v196
	ds_read_b128 v[186:189], v196 offset:1024
	ds_read_b128 v[198:201], v196 offset:2048
	ds_read_b128 v[202:205], v196 offset:3072
	ds_read_b128 v[206:209], v196 offset:4096
	ds_read_b128 v[210:213], v196 offset:5120
	ds_read_b128 v[214:217], v196 offset:6144
	ds_read_b128 v[218:221], v196 offset:7168
	global_load_lds_dwordx4 v[222:223], off
	v_lshl_add_u64 v[222:223], v[180:181], 0, s[30:31]
	s_mov_b32 m0, s69
	s_nop 0
	global_load_lds_dwordx4 v[222:223], off
	s_waitcnt vmcnt(8)
	s_waitcnt lgkmcnt(0)
	s_barrier
	s_setprio 1
	s_waitcnt lgkmcnt(0)
	v_mfma_scale_f32_16x16x128_f8f6f4 v[158:161], v[18:25], v[182:189], v[158:161], v190, v190 op_sel_hi:[0,0,0]
	v_mfma_scale_f32_16x16x128_f8f6f4 v[154:157], v[26:33], v[182:189], v[154:157], v190, v190 op_sel_hi:[0,0,0]
	v_mfma_scale_f32_16x16x128_f8f6f4 v[150:153], v[18:25], v[198:205], v[150:153], v190, v190 op_sel_hi:[0,0,0]
	v_mfma_scale_f32_16x16x128_f8f6f4 v[142:145], v[26:33], v[198:205], v[142:145], v190, v190 op_sel_hi:[0,0,0]
	v_mfma_scale_f32_16x16x128_f8f6f4 v[134:137], v[18:25], v[206:213], v[134:137], v190, v190 op_sel_hi:[0,0,0]
	v_mfma_scale_f32_16x16x128_f8f6f4 v[126:129], v[26:33], v[206:213], v[126:129], v190, v190 op_sel_hi:[0,0,0]
	v_mfma_scale_f32_16x16x128_f8f6f4 v[118:121], v[18:25], v[214:221], v[118:121], v190, v190 op_sel_hi:[0,0,0]
	v_mfma_scale_f32_16x16x128_f8f6f4 v[110:113], v[26:33], v[214:221], v[110:113], v190, v190 op_sel_hi:[0,0,0]
	s_setprio 0
	s_setprio 1
	v_mfma_scale_f32_16x16x128_f8f6f4 v[146:149], v[2:9], v[182:189], v[146:149], v190, v190 op_sel_hi:[0,0,0]
	v_mfma_scale_f32_16x16x128_f8f6f4 v[138:141], v[10:17], v[182:189], v[138:141], v190, v190 op_sel_hi:[0,0,0]
	v_mfma_scale_f32_16x16x128_f8f6f4 v[130:133], v[2:9], v[198:205], v[130:133], v190, v190 op_sel_hi:[0,0,0]
	v_mfma_scale_f32_16x16x128_f8f6f4 v[122:125], v[10:17], v[198:205], v[122:125], v190, v190 op_sel_hi:[0,0,0]
	v_mfma_scale_f32_16x16x128_f8f6f4 v[114:117], v[2:9], v[206:213], v[114:117], v190, v190 op_sel_hi:[0,0,0]
	v_mfma_scale_f32_16x16x128_f8f6f4 v[106:109], v[10:17], v[206:213], v[106:109], v190, v190 op_sel_hi:[0,0,0]
	v_mfma_scale_f32_16x16x128_f8f6f4 v[102:105], v[2:9], v[214:221], v[102:105], v190, v190 op_sel_hi:[0,0,0]
	v_mfma_scale_f32_16x16x128_f8f6f4 v[98:101], v[10:17], v[214:221], v[98:101], v190, v190 op_sel_hi:[0,0,0]
	s_setprio 0
	s_barrier
	s_mov_b32 m0, s68
	v_lshl_add_u64 v[184:185], s[28:29], 0, v[162:163]
	ds_read_b128 v[198:201], v196 offset:16384
	ds_read_b128 v[202:205], v196 offset:17408
	ds_read_b128 v[206:209], v196 offset:18432
	ds_read_b128 v[210:213], v196 offset:19456
	ds_read_b128 v[214:217], v196 offset:20480
	ds_read_b128 v[218:221], v196 offset:21504
	ds_read_b128 v[222:225], v196 offset:22528
	ds_read_b128 v[226:229], v196 offset:23552
	global_load_lds_dwordx4 v[184:185], off
	s_mov_b32 m0, s63
	s_cselect_b32 s63, s9, s25
	s_cselect_b32 s68, s8, s24
	s_add_u32 s30, s28, 0xb0000
	v_lshl_add_u64 v[182:183], s[28:29], 0, v[164:165]
	s_addc_u32 s31, s29, 0
	s_add_i32 s69, s44, s34
	global_load_lds_dwordx4 v[182:183], off
	v_lshl_add_u64 v[186:187], s[30:31], 0, v[162:163]
	s_mov_b32 m0, s69
	s_nop 0
	global_load_lds_dwordx4 v[186:187], off
	s_add_i32 m0, s69, 0x2000
	v_lshl_add_u64 v[186:187], s[30:31], 0, v[164:165]
	s_add_u32 s30, s68, s67
	s_addc_u32 s31, s63, s66
	global_load_lds_dwordx4 v[186:187], off
	v_lshl_add_u64 v[186:187], s[30:31], 0, v[166:167]
	s_mov_b32 m0, s35
	v_lshl_add_u64 v[188:189], s[30:31], 0, v[168:169]
	global_load_lds_dwordx4 v[186:187], off
	s_mov_b32 m0, s36
	s_nop 0
	global_load_lds_dwordx4 v[188:189], off
	s_waitcnt vmcnt(8)
	s_waitcnt lgkmcnt(0)
	s_barrier
	s_setprio 1
	s_waitcnt lgkmcnt(0)
	v_mfma_scale_f32_16x16x128_f8f6f4 v[94:97], v[18:25], v[198:205], v[94:97], v190, v190 op_sel_hi:[0,0,0]
	v_mfma_scale_f32_16x16x128_f8f6f4 v[90:93], v[26:33], v[198:205], v[90:93], v190, v190 op_sel_hi:[0,0,0]
	v_mfma_scale_f32_16x16x128_f8f6f4 v[86:89], v[18:25], v[206:213], v[86:89], v190, v190 op_sel_hi:[0,0,0]
	v_mfma_scale_f32_16x16x128_f8f6f4 v[78:81], v[26:33], v[206:213], v[78:81], v190, v190 op_sel_hi:[0,0,0]
	v_mfma_scale_f32_16x16x128_f8f6f4 v[62:65], v[18:25], v[214:221], v[62:65], v190, v190 op_sel_hi:[0,0,0]
	v_mfma_scale_f32_16x16x128_f8f6f4 v[54:57], v[26:33], v[214:221], v[54:57], v190, v190 op_sel_hi:[0,0,0]
	v_mfma_scale_f32_16x16x128_f8f6f4 v[46:49], v[18:25], v[222:229], v[46:49], v190, v190 op_sel_hi:[0,0,0]
	v_mfma_scale_f32_16x16x128_f8f6f4 v[38:41], v[26:33], v[222:229], v[38:41], v190, v190 op_sel_hi:[0,0,0]
	s_setprio 0
	s_setprio 1
	v_mfma_scale_f32_16x16x128_f8f6f4 v[82:85], v[2:9], v[198:205], v[82:85], v190, v190 op_sel_hi:[0,0,0]
	v_mfma_scale_f32_16x16x128_f8f6f4 v[74:77], v[10:17], v[198:205], v[74:77], v190, v190 op_sel_hi:[0,0,0]
	v_mfma_scale_f32_16x16x128_f8f6f4 v[58:61], v[2:9], v[206:213], v[58:61], v190, v190 op_sel_hi:[0,0,0]
	v_mfma_scale_f32_16x16x128_f8f6f4 v[50:53], v[10:17], v[206:213], v[50:53], v190, v190 op_sel_hi:[0,0,0]
	v_mfma_scale_f32_16x16x128_f8f6f4 v[42:45], v[2:9], v[214:221], v[42:45], v190, v190 op_sel_hi:[0,0,0]
	v_mfma_scale_f32_16x16x128_f8f6f4 v[34:37], v[10:17], v[214:221], v[34:37], v190, v190 op_sel_hi:[0,0,0]
	v_mfma_scale_f32_16x16x128_f8f6f4 v[70:73], v[2:9], v[222:229], v[70:73], v190, v190 op_sel_hi:[0,0,0]
	v_mfma_scale_f32_16x16x128_f8f6f4 v[66:69], v[10:17], v[222:229], v[66:69], v190, v190 op_sel_hi:[0,0,0]
	s_setprio 0
	s_barrier
; #define PG8_STAGE(bufoff, gbase, voff) do { _Pragma("unroll") for (int _i = 0; _i < 2; ++_i) \
;         __builtin_amdgcn_global_load_lds((const unsigned*)((const char*)(gbase) + (voff)[_i]), (LAS unsigned*)(lds + (bufoff) + ldsw + _i * 8192), 16, 0, 0); } while (0)
; #define PG8_LDA(dst, b, h) do { _Pragma("unroll") for (int m = 0; m < 4; ++m) dst[m] = PG8_LD32(lds + PG8_SA(b, h) + aoff + m * 2048); } while (0)
; #define PG8_LDB(dst, b, h) do { _Pragma("unroll") for (int n = 0; n < 2; ++n) dst[n] = PG8_LD32(lds + PG8_SB(b, h) + boff + n * 2048); } while (0)
; #define PG8_WAIT_V(n) asm volatile("s_waitcnt vmcnt(" #n ")" ::: "memory")
; #define PG8_WAIT_L(n) asm volatile("s_waitcnt lgkmcnt(" #n ")" ::: "memory")
; #define PG8_BAR __builtin_amdgcn_s_barrier()
; #define PG8_SCHED __builtin_amdgcn_sched_barrier(0)
; #define PG8_STA(bufoff, nextflag, h, koff) do { if constexpr (Sched::GATHER) { unsigned _o[2]; _o[0] = (nextflag) ? nxtA[h][0] : curA[h][0]; _o[1] = (nextflag) ? nxtA[h][1] : curA[h][1]; PG8_STAGE(bufoff, Ab + (koff), _o); } \
;         else { PG8_STAGE(bufoff, ((nextflag) ? nA : cA) + (size_t)(h) * hstep + (koff), voffA); } } while (0)
; template <class Epi, class Sched, bool ALIGN_EPI, int DT>
; __device__ __forceinline__ void gemm_phase(LAS unsigned char* lds, const int KB, const Sched& S, const Epi& E) {
;     ...
;         for (int t = 0; t < nt; t += 2) {
;             const bool last = (t == nt - 2);
;             const size_t k1 = (size_t)(t + 1) * kstep, k2 = last ? 0 : (size_t)(t + 2) * kstep, k3 = k2 + kstep;
;     ...
;             PG8_LDB(B0, 1, 0); PG8_LDB(B1, 1, 1); PG8_SCHED; PG8_LDA(At, 1, 0); PG8_STA(PG8_SA(0, 1), last, 1, k2);
;             PG8_WAIT_V(8); PG8_WAIT_L(0); PG8_BAR; PG8_MMA(0, 0, At, B0); PG8_MMA(0, 1, At, B1); PG8_BAR; PG8_SCHED;
;             PG8_LDA(At, 1, 1); PG8_STAGE(PG8_SB(1, 0), b3, voffB); PG8_STAGE(PG8_SB(1, 1), b3 + hstep, voffB); PG8_STA(PG8_SA(1, 0), last, 0, k3);
;             PG8_WAIT_V(8); PG8_WAIT_L(0); PG8_BAR; PG8_MMA(1, 0, At, B0); PG8_MMA(1, 1, At, B1); PG8_BAR; PG8_SCHED;
	s_add_i32 s63, 0, 0x18000
	s_add_i32 s66, 0, 0x1c000
	v_add_u32_e32 v14, s63, v191
	v_add_u32_e32 v30, s66, v191
	ds_read_b128 v[2:5], v14
	ds_read_b128 v[6:9], v14 offset:1024
	ds_read_b128 v[10:13], v14 offset:2048
	ds_read_b128 v[14:17], v14 offset:3072
	ds_read_b128 v[18:21], v30
	ds_read_b128 v[22:25], v30 offset:1024
	ds_read_b128 v[26:29], v30 offset:2048
	ds_read_b128 v[30:33], v30 offset:3072
	s_add_u32 s30, s30, 0xb0000
	s_addc_u32 s31, s31, 0
	s_mov_b32 m0, s37
	v_lshl_add_u64 v[230:231], s[30:31], 0, v[166:167]
	ds_read_b128 v[198:201], v196 offset:32768
	ds_read_b128 v[202:205], v196 offset:33792
	ds_read_b128 v[206:209], v196 offset:34816
	ds_read_b128 v[210:213], v196 offset:35840
	ds_read_b128 v[214:217], v196 offset:36864
	ds_read_b128 v[218:221], v196 offset:37888
	ds_read_b128 v[222:225], v196 offset:38912
	ds_read_b128 v[226:229], v196 offset:39936
	global_load_lds_dwordx4 v[230:231], off
	v_lshl_add_u64 v[230:231], s[30:31], 0, v[168:169]
	s_mov_b32 m0, s38
	s_nop 0
	global_load_lds_dwordx4 v[230:231], off
	s_waitcnt vmcnt(8)
	s_waitcnt lgkmcnt(0)
	s_barrier
	s_setprio 1
	s_waitcnt lgkmcnt(0)
	v_mfma_scale_f32_16x16x128_f8f6f4 v[158:161], v[2:9], v[198:205], v[158:161], v190, v190 op_sel_hi:[0,0,0]
	v_mfma_scale_f32_16x16x128_f8f6f4 v[154:157], v[10:17], v[198:205], v[154:157], v190, v190 op_sel_hi:[0,0,0]
	v_mfma_scale_f32_16x16x128_f8f6f4 v[150:153], v[2:9], v[206:213], v[150:153], v190, v190 op_sel_hi:[0,0,0]
	v_mfma_scale_f32_16x16x128_f8f6f4 v[142:145], v[10:17], v[206:213], v[142:145], v190, v190 op_sel_hi:[0,0,0]
	v_mfma_scale_f32_16x16x128_f8f6f4 v[134:137], v[2:9], v[214:221], v[134:137], v190, v190 op_sel_hi:[0,0,0]
	v_mfma_scale_f32_16x16x128_f8f6f4 v[126:129], v[10:17], v[214:221], v[126:129], v190, v190 op_sel_hi:[0,0,0]
	v_mfma_scale_f32_16x16x128_f8f6f4 v[118:121], v[2:9], v[222:229], v[118:121], v190, v190 op_sel_hi:[0,0,0]
	v_mfma_scale_f32_16x16x128_f8f6f4 v[110:113], v[10:17], v[222:229], v[110:113], v190, v190 op_sel_hi:[0,0,0]
	s_setprio 0
	s_setprio 1
	v_mfma_scale_f32_16x16x128_f8f6f4 v[146:149], v[18:25], v[198:205], v[146:149], v190, v190 op_sel_hi:[0,0,0]
	v_mfma_scale_f32_16x16x128_f8f6f4 v[138:141], v[26:33], v[198:205], v[138:141], v190, v190 op_sel_hi:[0,0,0]
	v_mfma_scale_f32_16x16x128_f8f6f4 v[130:133], v[18:25], v[206:213], v[130:133], v190, v190 op_sel_hi:[0,0,0]
	v_mfma_scale_f32_16x16x128_f8f6f4 v[122:125], v[26:33], v[206:213], v[122:125], v190, v190 op_sel_hi:[0,0,0]
	v_mfma_scale_f32_16x16x128_f8f6f4 v[114:117], v[18:25], v[214:221], v[114:117], v190, v190 op_sel_hi:[0,0,0]
	v_mfma_scale_f32_16x16x128_f8f6f4 v[106:109], v[26:33], v[214:221], v[106:109], v190, v190 op_sel_hi:[0,0,0]
	v_mfma_scale_f32_16x16x128_f8f6f4 v[102:105], v[18:25], v[222:229], v[102:105], v190, v190 op_sel_hi:[0,0,0]
	v_mfma_scale_f32_16x16x128_f8f6f4 v[98:101], v[26:33], v[222:229], v[98:101], v190, v190 op_sel_hi:[0,0,0]
	s_setprio 0
	s_barrier
	s_add_i32 s30, s63, s34
	v_lshl_add_u64 v[184:185], v[184:185], 0, s[12:13]
	s_mov_b32 m0, s30
	ds_read_b128 v[198:201], v196 offset:49152
	ds_read_b128 v[202:205], v196 offset:50176
	ds_read_b128 v[206:209], v196 offset:51200
	ds_read_b128 v[210:213], v196 offset:52224
	ds_read_b128 v[214:217], v196 offset:53248
	ds_read_b128 v[218:221], v196 offset:54272
	ds_read_b128 v[222:225], v196 offset:55296
	ds_read_b128 v[226:229], v196 offset:56320
	global_load_lds_dwordx4 v[184:185], off
	s_add_i32 m0, s30, 0x2000
	s_add_u32 s28, s28, 0xb0080
	v_lshl_add_u64 v[182:183], v[182:183], 0, s[12:13]
	s_addc_u32 s29, s29, 0
	s_add_i32 s30, s66, s34
	global_load_lds_dwordx4 v[182:183], off
	v_lshl_add_u64 v[182:183], s[28:29], 0, v[162:163]
	s_mov_b32 m0, s30
	s_nop 0
	global_load_lds_dwordx4 v[182:183], off
	v_lshl_add_u64 v[182:183], s[28:29], 0, v[164:165]
	s_add_i32 m0, s30, 0x2000
	s_nop 0
	global_load_lds_dwordx4 v[182:183], off
	v_lshl_add_u64 v[182:183], v[186:187], 0, s[12:13]
	s_mov_b32 m0, s40
	s_nop 0
	global_load_lds_dwordx4 v[182:183], off
	v_lshl_add_u64 v[182:183], v[188:189], 0, s[12:13]
	s_mov_b32 m0, s41
	s_nop 0
	global_load_lds_dwordx4 v[182:183], off
	s_waitcnt vmcnt(8)
	s_waitcnt lgkmcnt(0)
	s_barrier
	s_setprio 1
	s_waitcnt lgkmcnt(0)
	v_mfma_scale_f32_16x16x128_f8f6f4 v[94:97], v[2:9], v[198:205], v[94:97], v190, v190 op_sel_hi:[0,0,0]
	v_mfma_scale_f32_16x16x128_f8f6f4 v[90:93], v[10:17], v[198:205], v[90:93], v190, v190 op_sel_hi:[0,0,0]
	v_mfma_scale_f32_16x16x128_f8f6f4 v[86:89], v[2:9], v[206:213], v[86:89], v190, v190 op_sel_hi:[0,0,0]
	v_mfma_scale_f32_16x16x128_f8f6f4 v[78:81], v[10:17], v[206:213], v[78:81], v190, v190 op_sel_hi:[0,0,0]
	v_mfma_scale_f32_16x16x128_f8f6f4 v[62:65], v[2:9], v[214:221], v[62:65], v190, v190 op_sel_hi:[0,0,0]
	v_mfma_scale_f32_16x16x128_f8f6f4 v[54:57], v[10:17], v[214:221], v[54:57], v190, v190 op_sel_hi:[0,0,0]
	v_mfma_scale_f32_16x16x128_f8f6f4 v[46:49], v[2:9], v[222:229], v[46:49], v190, v190 op_sel_hi:[0,0,0]
	v_mfma_scale_f32_16x16x128_f8f6f4 v[38:41], v[10:17], v[222:229], v[38:41], v190, v190 op_sel_hi:[0,0,0]
	s_setprio 0
	s_setprio 1
	v_mfma_scale_f32_16x16x128_f8f6f4 v[82:85], v[18:25], v[198:205], v[82:85], v190, v190 op_sel_hi:[0,0,0]
	v_mfma_scale_f32_16x16x128_f8f6f4 v[74:77], v[26:33], v[198:205], v[74:77], v190, v190 op_sel_hi:[0,0,0]
	v_mfma_scale_f32_16x16x128_f8f6f4 v[58:61], v[18:25], v[206:213], v[58:61], v190, v190 op_sel_hi:[0,0,0]
	v_mfma_scale_f32_16x16x128_f8f6f4 v[50:53], v[26:33], v[206:213], v[50:53], v190, v190 op_sel_hi:[0,0,0]
	v_mfma_scale_f32_16x16x128_f8f6f4 v[42:45], v[18:25], v[214:221], v[42:45], v190, v190 op_sel_hi:[0,0,0]
	v_mfma_scale_f32_16x16x128_f8f6f4 v[34:37], v[26:33], v[214:221], v[34:37], v190, v190 op_sel_hi:[0,0,0]
	v_mfma_scale_f32_16x16x128_f8f6f4 v[70:73], v[18:25], v[222:229], v[70:73], v190, v190 op_sel_hi:[0,0,0]
	v_mfma_scale_f32_16x16x128_f8f6f4 v[66:69], v[26:33], v[222:229], v[66:69], v190, v190 op_sel_hi:[0,0,0]
	s_setprio 0
	s_add_i32 s62, s62, 2
	s_cmp_gt_u32 s62, 41
	s_mov_b64 s[30:31], s[26:27]
	s_barrier
	s_cbranch_scc0 .LBB0_1237
	s_and_b64 vcc, exec, s[14:15]
	s_cbranch_vccz .LBB0_1240
	s_barrier

; #define PG8_STAGE(bufoff, gbase, voff) do { _Pragma("unroll") for (int _i = 0; _i < 2; ++_i) \
;         __builtin_amdgcn_global_load_lds((const unsigned*)((const char*)(gbase) + (voff)[_i]), (LAS unsigned*)(lds + (bufoff) + ldsw + _i * 8192), 16, 0, 0); } while (0)
; #define PG8_LDA(dst, b, h) do { _Pragma("unroll") for (int m = 0; m < 4; ++m) dst[m] = PG8_LD32(lds + PG8_SA(b, h) + aoff + m * 2048); } while (0)
; #define PG8_LDB(dst, b, h) do { _Pragma("unroll") for (int n = 0; n < 2; ++n) dst[n] = PG8_LD32(lds + PG8_SB(b, h) + boff + n * 2048); } while (0)
; #define PG8_WAIT_V(n) asm volatile("s_waitcnt vmcnt(" #n ")" ::: "memory")
; #define PG8_WAIT_L(n) asm volatile("s_waitcnt lgkmcnt(" #n ")" ::: "memory")
; #define PG8_BAR __builtin_amdgcn_s_barrier()
; #define PG8_SCHED __builtin_amdgcn_sched_barrier(0)
; #define PG8_STA(bufoff, nextflag, h, koff) do { if constexpr (Sched::GATHER) { unsigned _o[2]; _o[0] = (nextflag) ? nxtA[h][0] : curA[h][0]; _o[1] = (nextflag) ? nxtA[h][1] : curA[h][1]; PG8_STAGE(bufoff, Ab + (koff), _o); } \
;         else { PG8_STAGE(bufoff, ((nextflag) ? nA : cA) + (size_t)(h) * hstep + (koff), voffA); } } while (0)
; template <class Epi, class Sched, bool ALIGN_EPI, int DT>
; __device__ __forceinline__ void gemm_phase(LAS unsigned char* lds, const int KB, const Sched& S, const Epi& E) {
;     ...
;             const size_t k1 = (size_t)(t + 1) * kstep, k2 = last ? 0 : (size_t)(t + 2) * kstep, k3 = k2 + kstep;
;             const char* b2 = last ? nB : cB + (size_t)(t + 2) * kstep; const char* b3 = b2 + kstep;
;             PG8_LDB(B0, 0, 0); PG8_LDB(B1, 0, 1); PG8_SCHED; PG8_LDA(At, 0, 0); PG8_STA(PG8_SA(1, 1), false, 1, k1);
;             PG8_WAIT_V(8); PG8_WAIT_L(0); PG8_BAR; PG8_MMA(0, 0, At, B0); PG8_MMA(0, 1, At, B1); PG8_BAR; PG8_SCHED;
;             PG8_LDA(At, 0, 1); PG8_STAGE(PG8_SB(0, 0), b2, voffB); PG8_STAGE(PG8_SB(0, 1), b2 + hstep, voffB); PG8_STA(PG8_SA(0, 0), last, 0, k2);
;             PG8_WAIT_V(8); PG8_WAIT_L(0); PG8_BAR; PG8_MMA(1, 0, At, B0); PG8_MMA(1, 1, At, B1); PG8_BAR; PG8_SCHED;
.LBB0_1385:
	ds_read_b128 v[152:155], v174
	ds_read_b128 v[156:159], v174 offset:1024
	ds_read_b128 v[160:163], v174 offset:2048
	ds_read_b128 v[164:167], v174 offset:3072
	ds_read_b128 v[168:171], v175
	ds_read_b128 v[180:183], v175 offset:1024
	ds_read_b128 v[184:187], v175 offset:2048
	ds_read_b128 v[188:191], v175 offset:3072
	s_add_u32 s38, s36, 0x100
	s_addc_u32 s39, s37, 0
	s_add_u32 s74, s25, s36
	s_addc_u32 s75, s70, s37
	s_cmp_eq_u32 s71, 12
	s_cselect_b64 s[42:43], -1, 0
	s_and_b64 s[40:41], s[42:43], exec
	s_cselect_b32 s76, 0, s38
	s_cselect_b32 s41, s0, s75
	s_cselect_b32 s40, s23, s74
	v_lshl_add_u64 v[192:193], v[148:149], 0, s[36:37]
	s_add_i32 m0, s47, 0xc000
	ds_read_b128 v[196:199], v176
	ds_read_b128 v[200:203], v176 offset:1024
	ds_read_b128 v[204:207], v176 offset:2048
	ds_read_b128 v[208:211], v176 offset:3072
	ds_read_b128 v[212:215], v176 offset:4096
	ds_read_b128 v[216:219], v176 offset:5120
	ds_read_b128 v[220:223], v176 offset:6144
	ds_read_b128 v[224:227], v176 offset:7168
	global_load_lds_dwordx4 v[192:193], off
	v_lshl_add_u64 v[192:193], v[150:151], 0, s[36:37]
	s_add_i32 m0, s47, 0xe000
	s_nop 0
	global_load_lds_dwordx4 v[192:193], off
	s_waitcnt vmcnt(8)
	s_waitcnt lgkmcnt(0)
	s_barrier
	s_setprio 1
	s_waitcnt lgkmcnt(0)
	v_mfma_i32_16x16x64_i8 v[126:129], v[152:155], v[196:199], v[126:129]
	v_mfma_i32_16x16x64_i8 v[122:125], v[160:163], v[196:199], v[122:125]
	v_mfma_i32_16x16x64_i8 v[110:113], v[152:155], v[204:207], v[110:113]
	v_mfma_i32_16x16x64_i8 v[106:109], v[160:163], v[204:207], v[106:109]
	v_mfma_i32_16x16x64_i8 v[94:97], v[152:155], v[212:215], v[94:97]
	v_mfma_i32_16x16x64_i8 v[90:93], v[160:163], v[212:215], v[90:93]
	v_mfma_i32_16x16x64_i8 v[78:81], v[152:155], v[220:223], v[78:81]
	v_mfma_i32_16x16x64_i8 v[74:77], v[160:163], v[220:223], v[74:77]
	v_mfma_i32_16x16x64_i8 v[126:129], v[156:159], v[200:203], v[126:129]
	v_mfma_i32_16x16x64_i8 v[122:125], v[164:167], v[200:203], v[122:125]
	v_mfma_i32_16x16x64_i8 v[110:113], v[156:159], v[208:211], v[110:113]
	v_mfma_i32_16x16x64_i8 v[106:109], v[164:167], v[208:211], v[106:109]
	v_mfma_i32_16x16x64_i8 v[94:97], v[156:159], v[216:219], v[94:97]
	v_mfma_i32_16x16x64_i8 v[90:93], v[164:167], v[216:219], v[90:93]
	v_mfma_i32_16x16x64_i8 v[78:81], v[156:159], v[224:227], v[78:81]
	v_mfma_i32_16x16x64_i8 v[74:77], v[164:167], v[224:227], v[74:77]
	s_setprio 0
	s_setprio 1
	v_mfma_i32_16x16x64_i8 v[118:121], v[168:171], v[196:199], v[118:121]
	v_mfma_i32_16x16x64_i8 v[114:117], v[184:187], v[196:199], v[114:117]
	v_mfma_i32_16x16x64_i8 v[102:105], v[168:171], v[204:207], v[102:105]
	v_mfma_i32_16x16x64_i8 v[98:101], v[184:187], v[204:207], v[98:101]
	v_mfma_i32_16x16x64_i8 v[86:89], v[168:171], v[212:215], v[86:89]
	v_mfma_i32_16x16x64_i8 v[82:85], v[184:187], v[212:215], v[82:85]
	v_mfma_i32_16x16x64_i8 v[70:73], v[168:171], v[220:223], v[70:73]
	v_mfma_i32_16x16x64_i8 v[66:69], v[184:187], v[220:223], v[66:69]
	v_mfma_i32_16x16x64_i8 v[118:121], v[180:183], v[200:203], v[118:121]
	v_mfma_i32_16x16x64_i8 v[114:117], v[188:191], v[200:203], v[114:117]
	v_mfma_i32_16x16x64_i8 v[102:105], v[180:183], v[208:211], v[102:105]
	v_mfma_i32_16x16x64_i8 v[98:101], v[188:191], v[208:211], v[98:101]
	v_mfma_i32_16x16x64_i8 v[86:89], v[180:183], v[216:219], v[86:89]
	v_mfma_i32_16x16x64_i8 v[82:85], v[188:191], v[216:219], v[82:85]
	v_mfma_i32_16x16x64_i8 v[70:73], v[180:183], v[224:227], v[70:73]
	v_mfma_i32_16x16x64_i8 v[66:69], v[188:191], v[224:227], v[66:69]
	s_setprio 0
	s_barrier
	s_add_i32 s36, s66, s44
	v_lshl_add_u64 v[192:193], s[40:41], 0, v[134:135]
	s_mov_b32 m0, s36
	ds_read_b128 v[196:199], v176 offset:16384
	ds_read_b128 v[200:203], v176 offset:17408
	ds_read_b128 v[204:207], v176 offset:18432
	ds_read_b128 v[208:211], v176 offset:19456
	ds_read_b128 v[212:215], v176 offset:20480
	ds_read_b128 v[216:219], v176 offset:21504
	ds_read_b128 v[220:223], v176 offset:22528
	ds_read_b128 v[224:227], v176 offset:23552
	global_load_lds_dwordx4 v[192:193], off
	s_add_i32 m0, s36, 0x2000
	s_add_u32 s36, s40, 0x40000
	v_lshl_add_u64 v[228:229], s[40:41], 0, v[132:133]
	s_addc_u32 s37, s41, 0
	s_add_i32 s74, s67, s44
	global_load_lds_dwordx4 v[228:229], off
	v_lshl_add_u64 v[230:231], s[36:37], 0, v[134:135]
	s_mov_b32 m0, s74
	s_nop 0
	global_load_lds_dwordx4 v[230:231], off
	v_lshl_add_u64 v[230:231], s[36:37], 0, v[132:133]
	s_add_i32 m0, s74, 0x2000
	s_and_b64 s[36:37], s[8:9], s[42:43]
	s_and_b64 s[36:37], s[36:37], exec
	s_cselect_b32 s36, s26, s34
	s_cselect_b32 s37, s27, s35
	s_add_u32 s36, s36, s76
	s_addc_u32 s37, s37, 0
	global_load_lds_dwordx4 v[230:231], off
	v_lshl_add_u64 v[230:231], s[36:37], 0, v[136:137]
	s_mov_b32 m0, s47
	v_lshl_add_u64 v[232:233], s[36:37], 0, v[138:139]
	global_load_lds_dwordx4 v[230:231], off
	s_mov_b32 m0, s49
	s_nop 0
	global_load_lds_dwordx4 v[232:233], off
	s_waitcnt vmcnt(8)
	s_waitcnt lgkmcnt(0)
	s_barrier
; #define PG8_LDA(dst, b, h) do { _Pragma("unroll") for (int m = 0; m < 4; ++m) dst[m] = PG8_LD32(lds + PG8_SA(b, h) + aoff + m * 2048); } while (0)
; #define PG8_LDB(dst, b, h) do { _Pragma("unroll") for (int n = 0; n < 2; ++n) dst[n] = PG8_LD32(lds + PG8_SB(b, h) + boff + n * 2048); } while (0)
; #define PG8_WAIT_V(n) asm volatile("s_waitcnt vmcnt(" #n ")" ::: "memory")
; #define PG8_WAIT_L(n) asm volatile("s_waitcnt lgkmcnt(" #n ")" ::: "memory")
; #define PG8_BAR __builtin_amdgcn_s_barrier()
; #define PG8_SCHED __builtin_amdgcn_sched_barrier(0)
; #define PG8_STA(bufoff, nextflag, h, koff) do { if constexpr (Sched::GATHER) { unsigned _o[2]; _o[0] = (nextflag) ? nxtA[h][0] : curA[h][0]; _o[1] = (nextflag) ? nxtA[h][1] : curA[h][1]; PG8_STAGE(bufoff, Ab + (koff), _o); } \
;         else { PG8_STAGE(bufoff, ((nextflag) ? nA : cA) + (size_t)(h) * hstep + (koff), voffA); } } while (0)
; template <class Epi, class Sched, bool ALIGN_EPI, int DT>
; __device__ __forceinline__ void gemm_phase(LAS unsigned char* lds, const int KB, const Sched& S, const Epi& E) {
;     ...
;             PG8_WAIT_V(8); PG8_WAIT_L(0); PG8_BAR; PG8_MMA(1, 0, At, B0); PG8_MMA(1, 1, At, B1); PG8_BAR; PG8_SCHED;
;             PG8_LDB(B0, 1, 0); PG8_LDB(B1, 1, 1); PG8_SCHED; PG8_LDA(At, 1, 0); PG8_STA(PG8_SA(0, 1), last, 1, k2);
;             PG8_WAIT_V(8); PG8_WAIT_L(0); PG8_BAR; PG8_MMA(0, 0, At, B0); PG8_MMA(0, 1, At, B1); PG8_BAR; PG8_SCHED;
	s_setprio 1
	s_waitcnt lgkmcnt(0)
	v_mfma_i32_16x16x64_i8 v[62:65], v[152:155], v[196:199], v[62:65]
	v_mfma_i32_16x16x64_i8 v[58:61], v[160:163], v[196:199], v[58:61]
	v_mfma_i32_16x16x64_i8 v[46:49], v[152:155], v[204:207], v[46:49]
	v_mfma_i32_16x16x64_i8 v[42:45], v[160:163], v[204:207], v[42:45]
	v_mfma_i32_16x16x64_i8 v[30:33], v[152:155], v[212:215], v[30:33]
	v_mfma_i32_16x16x64_i8 v[26:29], v[160:163], v[212:215], v[26:29]
	v_mfma_i32_16x16x64_i8 v[6:9], v[152:155], v[220:223], v[6:9]
	v_mfma_i32_16x16x64_i8 v[2:5], v[160:163], v[220:223], v[2:5]
	v_mfma_i32_16x16x64_i8 v[62:65], v[156:159], v[200:203], v[62:65]
	v_mfma_i32_16x16x64_i8 v[58:61], v[164:167], v[200:203], v[58:61]
	v_mfma_i32_16x16x64_i8 v[46:49], v[156:159], v[208:211], v[46:49]
	v_mfma_i32_16x16x64_i8 v[42:45], v[164:167], v[208:211], v[42:45]
	v_mfma_i32_16x16x64_i8 v[30:33], v[156:159], v[216:219], v[30:33]
	v_mfma_i32_16x16x64_i8 v[26:29], v[164:167], v[216:219], v[26:29]
	v_mfma_i32_16x16x64_i8 v[6:9], v[156:159], v[224:227], v[6:9]
	v_mfma_i32_16x16x64_i8 v[2:5], v[164:167], v[224:227], v[2:5]
	s_setprio 0
	s_setprio 1
	v_mfma_i32_16x16x64_i8 v[54:57], v[168:171], v[196:199], v[54:57]
	v_mfma_i32_16x16x64_i8 v[50:53], v[184:187], v[196:199], v[50:53]
	v_mfma_i32_16x16x64_i8 v[38:41], v[168:171], v[204:207], v[38:41]
	v_mfma_i32_16x16x64_i8 v[34:37], v[184:187], v[204:207], v[34:37]
	v_mfma_i32_16x16x64_i8 v[14:17], v[168:171], v[212:215], v[14:17]
	v_mfma_i32_16x16x64_i8 v[10:13], v[184:187], v[212:215], v[10:13]
	v_mfma_i32_16x16x64_i8 v[22:25], v[168:171], v[220:223], v[22:25]
	v_mfma_i32_16x16x64_i8 v[18:21], v[184:187], v[220:223], v[18:21]
	v_mfma_i32_16x16x64_i8 v[54:57], v[180:183], v[200:203], v[54:57]
	v_mfma_i32_16x16x64_i8 v[50:53], v[188:191], v[200:203], v[50:53]
	v_mfma_i32_16x16x64_i8 v[38:41], v[180:183], v[208:211], v[38:41]
	v_mfma_i32_16x16x64_i8 v[34:37], v[188:191], v[208:211], v[34:37]
	v_mfma_i32_16x16x64_i8 v[14:17], v[180:183], v[216:219], v[14:17]
	v_mfma_i32_16x16x64_i8 v[10:13], v[188:191], v[216:219], v[10:13]
	v_mfma_i32_16x16x64_i8 v[22:25], v[180:183], v[224:227], v[22:25]
	v_mfma_i32_16x16x64_i8 v[18:21], v[188:191], v[224:227], v[18:21]
	s_setprio 0
	s_barrier
	s_add_i32 s42, 0, 0x18000
	v_add_u32_e32 v1, s42, v172
	s_add_i32 s43, 0, 0x1c000
	ds_read_b128 v[152:155], v1
	ds_read_b128 v[156:159], v1 offset:1024
	ds_read_b128 v[160:163], v1 offset:2048
	ds_read_b128 v[164:167], v1 offset:3072
	v_add_u32_e32 v1, s43, v172
	ds_read_b128 v[168:171], v1
	ds_read_b128 v[180:183], v1 offset:1024
	ds_read_b128 v[184:187], v1 offset:2048
	ds_read_b128 v[188:191], v1 offset:3072
	s_add_u32 s36, s36, 0x40000
	s_addc_u32 s37, s37, 0
	s_mov_b32 m0, s52
	v_lshl_add_u64 v[234:235], s[36:37], 0, v[136:137]
	ds_read_b128 v[196:199], v176 offset:32768
	ds_read_b128 v[200:203], v176 offset:33792
	ds_read_b128 v[204:207], v176 offset:34816
	ds_read_b128 v[208:211], v176 offset:35840
	ds_read_b128 v[212:215], v176 offset:36864
	ds_read_b128 v[216:219], v176 offset:37888
	ds_read_b128 v[220:223], v176 offset:38912
	ds_read_b128 v[224:227], v176 offset:39936
	global_load_lds_dwordx4 v[234:235], off
	v_lshl_add_u64 v[234:235], s[36:37], 0, v[138:139]
	s_mov_b32 m0, s53
	s_nop 0
	global_load_lds_dwordx4 v[234:235], off
	s_waitcnt vmcnt(8)
	s_waitcnt lgkmcnt(0)
	s_barrier
	s_setprio 1
	s_waitcnt lgkmcnt(0)
	v_mfma_i32_16x16x64_i8 v[126:129], v[152:155], v[196:199], v[126:129]
	v_mfma_i32_16x16x64_i8 v[122:125], v[160:163], v[196:199], v[122:125]
	v_mfma_i32_16x16x64_i8 v[110:113], v[152:155], v[204:207], v[110:113]
	v_mfma_i32_16x16x64_i8 v[106:109], v[160:163], v[204:207], v[106:109]
	v_mfma_i32_16x16x64_i8 v[94:97], v[152:155], v[212:215], v[94:97]
	v_mfma_i32_16x16x64_i8 v[90:93], v[160:163], v[212:215], v[90:93]
	v_mfma_i32_16x16x64_i8 v[78:81], v[152:155], v[220:223], v[78:81]
	v_mfma_i32_16x16x64_i8 v[74:77], v[160:163], v[220:223], v[74:77]
	v_mfma_i32_16x16x64_i8 v[126:129], v[156:159], v[200:203], v[126:129]
	v_mfma_i32_16x16x64_i8 v[122:125], v[164:167], v[200:203], v[122:125]
	v_mfma_i32_16x16x64_i8 v[110:113], v[156:159], v[208:211], v[110:113]
	v_mfma_i32_16x16x64_i8 v[106:109], v[164:167], v[208:211], v[106:109]
	v_mfma_i32_16x16x64_i8 v[94:97], v[156:159], v[216:219], v[94:97]
	v_mfma_i32_16x16x64_i8 v[90:93], v[164:167], v[216:219], v[90:93]
	v_mfma_i32_16x16x64_i8 v[78:81], v[156:159], v[224:227], v[78:81]
	v_mfma_i32_16x16x64_i8 v[74:77], v[164:167], v[224:227], v[74:77]
	s_setprio 0
	s_setprio 1
	v_mfma_i32_16x16x64_i8 v[118:121], v[168:171], v[196:199], v[118:121]
	v_mfma_i32_16x16x64_i8 v[114:117], v[184:187], v[196:199], v[114:117]
	v_mfma_i32_16x16x64_i8 v[102:105], v[168:171], v[204:207], v[102:105]
	v_mfma_i32_16x16x64_i8 v[98:101], v[184:187], v[204:207], v[98:101]
	v_mfma_i32_16x16x64_i8 v[86:89], v[168:171], v[212:215], v[86:89]
	v_mfma_i32_16x16x64_i8 v[82:85], v[184:187], v[212:215], v[82:85]
	v_mfma_i32_16x16x64_i8 v[70:73], v[168:171], v[220:223], v[70:73]
	v_mfma_i32_16x16x64_i8 v[66:69], v[184:187], v[220:223], v[66:69]
	v_mfma_i32_16x16x64_i8 v[118:121], v[180:183], v[200:203], v[118:121]
	v_mfma_i32_16x16x64_i8 v[114:117], v[188:191], v[200:203], v[114:117]
	v_mfma_i32_16x16x64_i8 v[102:105], v[180:183], v[208:211], v[102:105]
	v_mfma_i32_16x16x64_i8 v[98:101], v[188:191], v[208:211], v[98:101]
	v_mfma_i32_16x16x64_i8 v[86:89], v[180:183], v[216:219], v[86:89]
	v_mfma_i32_16x16x64_i8 v[82:85], v[188:191], v[216:219], v[82:85]
	v_mfma_i32_16x16x64_i8 v[70:73], v[180:183], v[224:227], v[70:73]
	v_mfma_i32_16x16x64_i8 v[66:69], v[188:191], v[224:227], v[66:69]
	s_setprio 0
	s_barrier
; #define PG8_STAGE(bufoff, gbase, voff) do { _Pragma("unroll") for (int _i = 0; _i < 2; ++_i) \
;         __builtin_amdgcn_global_load_lds((const unsigned*)((const char*)(gbase) + (voff)[_i]), (LAS unsigned*)(lds + (bufoff) + ldsw + _i * 8192), 16, 0, 0); } while (0)
; #define PG8_LDA(dst, b, h) do { _Pragma("unroll") for (int m = 0; m < 4; ++m) dst[m] = PG8_LD32(lds + PG8_SA(b, h) + aoff + m * 2048); } while (0)
; #define PG8_WAIT_V(n) asm volatile("s_waitcnt vmcnt(" #n ")" ::: "memory")
; #define PG8_WAIT_L(n) asm volatile("s_waitcnt lgkmcnt(" #n ")" ::: "memory")
; #define PG8_BAR __builtin_amdgcn_s_barrier()
; #define PG8_SCHED __builtin_amdgcn_sched_barrier(0)
; #define PG8_STA(bufoff, nextflag, h, koff) do { if constexpr (Sched::GATHER) { unsigned _o[2]; _o[0] = (nextflag) ? nxtA[h][0] : curA[h][0]; _o[1] = (nextflag) ? nxtA[h][1] : curA[h][1]; PG8_STAGE(bufoff, Ab + (koff), _o); } \
;         else { PG8_STAGE(bufoff, ((nextflag) ? nA : cA) + (size_t)(h) * hstep + (koff), voffA); } } while (0)
; template <class Epi, class Sched, bool ALIGN_EPI, int DT>
; __device__ __forceinline__ void gemm_phase(LAS unsigned char* lds, const int KB, const Sched& S, const Epi& E) {
;     ...
;         for (int t = 0; t < nt; t += 2) {
;             const bool last = (t == nt - 2);
;             const size_t k1 = (size_t)(t + 1) * kstep, k2 = last ? 0 : (size_t)(t + 2) * kstep, k3 = k2 + kstep;
;     ...
;             PG8_LDA(At, 1, 1); PG8_STAGE(PG8_SB(1, 0), b3, voffB); PG8_STAGE(PG8_SB(1, 1), b3 + hstep, voffB); PG8_STA(PG8_SA(1, 0), last, 0, k3);
;             PG8_WAIT_V(8); PG8_WAIT_L(0); PG8_BAR; PG8_MMA(1, 0, At, B0); PG8_MMA(1, 1, At, B1); PG8_BAR; PG8_SCHED;
	s_add_i32 s36, s42, s44
	v_lshl_add_u64 v[192:193], v[192:193], 0, s[18:19]
	s_mov_b32 m0, s36
	ds_read_b128 v[196:199], v176 offset:49152
	ds_read_b128 v[200:203], v176 offset:50176
	ds_read_b128 v[204:207], v176 offset:51200
	ds_read_b128 v[208:211], v176 offset:52224
	ds_read_b128 v[212:215], v176 offset:53248
	ds_read_b128 v[216:219], v176 offset:54272
	ds_read_b128 v[220:223], v176 offset:55296
	ds_read_b128 v[224:227], v176 offset:56320
	global_load_lds_dwordx4 v[192:193], off
	s_add_i32 m0, s36, 0x2000
	s_add_u32 s36, s40, 0x40080
	v_lshl_add_u64 v[192:193], v[228:229], 0, s[18:19]
	s_addc_u32 s37, s41, 0
	s_add_i32 s40, s43, s44
	global_load_lds_dwordx4 v[192:193], off
	v_lshl_add_u64 v[192:193], s[36:37], 0, v[134:135]
	s_mov_b32 m0, s40
	s_nop 0
	global_load_lds_dwordx4 v[192:193], off
	v_lshl_add_u64 v[192:193], s[36:37], 0, v[132:133]
	s_add_i32 m0, s40, 0x2000
	s_nop 0
	global_load_lds_dwordx4 v[192:193], off
	v_lshl_add_u64 v[192:193], v[230:231], 0, s[18:19]
	s_mov_b32 m0, s57
	s_nop 0
	global_load_lds_dwordx4 v[192:193], off
	v_lshl_add_u64 v[192:193], v[232:233], 0, s[18:19]
	s_mov_b32 m0, s62
	s_nop 0
	global_load_lds_dwordx4 v[192:193], off
	s_waitcnt vmcnt(8)
	s_waitcnt lgkmcnt(0)
	s_barrier
	s_setprio 1
	s_waitcnt lgkmcnt(0)
	v_mfma_i32_16x16x64_i8 v[62:65], v[152:155], v[196:199], v[62:65]
	v_mfma_i32_16x16x64_i8 v[58:61], v[160:163], v[196:199], v[58:61]
	v_mfma_i32_16x16x64_i8 v[46:49], v[152:155], v[204:207], v[46:49]
	v_mfma_i32_16x16x64_i8 v[42:45], v[160:163], v[204:207], v[42:45]
	v_mfma_i32_16x16x64_i8 v[30:33], v[152:155], v[212:215], v[30:33]
	v_mfma_i32_16x16x64_i8 v[26:29], v[160:163], v[212:215], v[26:29]
	v_mfma_i32_16x16x64_i8 v[6:9], v[152:155], v[220:223], v[6:9]
	v_mfma_i32_16x16x64_i8 v[2:5], v[160:163], v[220:223], v[2:5]
	v_mfma_i32_16x16x64_i8 v[62:65], v[156:159], v[200:203], v[62:65]
	v_mfma_i32_16x16x64_i8 v[58:61], v[164:167], v[200:203], v[58:61]
	v_mfma_i32_16x16x64_i8 v[46:49], v[156:159], v[208:211], v[46:49]
	v_mfma_i32_16x16x64_i8 v[42:45], v[164:167], v[208:211], v[42:45]
	v_mfma_i32_16x16x64_i8 v[30:33], v[156:159], v[216:219], v[30:33]
	v_mfma_i32_16x16x64_i8 v[26:29], v[164:167], v[216:219], v[26:29]
	v_mfma_i32_16x16x64_i8 v[6:9], v[156:159], v[224:227], v[6:9]
	v_mfma_i32_16x16x64_i8 v[2:5], v[164:167], v[224:227], v[2:5]
	s_setprio 0
	s_setprio 1
	v_mfma_i32_16x16x64_i8 v[54:57], v[168:171], v[196:199], v[54:57]
	v_mfma_i32_16x16x64_i8 v[50:53], v[184:187], v[196:199], v[50:53]
	v_mfma_i32_16x16x64_i8 v[38:41], v[168:171], v[204:207], v[38:41]
	v_mfma_i32_16x16x64_i8 v[34:37], v[184:187], v[204:207], v[34:37]
	v_mfma_i32_16x16x64_i8 v[14:17], v[168:171], v[212:215], v[14:17]
	v_mfma_i32_16x16x64_i8 v[10:13], v[184:187], v[212:215], v[10:13]
	v_mfma_i32_16x16x64_i8 v[22:25], v[168:171], v[220:223], v[22:25]
	v_mfma_i32_16x16x64_i8 v[18:21], v[184:187], v[220:223], v[18:21]
	v_mfma_i32_16x16x64_i8 v[54:57], v[180:183], v[200:203], v[54:57]
	v_mfma_i32_16x16x64_i8 v[50:53], v[188:191], v[200:203], v[50:53]
	v_mfma_i32_16x16x64_i8 v[38:41], v[180:183], v[208:211], v[38:41]
	v_mfma_i32_16x16x64_i8 v[34:37], v[188:191], v[208:211], v[34:37]
	v_mfma_i32_16x16x64_i8 v[14:17], v[180:183], v[216:219], v[14:17]
	v_mfma_i32_16x16x64_i8 v[10:13], v[188:191], v[216:219], v[10:13]
	v_mfma_i32_16x16x64_i8 v[22:25], v[180:183], v[224:227], v[22:25]
	v_mfma_i32_16x16x64_i8 v[18:21], v[188:191], v[224:227], v[18:21]
	s_setprio 0
	s_add_i32 s71, s71, 2
	s_cmp_gt_u32 s71, 13
	s_mov_b64 s[36:37], s[38:39]
	s_barrier
	s_cbranch_scc0 .LBB0_1385
	s_and_b64 vcc, exec, s[20:21]
	s_cbranch_vccz .LBB0_1388
	s_barrier

; #define PG8_STAGE(bufoff, gbase, voff) do { _Pragma("unroll") for (int _i = 0; _i < 2; ++_i) \
;         __builtin_amdgcn_global_load_lds((const unsigned*)((const char*)(gbase) + (voff)[_i]), (LAS unsigned*)(lds + (bufoff) + ldsw + _i * 8192), 16, 0, 0); } while (0)
; #define PG8_LDA(dst, b, h) do { _Pragma("unroll") for (int m = 0; m < 4; ++m) dst[m] = PG8_LD32(lds + PG8_SA(b, h) + aoff + m * 2048); } while (0)
; #define PG8_LDB(dst, b, h) do { _Pragma("unroll") for (int n = 0; n < 2; ++n) dst[n] = PG8_LD32(lds + PG8_SB(b, h) + boff + n * 2048); } while (0)
; #define PG8_WAIT_V(n) asm volatile("s_waitcnt vmcnt(" #n ")" ::: "memory")
; #define PG8_WAIT_L(n) asm volatile("s_waitcnt lgkmcnt(" #n ")" ::: "memory")
; #define PG8_BAR __builtin_amdgcn_s_barrier()
; #define PG8_SCHED __builtin_amdgcn_sched_barrier(0)
; #define PG8_STA(bufoff, nextflag, h, koff) do { if constexpr (Sched::GATHER) { unsigned _o[2]; _o[0] = (nextflag) ? nxtA[h][0] : curA[h][0]; _o[1] = (nextflag) ? nxtA[h][1] : curA[h][1]; PG8_STAGE(bufoff, Ab + (koff), _o); } \
;         else { PG8_STAGE(bufoff, ((nextflag) ? nA : cA) + (size_t)(h) * hstep + (koff), voffA); } } while (0)
; template <class Epi, class Sched, bool ALIGN_EPI, int DT>
; __device__ __forceinline__ void gemm_phase(LAS unsigned char* lds, const int KB, const Sched& S, const Epi& E) {
;     ...
;             const size_t k1 = (size_t)(t + 1) * kstep, k2 = last ? 0 : (size_t)(t + 2) * kstep, k3 = k2 + kstep;
;             const char* b2 = last ? nB : cB + (size_t)(t + 2) * kstep; const char* b3 = b2 + kstep;
;             PG8_LDB(B0, 0, 0); PG8_LDB(B1, 0, 1); PG8_SCHED; PG8_LDA(At, 0, 0); PG8_STA(PG8_SA(1, 1), false, 1, k1);
;             PG8_WAIT_V(8); PG8_WAIT_L(0); PG8_BAR; PG8_MMA(0, 0, At, B0); PG8_MMA(0, 1, At, B1); PG8_BAR; PG8_SCHED;
;             PG8_LDA(At, 0, 1); PG8_STAGE(PG8_SB(0, 0), b2, voffB); PG8_STAGE(PG8_SB(0, 1), b2 + hstep, voffB); PG8_STA(PG8_SA(0, 0), last, 0, k2);
;             PG8_WAIT_V(8); PG8_WAIT_L(0); PG8_BAR; PG8_MMA(1, 0, At, B0); PG8_MMA(1, 1, At, B1); PG8_BAR; PG8_SCHED;
.LBB0_2108:
	ds_read_b128 v[18:21], v193
	ds_read_b128 v[22:25], v193 offset:1024
	ds_read_b128 v[26:29], v193 offset:2048
	ds_read_b128 v[30:33], v193 offset:3072
	ds_read_b128 v[2:5], v195
	ds_read_b128 v[6:9], v195 offset:1024
	ds_read_b128 v[10:13], v195 offset:2048
	ds_read_b128 v[14:17], v195 offset:3072
	s_add_u32 s38, s42, 0x100
	s_addc_u32 s39, s43, 0
	s_add_u32 s71, s68, s42
	s_addc_u32 s74, s69, s43
	s_cmp_eq_u32 s70, 12
	s_cselect_b64 s[44:45], -1, 0
	s_and_b64 s[40:41], s[44:45], exec
	s_cselect_b32 s41, s25, s74
	s_cselect_b32 s40, s27, s71
	s_cselect_b32 s71, 0, s39
	s_cselect_b32 s74, 0, s38
	v_lshl_add_u64 v[222:223], v[178:179], 0, s[42:43]
	s_add_i32 m0, s35, 0xc000
	ds_read_b128 v[182:185], v196
	ds_read_b128 v[186:189], v196 offset:1024
	ds_read_b128 v[198:201], v196 offset:2048
	ds_read_b128 v[202:205], v196 offset:3072
	ds_read_b128 v[206:209], v196 offset:4096
	ds_read_b128 v[210:213], v196 offset:5120
	ds_read_b128 v[214:217], v196 offset:6144
	ds_read_b128 v[218:221], v196 offset:7168
	global_load_lds_dwordx4 v[222:223], off
	v_lshl_add_u64 v[222:223], v[180:181], 0, s[42:43]
	s_add_i32 m0, s35, 0xe000
	s_nop 0
	global_load_lds_dwordx4 v[222:223], off
	s_waitcnt vmcnt(8)
	s_waitcnt lgkmcnt(0)
	s_barrier
	s_setprio 1
	s_waitcnt lgkmcnt(0)
	v_mfma_scale_f32_16x16x128_f8f6f4 v[158:161], v[18:25], v[182:189], v[158:161], v1, v1 op_sel_hi:[0,0,0]
	v_mfma_scale_f32_16x16x128_f8f6f4 v[154:157], v[26:33], v[182:189], v[154:157], v1, v1 op_sel_hi:[0,0,0]
	v_mfma_scale_f32_16x16x128_f8f6f4 v[150:153], v[18:25], v[198:205], v[150:153], v1, v1 op_sel_hi:[0,0,0]
	v_mfma_scale_f32_16x16x128_f8f6f4 v[142:145], v[26:33], v[198:205], v[142:145], v1, v1 op_sel_hi:[0,0,0]
	v_mfma_scale_f32_16x16x128_f8f6f4 v[134:137], v[18:25], v[206:213], v[134:137], v1, v1 op_sel_hi:[0,0,0]
	v_mfma_scale_f32_16x16x128_f8f6f4 v[126:129], v[26:33], v[206:213], v[126:129], v1, v1 op_sel_hi:[0,0,0]
	v_mfma_scale_f32_16x16x128_f8f6f4 v[118:121], v[18:25], v[214:221], v[118:121], v1, v1 op_sel_hi:[0,0,0]
	v_mfma_scale_f32_16x16x128_f8f6f4 v[110:113], v[26:33], v[214:221], v[110:113], v1, v1 op_sel_hi:[0,0,0]
	s_setprio 0
	s_setprio 1
	v_mfma_scale_f32_16x16x128_f8f6f4 v[146:149], v[2:9], v[182:189], v[146:149], v1, v1 op_sel_hi:[0,0,0]
	v_mfma_scale_f32_16x16x128_f8f6f4 v[138:141], v[10:17], v[182:189], v[138:141], v1, v1 op_sel_hi:[0,0,0]
	v_mfma_scale_f32_16x16x128_f8f6f4 v[130:133], v[2:9], v[198:205], v[130:133], v1, v1 op_sel_hi:[0,0,0]
	v_mfma_scale_f32_16x16x128_f8f6f4 v[122:125], v[10:17], v[198:205], v[122:125], v1, v1 op_sel_hi:[0,0,0]
	v_mfma_scale_f32_16x16x128_f8f6f4 v[114:117], v[2:9], v[206:213], v[114:117], v1, v1 op_sel_hi:[0,0,0]
	v_mfma_scale_f32_16x16x128_f8f6f4 v[106:109], v[10:17], v[206:213], v[106:109], v1, v1 op_sel_hi:[0,0,0]
	v_mfma_scale_f32_16x16x128_f8f6f4 v[102:105], v[2:9], v[214:221], v[102:105], v1, v1 op_sel_hi:[0,0,0]
	v_mfma_scale_f32_16x16x128_f8f6f4 v[98:101], v[10:17], v[214:221], v[98:101], v1, v1 op_sel_hi:[0,0,0]
	s_setprio 0
	s_barrier
	s_add_i32 s42, s57, s46
	v_lshl_add_u64 v[182:183], s[40:41], 0, v[162:163]
	s_mov_b32 m0, s42
	ds_read_b128 v[198:201], v196 offset:16384
	ds_read_b128 v[202:205], v196 offset:17408
	ds_read_b128 v[206:209], v196 offset:18432
	ds_read_b128 v[210:213], v196 offset:19456
	ds_read_b128 v[214:217], v196 offset:20480
	ds_read_b128 v[218:221], v196 offset:21504
	ds_read_b128 v[222:225], v196 offset:22528
	ds_read_b128 v[226:229], v196 offset:23552
	global_load_lds_dwordx4 v[182:183], off
	s_add_i32 m0, s42, 0x2000
	s_add_u32 s42, s40, 0x40000
	v_lshl_add_u64 v[184:185], s[40:41], 0, v[164:165]
	s_addc_u32 s43, s41, 0
	s_add_i32 s75, s62, s46
	global_load_lds_dwordx4 v[184:185], off
	v_lshl_add_u64 v[186:187], s[42:43], 0, v[162:163]
	s_mov_b32 m0, s75
	s_nop 0
	global_load_lds_dwordx4 v[186:187], off
	v_lshl_add_u64 v[186:187], s[42:43], 0, v[164:165]
	s_add_i32 m0, s75, 0x2000
	s_and_b64 s[42:43], s[6:7], s[44:45]
	s_and_b64 s[42:43], s[42:43], exec
	s_cselect_b32 s42, s28, s36
	s_cselect_b32 s43, s29, s37
	s_add_u32 s42, s42, s74
	s_addc_u32 s43, s43, s71
	global_load_lds_dwordx4 v[186:187], off
	v_lshl_add_u64 v[186:187], s[42:43], 0, v[166:167]
	s_mov_b32 m0, s35
	v_lshl_add_u64 v[188:189], s[42:43], 0, v[168:169]
	global_load_lds_dwordx4 v[186:187], off
	s_mov_b32 m0, s47
	s_nop 0
	global_load_lds_dwordx4 v[188:189], off
	s_waitcnt vmcnt(8)
	s_waitcnt lgkmcnt(0)
	s_barrier
	s_setprio 1
	s_waitcnt lgkmcnt(0)
	v_mfma_scale_f32_16x16x128_f8f6f4 v[94:97], v[18:25], v[198:205], v[94:97], v1, v1 op_sel_hi:[0,0,0]
	v_mfma_scale_f32_16x16x128_f8f6f4 v[90:93], v[26:33], v[198:205], v[90:93], v1, v1 op_sel_hi:[0,0,0]
	v_mfma_scale_f32_16x16x128_f8f6f4 v[86:89], v[18:25], v[206:213], v[86:89], v1, v1 op_sel_hi:[0,0,0]
	v_mfma_scale_f32_16x16x128_f8f6f4 v[78:81], v[26:33], v[206:213], v[78:81], v1, v1 op_sel_hi:[0,0,0]
	v_mfma_scale_f32_16x16x128_f8f6f4 v[62:65], v[18:25], v[214:221], v[62:65], v1, v1 op_sel_hi:[0,0,0]
	v_mfma_scale_f32_16x16x128_f8f6f4 v[54:57], v[26:33], v[214:221], v[54:57], v1, v1 op_sel_hi:[0,0,0]
	v_mfma_scale_f32_16x16x128_f8f6f4 v[46:49], v[18:25], v[222:229], v[46:49], v1, v1 op_sel_hi:[0,0,0]
	v_mfma_scale_f32_16x16x128_f8f6f4 v[38:41], v[26:33], v[222:229], v[38:41], v1, v1 op_sel_hi:[0,0,0]
	s_setprio 0
	s_setprio 1
	v_mfma_scale_f32_16x16x128_f8f6f4 v[82:85], v[2:9], v[198:205], v[82:85], v1, v1 op_sel_hi:[0,0,0]
	v_mfma_scale_f32_16x16x128_f8f6f4 v[74:77], v[10:17], v[198:205], v[74:77], v1, v1 op_sel_hi:[0,0,0]
	v_mfma_scale_f32_16x16x128_f8f6f4 v[58:61], v[2:9], v[206:213], v[58:61], v1, v1 op_sel_hi:[0,0,0]
	v_mfma_scale_f32_16x16x128_f8f6f4 v[50:53], v[10:17], v[206:213], v[50:53], v1, v1 op_sel_hi:[0,0,0]
	v_mfma_scale_f32_16x16x128_f8f6f4 v[42:45], v[2:9], v[214:221], v[42:45], v1, v1 op_sel_hi:[0,0,0]
	v_mfma_scale_f32_16x16x128_f8f6f4 v[34:37], v[10:17], v[214:221], v[34:37], v1, v1 op_sel_hi:[0,0,0]
	v_mfma_scale_f32_16x16x128_f8f6f4 v[70:73], v[2:9], v[222:229], v[70:73], v1, v1 op_sel_hi:[0,0,0]
	v_mfma_scale_f32_16x16x128_f8f6f4 v[66:69], v[10:17], v[222:229], v[66:69], v1, v1 op_sel_hi:[0,0,0]
	s_setprio 0
	s_barrier
; #define PG8_STAGE(bufoff, gbase, voff) do { _Pragma("unroll") for (int _i = 0; _i < 2; ++_i) \
;         __builtin_amdgcn_global_load_lds((const unsigned*)((const char*)(gbase) + (voff)[_i]), (LAS unsigned*)(lds + (bufoff) + ldsw + _i * 8192), 16, 0, 0); } while (0)
; #define PG8_LDA(dst, b, h) do { _Pragma("unroll") for (int m = 0; m < 4; ++m) dst[m] = PG8_LD32(lds + PG8_SA(b, h) + aoff + m * 2048); } while (0)
; #define PG8_LDB(dst, b, h) do { _Pragma("unroll") for (int n = 0; n < 2; ++n) dst[n] = PG8_LD32(lds + PG8_SB(b, h) + boff + n * 2048); } while (0)
; #define PG8_WAIT_V(n) asm volatile("s_waitcnt vmcnt(" #n ")" ::: "memory")
; #define PG8_WAIT_L(n) asm volatile("s_waitcnt lgkmcnt(" #n ")" ::: "memory")
; #define PG8_BAR __builtin_amdgcn_s_barrier()
; #define PG8_SCHED __builtin_amdgcn_sched_barrier(0)
; #define PG8_STA(bufoff, nextflag, h, koff) do { if constexpr (Sched::GATHER) { unsigned _o[2]; _o[0] = (nextflag) ? nxtA[h][0] : curA[h][0]; _o[1] = (nextflag) ? nxtA[h][1] : curA[h][1]; PG8_STAGE(bufoff, Ab + (koff), _o); } \
;         else { PG8_STAGE(bufoff, ((nextflag) ? nA : cA) + (size_t)(h) * hstep + (koff), voffA); } } while (0)
; template <class Epi, class Sched, bool ALIGN_EPI, int DT>
; __device__ __forceinline__ void gemm_phase(LAS unsigned char* lds, const int KB, const Sched& S, const Epi& E) {
;     ...
;         for (int t = 0; t < nt; t += 2) {
;             const bool last = (t == nt - 2);
;             const size_t k1 = (size_t)(t + 1) * kstep, k2 = last ? 0 : (size_t)(t + 2) * kstep, k3 = k2 + kstep;
;     ...
;             PG8_LDB(B0, 1, 0); PG8_LDB(B1, 1, 1); PG8_SCHED; PG8_LDA(At, 1, 0); PG8_STA(PG8_SA(0, 1), last, 1, k2);
;             PG8_WAIT_V(8); PG8_WAIT_L(0); PG8_BAR; PG8_MMA(0, 0, At, B0); PG8_MMA(0, 1, At, B1); PG8_BAR; PG8_SCHED;
;             PG8_LDA(At, 1, 1); PG8_STAGE(PG8_SB(1, 0), b3, voffB); PG8_STAGE(PG8_SB(1, 1), b3 + hstep, voffB); PG8_STA(PG8_SA(1, 0), last, 0, k3);
;             PG8_WAIT_V(8); PG8_WAIT_L(0); PG8_BAR; PG8_MMA(1, 0, At, B0); PG8_MMA(1, 1, At, B1); PG8_BAR; PG8_SCHED;
	s_add_i32 s44, 0, 0x18000
	s_add_i32 s45, 0, 0x1c000
	v_add_u32_e32 v14, s44, v191
	v_add_u32_e32 v30, s45, v191
	ds_read_b128 v[2:5], v14
	ds_read_b128 v[6:9], v14 offset:1024
	ds_read_b128 v[10:13], v14 offset:2048
	ds_read_b128 v[14:17], v14 offset:3072
	ds_read_b128 v[18:21], v30
	ds_read_b128 v[22:25], v30 offset:1024
	ds_read_b128 v[26:29], v30 offset:2048
	ds_read_b128 v[30:33], v30 offset:3072
	s_add_u32 s42, s42, 0x40000
	s_addc_u32 s43, s43, 0
	s_mov_b32 m0, s49
	v_lshl_add_u64 v[230:231], s[42:43], 0, v[166:167]
	ds_read_b128 v[198:201], v196 offset:32768
	ds_read_b128 v[202:205], v196 offset:33792
	ds_read_b128 v[206:209], v196 offset:34816
	ds_read_b128 v[210:213], v196 offset:35840
	ds_read_b128 v[214:217], v196 offset:36864
	ds_read_b128 v[218:221], v196 offset:37888
	ds_read_b128 v[222:225], v196 offset:38912
	ds_read_b128 v[226:229], v196 offset:39936
	global_load_lds_dwordx4 v[230:231], off
	v_lshl_add_u64 v[230:231], s[42:43], 0, v[168:169]
	s_mov_b32 m0, s52
	s_nop 0
	global_load_lds_dwordx4 v[230:231], off
	s_waitcnt vmcnt(8)
	s_waitcnt lgkmcnt(0)
	s_barrier
	s_setprio 1
	s_waitcnt lgkmcnt(0)
	v_mfma_scale_f32_16x16x128_f8f6f4 v[158:161], v[2:9], v[198:205], v[158:161], v1, v1 op_sel_hi:[0,0,0]
	v_mfma_scale_f32_16x16x128_f8f6f4 v[154:157], v[10:17], v[198:205], v[154:157], v1, v1 op_sel_hi:[0,0,0]
	v_mfma_scale_f32_16x16x128_f8f6f4 v[150:153], v[2:9], v[206:213], v[150:153], v1, v1 op_sel_hi:[0,0,0]
	v_mfma_scale_f32_16x16x128_f8f6f4 v[142:145], v[10:17], v[206:213], v[142:145], v1, v1 op_sel_hi:[0,0,0]
	v_mfma_scale_f32_16x16x128_f8f6f4 v[134:137], v[2:9], v[214:221], v[134:137], v1, v1 op_sel_hi:[0,0,0]
	v_mfma_scale_f32_16x16x128_f8f6f4 v[126:129], v[10:17], v[214:221], v[126:129], v1, v1 op_sel_hi:[0,0,0]
	v_mfma_scale_f32_16x16x128_f8f6f4 v[118:121], v[2:9], v[222:229], v[118:121], v1, v1 op_sel_hi:[0,0,0]
	v_mfma_scale_f32_16x16x128_f8f6f4 v[110:113], v[10:17], v[222:229], v[110:113], v1, v1 op_sel_hi:[0,0,0]
	s_setprio 0
	s_setprio 1
	v_mfma_scale_f32_16x16x128_f8f6f4 v[146:149], v[18:25], v[198:205], v[146:149], v1, v1 op_sel_hi:[0,0,0]
	v_mfma_scale_f32_16x16x128_f8f6f4 v[138:141], v[26:33], v[198:205], v[138:141], v1, v1 op_sel_hi:[0,0,0]
	v_mfma_scale_f32_16x16x128_f8f6f4 v[130:133], v[18:25], v[206:213], v[130:133], v1, v1 op_sel_hi:[0,0,0]
	v_mfma_scale_f32_16x16x128_f8f6f4 v[122:125], v[26:33], v[206:213], v[122:125], v1, v1 op_sel_hi:[0,0,0]
	v_mfma_scale_f32_16x16x128_f8f6f4 v[114:117], v[18:25], v[214:221], v[114:117], v1, v1 op_sel_hi:[0,0,0]
	v_mfma_scale_f32_16x16x128_f8f6f4 v[106:109], v[26:33], v[214:221], v[106:109], v1, v1 op_sel_hi:[0,0,0]
	v_mfma_scale_f32_16x16x128_f8f6f4 v[102:105], v[18:25], v[222:229], v[102:105], v1, v1 op_sel_hi:[0,0,0]
	v_mfma_scale_f32_16x16x128_f8f6f4 v[98:101], v[26:33], v[222:229], v[98:101], v1, v1 op_sel_hi:[0,0,0]
	s_setprio 0
	s_barrier
	s_add_i32 s42, s44, s46
	v_lshl_add_u64 v[182:183], v[182:183], 0, s[10:11]
	s_mov_b32 m0, s42
	ds_read_b128 v[198:201], v196 offset:49152
	ds_read_b128 v[202:205], v196 offset:50176
	ds_read_b128 v[206:209], v196 offset:51200
	ds_read_b128 v[210:213], v196 offset:52224
	ds_read_b128 v[214:217], v196 offset:53248
	ds_read_b128 v[218:221], v196 offset:54272
	ds_read_b128 v[222:225], v196 offset:55296
	ds_read_b128 v[226:229], v196 offset:56320
	global_load_lds_dwordx4 v[182:183], off
	s_add_i32 m0, s42, 0x2000
	s_add_u32 s40, s40, 0x40080
	v_lshl_add_u64 v[182:183], v[184:185], 0, s[10:11]
	s_addc_u32 s41, s41, 0
	s_add_i32 s42, s45, s46
	global_load_lds_dwordx4 v[182:183], off
	v_lshl_add_u64 v[182:183], s[40:41], 0, v[162:163]
	s_mov_b32 m0, s42
	s_nop 0
	global_load_lds_dwordx4 v[182:183], off
	v_lshl_add_u64 v[182:183], s[40:41], 0, v[164:165]
	s_add_i32 m0, s42, 0x2000
	s_nop 0
	global_load_lds_dwordx4 v[182:183], off
	v_lshl_add_u64 v[182:183], v[186:187], 0, s[10:11]
	s_mov_b32 m0, s54
	s_nop 0
	global_load_lds_dwordx4 v[182:183], off
	v_lshl_add_u64 v[182:183], v[188:189], 0, s[10:11]
	s_mov_b32 m0, s55
	s_nop 0
	global_load_lds_dwordx4 v[182:183], off
	s_waitcnt vmcnt(8)
	s_waitcnt lgkmcnt(0)
	s_barrier
	s_setprio 1
	s_waitcnt lgkmcnt(0)
	v_mfma_scale_f32_16x16x128_f8f6f4 v[94:97], v[2:9], v[198:205], v[94:97], v1, v1 op_sel_hi:[0,0,0]
	v_mfma_scale_f32_16x16x128_f8f6f4 v[90:93], v[10:17], v[198:205], v[90:93], v1, v1 op_sel_hi:[0,0,0]
	v_mfma_scale_f32_16x16x128_f8f6f4 v[86:89], v[2:9], v[206:213], v[86:89], v1, v1 op_sel_hi:[0,0,0]
	v_mfma_scale_f32_16x16x128_f8f6f4 v[78:81], v[10:17], v[206:213], v[78:81], v1, v1 op_sel_hi:[0,0,0]
	v_mfma_scale_f32_16x16x128_f8f6f4 v[62:65], v[2:9], v[214:221], v[62:65], v1, v1 op_sel_hi:[0,0,0]
	v_mfma_scale_f32_16x16x128_f8f6f4 v[54:57], v[10:17], v[214:221], v[54:57], v1, v1 op_sel_hi:[0,0,0]
	v_mfma_scale_f32_16x16x128_f8f6f4 v[46:49], v[2:9], v[222:229], v[46:49], v1, v1 op_sel_hi:[0,0,0]
	v_mfma_scale_f32_16x16x128_f8f6f4 v[38:41], v[10:17], v[222:229], v[38:41], v1, v1 op_sel_hi:[0,0,0]
	s_setprio 0
	s_setprio 1
	v_mfma_scale_f32_16x16x128_f8f6f4 v[82:85], v[18:25], v[198:205], v[82:85], v1, v1 op_sel_hi:[0,0,0]
	v_mfma_scale_f32_16x16x128_f8f6f4 v[74:77], v[26:33], v[198:205], v[74:77], v1, v1 op_sel_hi:[0,0,0]
	v_mfma_scale_f32_16x16x128_f8f6f4 v[58:61], v[18:25], v[206:213], v[58:61], v1, v1 op_sel_hi:[0,0,0]
	v_mfma_scale_f32_16x16x128_f8f6f4 v[50:53], v[26:33], v[206:213], v[50:53], v1, v1 op_sel_hi:[0,0,0]
	v_mfma_scale_f32_16x16x128_f8f6f4 v[42:45], v[18:25], v[214:221], v[42:45], v1, v1 op_sel_hi:[0,0,0]
	v_mfma_scale_f32_16x16x128_f8f6f4 v[34:37], v[26:33], v[214:221], v[34:37], v1, v1 op_sel_hi:[0,0,0]
	v_mfma_scale_f32_16x16x128_f8f6f4 v[70:73], v[18:25], v[222:229], v[70:73], v1, v1 op_sel_hi:[0,0,0]
	v_mfma_scale_f32_16x16x128_f8f6f4 v[66:69], v[26:33], v[222:229], v[66:69], v1, v1 op_sel_hi:[0,0,0]
	s_setprio 0
	s_add_i32 s70, s70, 2
	s_cmp_gt_u32 s70, 13
	s_mov_b64 s[42:43], s[38:39]
	s_barrier
	s_cbranch_scc0 .LBB0_2108
	s_and_b64 vcc, exec, s[12:13]
	s_cbranch_vccz .LBB0_2111
	s_barrier

; #define PG8_STAGE(bufoff, gbase, voff) do { _Pragma("unroll") for (int _i = 0; _i < 2; ++_i) \
;         __builtin_amdgcn_global_load_lds((const unsigned*)((const char*)(gbase) + (voff)[_i]), (LAS unsigned*)(lds + (bufoff) + ldsw + _i * 8192), 16, 0, 0); } while (0)
; #define PG8_LDA(dst, b, h) do { _Pragma("unroll") for (int m = 0; m < 4; ++m) dst[m] = PG8_LD32(lds + PG8_SA(b, h) + aoff + m * 2048); } while (0)
; #define PG8_LDB(dst, b, h) do { _Pragma("unroll") for (int n = 0; n < 2; ++n) dst[n] = PG8_LD32(lds + PG8_SB(b, h) + boff + n * 2048); } while (0)
; #define PG8_WAIT_V(n) asm volatile("s_waitcnt vmcnt(" #n ")" ::: "memory")
; #define PG8_WAIT_L(n) asm volatile("s_waitcnt lgkmcnt(" #n ")" ::: "memory")
; #define PG8_BAR __builtin_amdgcn_s_barrier()
; #define PG8_SCHED __builtin_amdgcn_sched_barrier(0)
; #define PG8_STA(bufoff, nextflag, h, koff) do { if constexpr (Sched::GATHER) { unsigned _o[2]; _o[0] = (nextflag) ? nxtA[h][0] : curA[h][0]; _o[1] = (nextflag) ? nxtA[h][1] : curA[h][1]; PG8_STAGE(bufoff, Ab + (koff), _o); } \
;         else { PG8_STAGE(bufoff, ((nextflag) ? nA : cA) + (size_t)(h) * hstep + (koff), voffA); } } while (0)
; template <class Epi, class Sched, bool ALIGN_EPI, int DT>
; __device__ __forceinline__ void gemm_phase(LAS unsigned char* lds, const int KB, const Sched& S, const Epi& E) {
;     ...
;             const size_t k1 = (size_t)(t + 1) * kstep, k2 = last ? 0 : (size_t)(t + 2) * kstep, k3 = k2 + kstep;
;             const char* b2 = last ? nB : cB + (size_t)(t + 2) * kstep; const char* b3 = b2 + kstep;
;             PG8_LDB(B0, 0, 0); PG8_LDB(B1, 0, 1); PG8_SCHED; PG8_LDA(At, 0, 0); PG8_STA(PG8_SA(1, 1), false, 1, k1);
;             PG8_WAIT_V(8); PG8_WAIT_L(0); PG8_BAR; PG8_MMA(0, 0, At, B0); PG8_MMA(0, 1, At, B1); PG8_BAR; PG8_SCHED;
;             PG8_LDA(At, 0, 1); PG8_STAGE(PG8_SB(0, 0), b2, voffB); PG8_STAGE(PG8_SB(0, 1), b2 + hstep, voffB); PG8_STA(PG8_SA(0, 0), last, 0, k2);
;             PG8_WAIT_V(8); PG8_WAIT_L(0); PG8_BAR; PG8_MMA(1, 0, At, B0); PG8_MMA(1, 1, At, B1); PG8_BAR; PG8_SCHED;
.LBB0_2294:
	v_add_u32_e32 v79, s65, v167
	ds_read_b128 v[142:145], v79
	ds_read_b128 v[156:159], v79 offset:1024
	ds_read_b128 v[178:181], v79 offset:2048
	ds_read_b128 v[182:185], v79 offset:3072
	v_add_u32_e32 v79, s66, v167
	ds_read_b128 v[186:189], v79
	ds_read_b128 v[190:193], v79 offset:1024
	ds_read_b128 v[196:199], v79 offset:2048
	ds_read_b128 v[200:203], v79 offset:3072
	s_add_u32 s40, s8, 0x100
	s_addc_u32 s41, s9, 0
	s_cmpk_eq_i32 s8, 0x700
	s_cselect_b64 vcc, -1, 0
	v_lshl_add_u64 v[160:161], v[88:89], 0, s[8:9]
	s_and_b64 s[76:77], vcc, exec
	v_cndmask_b32_e32 v161, v161, v155, vcc
	s_cselect_b32 s75, 0, s40
	v_cndmask_b32_e32 v160, v160, v154, vcc
	v_lshl_add_u64 v[236:237], v[140:141], 0, s[8:9]
	s_add_i32 m0, s42, 0xc000
	ds_read_b128 v[204:207], v169
	ds_read_b128 v[208:211], v169 offset:1024
	ds_read_b128 v[212:215], v169 offset:2048
	ds_read_b128 v[216:219], v169 offset:3072
	ds_read_b128 v[220:223], v169 offset:4096
	ds_read_b128 v[224:227], v169 offset:5120
	ds_read_b128 v[228:231], v169 offset:6144
	ds_read_b128 v[232:235], v169 offset:7168
	global_load_lds_dwordx4 v[236:237], off
	v_lshl_add_u64 v[236:237], v[138:139], 0, s[8:9]
	s_add_i32 m0, s42, 0xe000
	s_nop 0
	global_load_lds_dwordx4 v[236:237], off
	s_waitcnt vmcnt(8)
	s_waitcnt lgkmcnt(0)
	s_barrier
	s_setprio 1
	s_waitcnt lgkmcnt(0)
	v_mfma_i32_16x16x64_i8 v[134:137], v[142:145], v[204:207], v[134:137]
	v_mfma_i32_16x16x64_i8 v[126:129], v[178:181], v[204:207], v[126:129]
	v_mfma_i32_16x16x64_i8 v[118:121], v[142:145], v[212:215], v[118:121]
	v_mfma_i32_16x16x64_i8 v[110:113], v[178:181], v[212:215], v[110:113]
	v_mfma_i32_16x16x64_i8 v[102:105], v[142:145], v[220:223], v[102:105]
	v_mfma_i32_16x16x64_i8 v[94:97], v[178:181], v[220:223], v[94:97]
	v_mfma_i32_16x16x64_i8 v[82:85], v[142:145], v[228:231], v[82:85]
	v_mfma_i32_16x16x64_i8 v[70:73], v[178:181], v[228:231], v[70:73]
	v_mfma_i32_16x16x64_i8 v[134:137], v[156:159], v[208:211], v[134:137]
	v_mfma_i32_16x16x64_i8 v[126:129], v[182:185], v[208:211], v[126:129]
	v_mfma_i32_16x16x64_i8 v[118:121], v[156:159], v[216:219], v[118:121]
	v_mfma_i32_16x16x64_i8 v[110:113], v[182:185], v[216:219], v[110:113]
	v_mfma_i32_16x16x64_i8 v[102:105], v[156:159], v[224:227], v[102:105]
	v_mfma_i32_16x16x64_i8 v[94:97], v[182:185], v[224:227], v[94:97]
	v_mfma_i32_16x16x64_i8 v[82:85], v[156:159], v[232:235], v[82:85]
	v_mfma_i32_16x16x64_i8 v[70:73], v[182:185], v[232:235], v[70:73]
	s_setprio 0
	s_setprio 1
	v_mfma_i32_16x16x64_i8 v[130:133], v[186:189], v[204:207], v[130:133]
	v_mfma_i32_16x16x64_i8 v[122:125], v[196:199], v[204:207], v[122:125]
	v_mfma_i32_16x16x64_i8 v[114:117], v[186:189], v[212:215], v[114:117]
	v_mfma_i32_16x16x64_i8 v[106:109], v[196:199], v[212:215], v[106:109]
	v_mfma_i32_16x16x64_i8 v[98:101], v[186:189], v[220:223], v[98:101]
	v_mfma_i32_16x16x64_i8 v[90:93], v[196:199], v[220:223], v[90:93]
	v_mfma_i32_16x16x64_i8 v[74:77], v[186:189], v[228:231], v[74:77]
	v_mfma_i32_16x16x64_i8 v[66:69], v[196:199], v[228:231], v[66:69]
	v_mfma_i32_16x16x64_i8 v[130:133], v[190:193], v[208:211], v[130:133]
	v_mfma_i32_16x16x64_i8 v[122:125], v[200:203], v[208:211], v[122:125]
	v_mfma_i32_16x16x64_i8 v[114:117], v[190:193], v[216:219], v[114:117]
	v_mfma_i32_16x16x64_i8 v[106:109], v[200:203], v[216:219], v[106:109]
	v_mfma_i32_16x16x64_i8 v[98:101], v[190:193], v[224:227], v[98:101]
	v_mfma_i32_16x16x64_i8 v[90:93], v[200:203], v[224:227], v[90:93]
	v_mfma_i32_16x16x64_i8 v[74:77], v[190:193], v[232:235], v[74:77]
	v_mfma_i32_16x16x64_i8 v[66:69], v[200:203], v[232:235], v[66:69]
	s_setprio 0
	s_barrier
	s_add_i32 s8, s65, s33
	v_lshl_add_u64 v[236:237], v[160:161], 0, v[148:149]
	s_mov_b32 m0, s8
	ds_read_b128 v[204:207], v169 offset:16384
	ds_read_b128 v[208:211], v169 offset:17408
	ds_read_b128 v[212:215], v169 offset:18432
	ds_read_b128 v[216:219], v169 offset:19456
	ds_read_b128 v[220:223], v169 offset:20480
	ds_read_b128 v[224:227], v169 offset:21504
	ds_read_b128 v[228:231], v169 offset:22528
	ds_read_b128 v[232:235], v169 offset:23552
	global_load_lds_dwordx4 v[236:237], off
	v_lshl_add_u64 v[238:239], v[160:161], 0, v[150:151]
	s_add_i32 m0, s8, 0x2000
	v_lshl_add_u64 v[240:241], v[160:161], 0, s[10:11]
	s_add_i32 s8, s66, s33
	global_load_lds_dwordx4 v[238:239], off
	v_lshl_add_u64 v[242:243], v[240:241], 0, v[148:149]
	s_mov_b32 m0, s8
	v_lshl_add_u64 v[240:241], v[240:241], 0, v[150:151]
	global_load_lds_dwordx4 v[242:243], off
	s_add_i32 m0, s8, 0x2000
	s_add_u32 s8, s60, s75
	global_load_lds_dwordx4 v[240:241], off
	v_cndmask_b32_e32 v146, v81, v173, vcc
	s_addc_u32 s9, s61, 0
	s_mov_b32 m0, s42
	v_cndmask_b32_e32 v240, v80, v174, vcc
	global_load_lds_dwordx4 v146, s[8:9]
	s_mov_b32 m0, s43
	v_mov_b32_e32 v241, v147
	global_load_lds_dwordx4 v240, s[8:9]
	s_waitcnt vmcnt(8)
	s_waitcnt lgkmcnt(0)
	v_lshl_add_u64 v[242:243], s[8:9], 0, v[146:147]
	v_lshl_add_u64 v[240:241], s[8:9], 0, v[240:241]
	s_barrier
; #define PG8_LDA(dst, b, h) do { _Pragma("unroll") for (int m = 0; m < 4; ++m) dst[m] = PG8_LD32(lds + PG8_SA(b, h) + aoff + m * 2048); } while (0)
; #define PG8_LDB(dst, b, h) do { _Pragma("unroll") for (int n = 0; n < 2; ++n) dst[n] = PG8_LD32(lds + PG8_SB(b, h) + boff + n * 2048); } while (0)
; #define PG8_WAIT_V(n) asm volatile("s_waitcnt vmcnt(" #n ")" ::: "memory")
; #define PG8_WAIT_L(n) asm volatile("s_waitcnt lgkmcnt(" #n ")" ::: "memory")
; #define PG8_BAR __builtin_amdgcn_s_barrier()
; #define PG8_SCHED __builtin_amdgcn_sched_barrier(0)
; #define PG8_STA(bufoff, nextflag, h, koff) do { if constexpr (Sched::GATHER) { unsigned _o[2]; _o[0] = (nextflag) ? nxtA[h][0] : curA[h][0]; _o[1] = (nextflag) ? nxtA[h][1] : curA[h][1]; PG8_STAGE(bufoff, Ab + (koff), _o); } \
;         else { PG8_STAGE(bufoff, ((nextflag) ? nA : cA) + (size_t)(h) * hstep + (koff), voffA); } } while (0)
; template <class Epi, class Sched, bool ALIGN_EPI, int DT>
; __device__ __forceinline__ void gemm_phase(LAS unsigned char* lds, const int KB, const Sched& S, const Epi& E) {
;     ...
;             PG8_WAIT_V(8); PG8_WAIT_L(0); PG8_BAR; PG8_MMA(1, 0, At, B0); PG8_MMA(1, 1, At, B1); PG8_BAR; PG8_SCHED;
;             PG8_LDB(B0, 1, 0); PG8_LDB(B1, 1, 1); PG8_SCHED; PG8_LDA(At, 1, 0); PG8_STA(PG8_SA(0, 1), last, 1, k2);
;             PG8_WAIT_V(8); PG8_WAIT_L(0); PG8_BAR; PG8_MMA(0, 0, At, B0); PG8_MMA(0, 1, At, B1); PG8_BAR; PG8_SCHED;
	s_setprio 1
	s_waitcnt lgkmcnt(0)
	v_mfma_i32_16x16x64_i8 v[54:57], v[142:145], v[204:207], v[54:57]
	v_mfma_i32_16x16x64_i8 v[50:53], v[178:181], v[204:207], v[50:53]
	v_mfma_i32_16x16x64_i8 v[42:45], v[142:145], v[212:215], v[42:45]
	v_mfma_i32_16x16x64_i8 v[34:37], v[178:181], v[212:215], v[34:37]
	v_mfma_i32_16x16x64_i8 v[26:29], v[142:145], v[220:223], v[26:29]
	v_mfma_i32_16x16x64_i8 v[18:21], v[178:181], v[220:223], v[18:21]
	v_mfma_i32_16x16x64_i8 v[10:13], v[142:145], v[228:231], v[10:13]
	v_mfma_i32_16x16x64_i8 v[2:5], v[178:181], v[228:231], v[2:5]
	v_mfma_i32_16x16x64_i8 v[54:57], v[156:159], v[208:211], v[54:57]
	v_mfma_i32_16x16x64_i8 v[50:53], v[182:185], v[208:211], v[50:53]
	v_mfma_i32_16x16x64_i8 v[42:45], v[156:159], v[216:219], v[42:45]
	v_mfma_i32_16x16x64_i8 v[34:37], v[182:185], v[216:219], v[34:37]
	v_mfma_i32_16x16x64_i8 v[26:29], v[156:159], v[224:227], v[26:29]
	v_mfma_i32_16x16x64_i8 v[18:21], v[182:185], v[224:227], v[18:21]
	v_mfma_i32_16x16x64_i8 v[10:13], v[156:159], v[232:235], v[10:13]
	v_mfma_i32_16x16x64_i8 v[2:5], v[182:185], v[232:235], v[2:5]
	s_setprio 0
	s_setprio 1
	v_mfma_i32_16x16x64_i8 v[62:65], v[186:189], v[204:207], v[62:65]
	v_mfma_i32_16x16x64_i8 v[58:61], v[196:199], v[204:207], v[58:61]
	v_mfma_i32_16x16x64_i8 v[46:49], v[186:189], v[212:215], v[46:49]
	v_mfma_i32_16x16x64_i8 v[38:41], v[196:199], v[212:215], v[38:41]
	v_mfma_i32_16x16x64_i8 v[30:33], v[186:189], v[220:223], v[30:33]
	v_mfma_i32_16x16x64_i8 v[22:25], v[196:199], v[220:223], v[22:25]
	v_mfma_i32_16x16x64_i8 v[14:17], v[186:189], v[228:231], v[14:17]
	v_mfma_i32_16x16x64_i8 v[6:9], v[196:199], v[228:231], v[6:9]
	v_mfma_i32_16x16x64_i8 v[62:65], v[190:193], v[208:211], v[62:65]
	v_mfma_i32_16x16x64_i8 v[58:61], v[200:203], v[208:211], v[58:61]
	v_mfma_i32_16x16x64_i8 v[46:49], v[190:193], v[216:219], v[46:49]
	v_mfma_i32_16x16x64_i8 v[38:41], v[200:203], v[216:219], v[38:41]
	v_mfma_i32_16x16x64_i8 v[30:33], v[190:193], v[224:227], v[30:33]
	v_mfma_i32_16x16x64_i8 v[22:25], v[200:203], v[224:227], v[22:25]
	v_mfma_i32_16x16x64_i8 v[14:17], v[190:193], v[232:235], v[14:17]
	v_mfma_i32_16x16x64_i8 v[6:9], v[200:203], v[232:235], v[6:9]
	s_setprio 0
	s_barrier
	s_add_i32 s75, 0, 0x18000
	v_add_u32_e32 v79, s75, v167
	s_add_i32 s76, 0, 0x1c000
	ds_read_b128 v[142:145], v79
	ds_read_b128 v[156:159], v79 offset:1024
	ds_read_b128 v[178:181], v79 offset:2048
	ds_read_b128 v[182:185], v79 offset:3072
	v_add_u32_e32 v79, s76, v167
	ds_read_b128 v[186:189], v79
	ds_read_b128 v[190:193], v79 offset:1024
	ds_read_b128 v[196:199], v79 offset:2048
	ds_read_b128 v[200:203], v79 offset:3072
	s_mov_b32 m0, s44
	v_cndmask_b32_e32 v79, v78, v175, vcc
	ds_read_b128 v[204:207], v169 offset:32768
	ds_read_b128 v[208:211], v169 offset:33792
	ds_read_b128 v[212:215], v169 offset:34816
	ds_read_b128 v[216:219], v169 offset:35840
	ds_read_b128 v[220:223], v169 offset:36864
	ds_read_b128 v[224:227], v169 offset:37888
	ds_read_b128 v[228:231], v169 offset:38912
	ds_read_b128 v[232:235], v169 offset:39936
	v_cndmask_b32_e32 v87, v86, v176, vcc
	global_load_lds_dwordx4 v79, s[8:9]
	s_mov_b32 m0, s45
	s_nop 0
	global_load_lds_dwordx4 v87, s[8:9]
	s_waitcnt vmcnt(8)
	s_waitcnt lgkmcnt(0)
	s_barrier
	s_setprio 1
	s_waitcnt lgkmcnt(0)
	v_mfma_i32_16x16x64_i8 v[134:137], v[142:145], v[204:207], v[134:137]
	v_mfma_i32_16x16x64_i8 v[126:129], v[178:181], v[204:207], v[126:129]
	v_mfma_i32_16x16x64_i8 v[118:121], v[142:145], v[212:215], v[118:121]
	v_mfma_i32_16x16x64_i8 v[110:113], v[178:181], v[212:215], v[110:113]
	v_mfma_i32_16x16x64_i8 v[102:105], v[142:145], v[220:223], v[102:105]
	v_mfma_i32_16x16x64_i8 v[94:97], v[178:181], v[220:223], v[94:97]
	v_mfma_i32_16x16x64_i8 v[82:85], v[142:145], v[228:231], v[82:85]
	v_mfma_i32_16x16x64_i8 v[70:73], v[178:181], v[228:231], v[70:73]
	v_mfma_i32_16x16x64_i8 v[134:137], v[156:159], v[208:211], v[134:137]
	v_mfma_i32_16x16x64_i8 v[126:129], v[182:185], v[208:211], v[126:129]
	v_mfma_i32_16x16x64_i8 v[118:121], v[156:159], v[216:219], v[118:121]
	v_mfma_i32_16x16x64_i8 v[110:113], v[182:185], v[216:219], v[110:113]
	v_mfma_i32_16x16x64_i8 v[102:105], v[156:159], v[224:227], v[102:105]
	v_mfma_i32_16x16x64_i8 v[94:97], v[182:185], v[224:227], v[94:97]
	v_mfma_i32_16x16x64_i8 v[82:85], v[156:159], v[232:235], v[82:85]
	v_mfma_i32_16x16x64_i8 v[70:73], v[182:185], v[232:235], v[70:73]
	s_setprio 0
	s_setprio 1
	v_mfma_i32_16x16x64_i8 v[130:133], v[186:189], v[204:207], v[130:133]
	v_mfma_i32_16x16x64_i8 v[122:125], v[196:199], v[204:207], v[122:125]
	v_mfma_i32_16x16x64_i8 v[114:117], v[186:189], v[212:215], v[114:117]
	v_mfma_i32_16x16x64_i8 v[106:109], v[196:199], v[212:215], v[106:109]
	v_mfma_i32_16x16x64_i8 v[98:101], v[186:189], v[220:223], v[98:101]
	v_mfma_i32_16x16x64_i8 v[90:93], v[196:199], v[220:223], v[90:93]
	v_mfma_i32_16x16x64_i8 v[74:77], v[186:189], v[228:231], v[74:77]
	v_mfma_i32_16x16x64_i8 v[66:69], v[196:199], v[228:231], v[66:69]
	v_mfma_i32_16x16x64_i8 v[130:133], v[190:193], v[208:211], v[130:133]
	v_mfma_i32_16x16x64_i8 v[122:125], v[200:203], v[208:211], v[122:125]
	v_mfma_i32_16x16x64_i8 v[114:117], v[190:193], v[216:219], v[114:117]
	v_mfma_i32_16x16x64_i8 v[106:109], v[200:203], v[216:219], v[106:109]
	v_mfma_i32_16x16x64_i8 v[98:101], v[190:193], v[224:227], v[98:101]
	v_mfma_i32_16x16x64_i8 v[90:93], v[200:203], v[224:227], v[90:93]
	v_mfma_i32_16x16x64_i8 v[74:77], v[190:193], v[232:235], v[74:77]
	v_mfma_i32_16x16x64_i8 v[66:69], v[200:203], v[232:235], v[66:69]
	s_setprio 0
	s_barrier
; #define PG8_STAGE(bufoff, gbase, voff) do { _Pragma("unroll") for (int _i = 0; _i < 2; ++_i) \
;         __builtin_amdgcn_global_load_lds((const unsigned*)((const char*)(gbase) + (voff)[_i]), (LAS unsigned*)(lds + (bufoff) + ldsw + _i * 8192), 16, 0, 0); } while (0)
; #define PG8_LDA(dst, b, h) do { _Pragma("unroll") for (int m = 0; m < 4; ++m) dst[m] = PG8_LD32(lds + PG8_SA(b, h) + aoff + m * 2048); } while (0)
; #define PG8_WAIT_V(n) asm volatile("s_waitcnt vmcnt(" #n ")" ::: "memory")
; #define PG8_WAIT_L(n) asm volatile("s_waitcnt lgkmcnt(" #n ")" ::: "memory")
; #define PG8_BAR __builtin_amdgcn_s_barrier()
; #define PG8_SCHED __builtin_amdgcn_sched_barrier(0)
; #define PG8_STA(bufoff, nextflag, h, koff) do { if constexpr (Sched::GATHER) { unsigned _o[2]; _o[0] = (nextflag) ? nxtA[h][0] : curA[h][0]; _o[1] = (nextflag) ? nxtA[h][1] : curA[h][1]; PG8_STAGE(bufoff, Ab + (koff), _o); } \
;         else { PG8_STAGE(bufoff, ((nextflag) ? nA : cA) + (size_t)(h) * hstep + (koff), voffA); } } while (0)
; template <class Epi, class Sched, bool ALIGN_EPI, int DT>
; __device__ __forceinline__ void gemm_phase(LAS unsigned char* lds, const int KB, const Sched& S, const Epi& E) {
;     ...
;         for (int t = 0; t < nt; t += 2) {
;             const bool last = (t == nt - 2);
;             const size_t k1 = (size_t)(t + 1) * kstep, k2 = last ? 0 : (size_t)(t + 2) * kstep, k3 = k2 + kstep;
;     ...
;             PG8_LDA(At, 1, 1); PG8_STAGE(PG8_SB(1, 0), b3, voffB); PG8_STAGE(PG8_SB(1, 1), b3 + hstep, voffB); PG8_STA(PG8_SA(1, 0), last, 0, k3);
;             PG8_WAIT_V(8); PG8_WAIT_L(0); PG8_BAR; PG8_MMA(1, 0, At, B0); PG8_MMA(1, 1, At, B1); PG8_BAR; PG8_SCHED;
	s_add_i32 s8, s75, s33
	v_lshl_add_u64 v[236:237], v[236:237], 0, s[20:21]
	s_mov_b32 m0, s8
	ds_read_b128 v[204:207], v169 offset:49152
	ds_read_b128 v[208:211], v169 offset:50176
	ds_read_b128 v[212:215], v169 offset:51200
	ds_read_b128 v[216:219], v169 offset:52224
	ds_read_b128 v[220:223], v169 offset:53248
	ds_read_b128 v[224:227], v169 offset:54272
	ds_read_b128 v[228:231], v169 offset:55296
	ds_read_b128 v[232:235], v169 offset:56320
	global_load_lds_dwordx4 v[236:237], off
	v_lshl_add_u64 v[236:237], v[238:239], 0, s[20:21]
	s_add_i32 m0, s8, 0x2000
	v_lshl_add_u64 v[160:161], v[160:161], 0, s[24:25]
	s_add_i32 s8, s76, s33
	global_load_lds_dwordx4 v[236:237], off
	v_lshl_add_u64 v[236:237], v[160:161], 0, v[148:149]
	s_mov_b32 m0, s8
	v_lshl_add_u64 v[160:161], v[160:161], 0, v[150:151]
	global_load_lds_dwordx4 v[236:237], off
	s_add_i32 m0, s8, 0x2000
	s_nop 0
	global_load_lds_dwordx4 v[160:161], off
	v_lshl_add_u64 v[160:161], v[242:243], 0, s[20:21]
	s_mov_b32 m0, s46
	s_nop 0
	global_load_lds_dwordx4 v[160:161], off
	v_lshl_add_u64 v[160:161], v[240:241], 0, s[20:21]
	s_mov_b32 m0, s47
	s_nop 0
	global_load_lds_dwordx4 v[160:161], off
	s_waitcnt vmcnt(8)
	s_waitcnt lgkmcnt(0)
	s_barrier
	s_setprio 1
	s_waitcnt lgkmcnt(0)
	v_mfma_i32_16x16x64_i8 v[54:57], v[142:145], v[204:207], v[54:57]
	v_mfma_i32_16x16x64_i8 v[50:53], v[178:181], v[204:207], v[50:53]
	v_mfma_i32_16x16x64_i8 v[42:45], v[142:145], v[212:215], v[42:45]
	v_mfma_i32_16x16x64_i8 v[34:37], v[178:181], v[212:215], v[34:37]
	v_mfma_i32_16x16x64_i8 v[26:29], v[142:145], v[220:223], v[26:29]
	v_mfma_i32_16x16x64_i8 v[18:21], v[178:181], v[220:223], v[18:21]
	v_mfma_i32_16x16x64_i8 v[10:13], v[142:145], v[228:231], v[10:13]
	v_mfma_i32_16x16x64_i8 v[2:5], v[178:181], v[228:231], v[2:5]
	v_mfma_i32_16x16x64_i8 v[54:57], v[156:159], v[208:211], v[54:57]
	v_mfma_i32_16x16x64_i8 v[50:53], v[182:185], v[208:211], v[50:53]
	v_mfma_i32_16x16x64_i8 v[42:45], v[156:159], v[216:219], v[42:45]
	v_mfma_i32_16x16x64_i8 v[34:37], v[182:185], v[216:219], v[34:37]
	v_mfma_i32_16x16x64_i8 v[26:29], v[156:159], v[224:227], v[26:29]
	v_mfma_i32_16x16x64_i8 v[18:21], v[182:185], v[224:227], v[18:21]
	v_mfma_i32_16x16x64_i8 v[10:13], v[156:159], v[232:235], v[10:13]
	v_mfma_i32_16x16x64_i8 v[2:5], v[182:185], v[232:235], v[2:5]
	s_setprio 0
	s_setprio 1
	v_mfma_i32_16x16x64_i8 v[62:65], v[186:189], v[204:207], v[62:65]
	v_mfma_i32_16x16x64_i8 v[58:61], v[196:199], v[204:207], v[58:61]
	v_mfma_i32_16x16x64_i8 v[46:49], v[186:189], v[212:215], v[46:49]
	v_mfma_i32_16x16x64_i8 v[38:41], v[196:199], v[212:215], v[38:41]
	v_mfma_i32_16x16x64_i8 v[30:33], v[186:189], v[220:223], v[30:33]
	v_mfma_i32_16x16x64_i8 v[22:25], v[196:199], v[220:223], v[22:25]
	v_mfma_i32_16x16x64_i8 v[14:17], v[186:189], v[228:231], v[14:17]
	v_mfma_i32_16x16x64_i8 v[6:9], v[196:199], v[228:231], v[6:9]
	v_mfma_i32_16x16x64_i8 v[62:65], v[190:193], v[208:211], v[62:65]
	v_mfma_i32_16x16x64_i8 v[58:61], v[200:203], v[208:211], v[58:61]
	v_mfma_i32_16x16x64_i8 v[46:49], v[190:193], v[216:219], v[46:49]
	v_mfma_i32_16x16x64_i8 v[38:41], v[200:203], v[216:219], v[38:41]
	v_mfma_i32_16x16x64_i8 v[30:33], v[190:193], v[224:227], v[30:33]
	v_mfma_i32_16x16x64_i8 v[22:25], v[200:203], v[224:227], v[22:25]
	v_mfma_i32_16x16x64_i8 v[14:17], v[190:193], v[232:235], v[14:17]
	v_mfma_i32_16x16x64_i8 v[6:9], v[200:203], v[232:235], v[6:9]
	s_setprio 0
	s_add_i32 s37, s37, 2
	s_cmp_gt_u32 s37, 13
	s_mov_b64 s[8:9], s[40:41]
	s_barrier
	s_cbranch_scc0 .LBB0_2294
	s_and_b64 vcc, exec, s[26:27]
	s_cbranch_vccz .LBB0_2297
	s_barrier

; #define PG8_STAGE(bufoff, gbase, voff) do { _Pragma("unroll") for (int _i = 0; _i < 2; ++_i) \
;         __builtin_amdgcn_global_load_lds((const unsigned*)((const char*)(gbase) + (voff)[_i]), (LAS unsigned*)(lds + (bufoff) + ldsw + _i * 8192), 16, 0, 0); } while (0)
; #define PG8_LDA(dst, b, h) do { _Pragma("unroll") for (int m = 0; m < 4; ++m) dst[m] = PG8_LD32(lds + PG8_SA(b, h) + aoff + m * 2048); } while (0)
; #define PG8_LDB(dst, b, h) do { _Pragma("unroll") for (int n = 0; n < 2; ++n) dst[n] = PG8_LD32(lds + PG8_SB(b, h) + boff + n * 2048); } while (0)
; #define PG8_WAIT_V(n) asm volatile("s_waitcnt vmcnt(" #n ")" ::: "memory")
; #define PG8_WAIT_L(n) asm volatile("s_waitcnt lgkmcnt(" #n ")" ::: "memory")
; #define PG8_BAR __builtin_amdgcn_s_barrier()
; #define PG8_SCHED __builtin_amdgcn_sched_barrier(0)
; #define PG8_STA(bufoff, nextflag, h, koff) do { if constexpr (Sched::GATHER) { unsigned _o[2]; _o[0] = (nextflag) ? nxtA[h][0] : curA[h][0]; _o[1] = (nextflag) ? nxtA[h][1] : curA[h][1]; PG8_STAGE(bufoff, Ab + (koff), _o); } \
;         else { PG8_STAGE(bufoff, ((nextflag) ? nA : cA) + (size_t)(h) * hstep + (koff), voffA); } } while (0)
; template <class Epi, class Sched, bool ALIGN_EPI, int DT>
; __device__ __forceinline__ void gemm_phase(LAS unsigned char* lds, const int KB, const Sched& S, const Epi& E) {
;     ...
;             const size_t k1 = (size_t)(t + 1) * kstep, k2 = last ? 0 : (size_t)(t + 2) * kstep, k3 = k2 + kstep;
;             const char* b2 = last ? nB : cB + (size_t)(t + 2) * kstep; const char* b3 = b2 + kstep;
;             PG8_LDB(B0, 0, 0); PG8_LDB(B1, 0, 1); PG8_SCHED; PG8_LDA(At, 0, 0); PG8_STA(PG8_SA(1, 1), false, 1, k1);
;             PG8_WAIT_V(8); PG8_WAIT_L(0); PG8_BAR; PG8_MMA(0, 0, At, B0); PG8_MMA(0, 1, At, B1); PG8_BAR; PG8_SCHED;
;             PG8_LDA(At, 0, 1); PG8_STAGE(PG8_SB(0, 0), b2, voffB); PG8_STAGE(PG8_SB(0, 1), b2 + hstep, voffB); PG8_STA(PG8_SA(0, 0), last, 0, k2);
;             PG8_WAIT_V(8); PG8_WAIT_L(0); PG8_BAR; PG8_MMA(1, 0, At, B0); PG8_MMA(1, 1, At, B1); PG8_BAR; PG8_SCHED;
.LBB0_2387:
	ds_read_b128 v[18:21], v198
	ds_read_b128 v[22:25], v198 offset:1024
	ds_read_b128 v[26:29], v198 offset:2048
	ds_read_b128 v[30:33], v198 offset:3072
	ds_read_b128 v[2:5], v199
	ds_read_b128 v[6:9], v199 offset:1024
	ds_read_b128 v[10:13], v199 offset:2048
	ds_read_b128 v[14:17], v199 offset:3072
	s_add_u32 s42, s44, 0x100
	s_addc_u32 s43, s45, 0
	s_add_i32 s76, s63, s4
	s_add_i32 m0, s33, 0xc000
	s_add_i32 s77, s33, 0xe000
	s_add_i32 s74, s76, 0x2000
	s_cmp_eq_u32 s71, 18
	v_lshl_add_u64 v[184:185], v[178:179], 0, s[44:45]
	s_cselect_b64 vcc, -1, 0
	s_cselect_b32 s75, 0, s42
	v_cndmask_b32_e32 v185, v185, v177, vcc
	v_cndmask_b32_e32 v184, v184, v176, vcc
	v_lshl_add_u64 v[226:227], v[180:181], 0, s[44:45]
	ds_read_b128 v[186:189], v200
	ds_read_b128 v[190:193], v200 offset:1024
	ds_read_b128 v[202:205], v200 offset:2048
	ds_read_b128 v[206:209], v200 offset:3072
	ds_read_b128 v[210:213], v200 offset:4096
	ds_read_b128 v[214:217], v200 offset:5120
	ds_read_b128 v[218:221], v200 offset:6144
	ds_read_b128 v[222:225], v200 offset:7168
	global_load_lds_dwordx4 v[226:227], off
	v_lshl_add_u64 v[226:227], v[182:183], 0, s[44:45]
	s_mov_b32 m0, s77
	s_nop 0
	global_load_lds_dwordx4 v[226:227], off
	s_waitcnt vmcnt(8)
	s_waitcnt lgkmcnt(0)
	s_barrier
	s_setprio 1
	s_waitcnt lgkmcnt(0)
	v_mfma_scale_f32_16x16x128_f8f6f4 v[158:161], v[18:25], v[186:193], v[158:161], v1, v1 op_sel_hi:[0,0,0]
	v_mfma_scale_f32_16x16x128_f8f6f4 v[154:157], v[26:33], v[186:193], v[154:157], v1, v1 op_sel_hi:[0,0,0]
	v_mfma_scale_f32_16x16x128_f8f6f4 v[150:153], v[18:25], v[202:209], v[150:153], v1, v1 op_sel_hi:[0,0,0]
	v_mfma_scale_f32_16x16x128_f8f6f4 v[142:145], v[26:33], v[202:209], v[142:145], v1, v1 op_sel_hi:[0,0,0]
	v_mfma_scale_f32_16x16x128_f8f6f4 v[134:137], v[18:25], v[210:217], v[134:137], v1, v1 op_sel_hi:[0,0,0]
	v_mfma_scale_f32_16x16x128_f8f6f4 v[126:129], v[26:33], v[210:217], v[126:129], v1, v1 op_sel_hi:[0,0,0]
	v_mfma_scale_f32_16x16x128_f8f6f4 v[118:121], v[18:25], v[218:225], v[118:121], v1, v1 op_sel_hi:[0,0,0]
	v_mfma_scale_f32_16x16x128_f8f6f4 v[110:113], v[26:33], v[218:225], v[110:113], v1, v1 op_sel_hi:[0,0,0]
	s_setprio 0
	s_setprio 1
	v_mfma_scale_f32_16x16x128_f8f6f4 v[146:149], v[2:9], v[186:193], v[146:149], v1, v1 op_sel_hi:[0,0,0]
	v_mfma_scale_f32_16x16x128_f8f6f4 v[138:141], v[10:17], v[186:193], v[138:141], v1, v1 op_sel_hi:[0,0,0]
	v_mfma_scale_f32_16x16x128_f8f6f4 v[130:133], v[2:9], v[202:209], v[130:133], v1, v1 op_sel_hi:[0,0,0]
	v_mfma_scale_f32_16x16x128_f8f6f4 v[122:125], v[10:17], v[202:209], v[122:125], v1, v1 op_sel_hi:[0,0,0]
	v_mfma_scale_f32_16x16x128_f8f6f4 v[114:117], v[2:9], v[210:217], v[114:117], v1, v1 op_sel_hi:[0,0,0]
	v_mfma_scale_f32_16x16x128_f8f6f4 v[106:109], v[10:17], v[210:217], v[106:109], v1, v1 op_sel_hi:[0,0,0]
	v_mfma_scale_f32_16x16x128_f8f6f4 v[102:105], v[2:9], v[218:225], v[102:105], v1, v1 op_sel_hi:[0,0,0]
	v_mfma_scale_f32_16x16x128_f8f6f4 v[98:101], v[10:17], v[218:225], v[98:101], v1, v1 op_sel_hi:[0,0,0]
	s_setprio 0
	s_barrier
	s_mov_b32 m0, s76
	v_lshl_add_u64 v[188:189], v[184:185], 0, v[170:171]
	ds_read_b128 v[202:205], v200 offset:16384
	ds_read_b128 v[206:209], v200 offset:17408
	ds_read_b128 v[210:213], v200 offset:18432
	ds_read_b128 v[214:217], v200 offset:19456
	ds_read_b128 v[218:221], v200 offset:20480
	ds_read_b128 v[222:225], v200 offset:21504
	ds_read_b128 v[226:229], v200 offset:22528
	ds_read_b128 v[230:233], v200 offset:23552
	global_load_lds_dwordx4 v[188:189], off
	v_lshl_add_u64 v[186:187], v[184:185], 0, v[164:165]
	s_mov_b32 m0, s74
	s_cselect_b32 s45, s9, s41
	s_cselect_b32 s44, s8, s40
	v_lshl_add_u64 v[190:191], v[184:185], 0, s[12:13]
	s_add_i32 s74, s64, s4
	global_load_lds_dwordx4 v[186:187], off
	v_lshl_add_u64 v[192:193], v[190:191], 0, v[170:171]
	s_mov_b32 m0, s74
	v_lshl_add_u64 v[190:191], v[190:191], 0, v[164:165]
	global_load_lds_dwordx4 v[192:193], off
	s_add_i32 m0, s74, 0x2000
	s_add_u32 s44, s44, s75
	s_addc_u32 s45, s45, 0
	global_load_lds_dwordx4 v[190:191], off
	v_lshl_add_u64 v[190:191], s[44:45], 0, v[166:167]
	s_mov_b32 m0, s33
	v_lshl_add_u64 v[192:193], s[44:45], 0, v[168:169]
	global_load_lds_dwordx4 v[190:191], off
	s_mov_b32 m0, s39
	s_nop 0
	global_load_lds_dwordx4 v[192:193], off
	s_waitcnt vmcnt(8)
	s_waitcnt lgkmcnt(0)
	s_barrier
	s_setprio 1
	s_waitcnt lgkmcnt(0)
	v_mfma_scale_f32_16x16x128_f8f6f4 v[94:97], v[18:25], v[202:209], v[94:97], v1, v1 op_sel_hi:[0,0,0]
	v_mfma_scale_f32_16x16x128_f8f6f4 v[90:93], v[26:33], v[202:209], v[90:93], v1, v1 op_sel_hi:[0,0,0]
	v_mfma_scale_f32_16x16x128_f8f6f4 v[86:89], v[18:25], v[210:217], v[86:89], v1, v1 op_sel_hi:[0,0,0]
	v_mfma_scale_f32_16x16x128_f8f6f4 v[78:81], v[26:33], v[210:217], v[78:81], v1, v1 op_sel_hi:[0,0,0]
	v_mfma_scale_f32_16x16x128_f8f6f4 v[62:65], v[18:25], v[218:225], v[62:65], v1, v1 op_sel_hi:[0,0,0]
	v_mfma_scale_f32_16x16x128_f8f6f4 v[54:57], v[26:33], v[218:225], v[54:57], v1, v1 op_sel_hi:[0,0,0]
	v_mfma_scale_f32_16x16x128_f8f6f4 v[46:49], v[18:25], v[226:233], v[46:49], v1, v1 op_sel_hi:[0,0,0]
	v_mfma_scale_f32_16x16x128_f8f6f4 v[38:41], v[26:33], v[226:233], v[38:41], v1, v1 op_sel_hi:[0,0,0]
	s_setprio 0
	s_setprio 1
	v_mfma_scale_f32_16x16x128_f8f6f4 v[82:85], v[2:9], v[202:209], v[82:85], v1, v1 op_sel_hi:[0,0,0]
	v_mfma_scale_f32_16x16x128_f8f6f4 v[74:77], v[10:17], v[202:209], v[74:77], v1, v1 op_sel_hi:[0,0,0]
	v_mfma_scale_f32_16x16x128_f8f6f4 v[58:61], v[2:9], v[210:217], v[58:61], v1, v1 op_sel_hi:[0,0,0]
	v_mfma_scale_f32_16x16x128_f8f6f4 v[50:53], v[10:17], v[210:217], v[50:53], v1, v1 op_sel_hi:[0,0,0]
	v_mfma_scale_f32_16x16x128_f8f6f4 v[42:45], v[2:9], v[218:225], v[42:45], v1, v1 op_sel_hi:[0,0,0]
	v_mfma_scale_f32_16x16x128_f8f6f4 v[34:37], v[10:17], v[218:225], v[34:37], v1, v1 op_sel_hi:[0,0,0]
	v_mfma_scale_f32_16x16x128_f8f6f4 v[70:73], v[2:9], v[226:233], v[70:73], v1, v1 op_sel_hi:[0,0,0]
	v_mfma_scale_f32_16x16x128_f8f6f4 v[66:69], v[10:17], v[226:233], v[66:69], v1, v1 op_sel_hi:[0,0,0]
	s_setprio 0
	s_barrier
; #define PG8_STAGE(bufoff, gbase, voff) do { _Pragma("unroll") for (int _i = 0; _i < 2; ++_i) \
;         __builtin_amdgcn_global_load_lds((const unsigned*)((const char*)(gbase) + (voff)[_i]), (LAS unsigned*)(lds + (bufoff) + ldsw + _i * 8192), 16, 0, 0); } while (0)
; #define PG8_LDA(dst, b, h) do { _Pragma("unroll") for (int m = 0; m < 4; ++m) dst[m] = PG8_LD32(lds + PG8_SA(b, h) + aoff + m * 2048); } while (0)
; #define PG8_LDB(dst, b, h) do { _Pragma("unroll") for (int n = 0; n < 2; ++n) dst[n] = PG8_LD32(lds + PG8_SB(b, h) + boff + n * 2048); } while (0)
; #define PG8_WAIT_V(n) asm volatile("s_waitcnt vmcnt(" #n ")" ::: "memory")
; #define PG8_WAIT_L(n) asm volatile("s_waitcnt lgkmcnt(" #n ")" ::: "memory")
; #define PG8_BAR __builtin_amdgcn_s_barrier()
; #define PG8_SCHED __builtin_amdgcn_sched_barrier(0)
; #define PG8_STA(bufoff, nextflag, h, koff) do { if constexpr (Sched::GATHER) { unsigned _o[2]; _o[0] = (nextflag) ? nxtA[h][0] : curA[h][0]; _o[1] = (nextflag) ? nxtA[h][1] : curA[h][1]; PG8_STAGE(bufoff, Ab + (koff), _o); } \
;         else { PG8_STAGE(bufoff, ((nextflag) ? nA : cA) + (size_t)(h) * hstep + (koff), voffA); } } while (0)
; template <class Epi, class Sched, bool ALIGN_EPI, int DT>
; __device__ __forceinline__ void gemm_phase(LAS unsigned char* lds, const int KB, const Sched& S, const Epi& E) {
;     ...
;         for (int t = 0; t < nt; t += 2) {
;             const bool last = (t == nt - 2);
;             const size_t k1 = (size_t)(t + 1) * kstep, k2 = last ? 0 : (size_t)(t + 2) * kstep, k3 = k2 + kstep;
;     ...
;             PG8_LDB(B0, 1, 0); PG8_LDB(B1, 1, 1); PG8_SCHED; PG8_LDA(At, 1, 0); PG8_STA(PG8_SA(0, 1), last, 1, k2);
;             PG8_WAIT_V(8); PG8_WAIT_L(0); PG8_BAR; PG8_MMA(0, 0, At, B0); PG8_MMA(0, 1, At, B1); PG8_BAR; PG8_SCHED;
;             PG8_LDA(At, 1, 1); PG8_STAGE(PG8_SB(1, 0), b3, voffB); PG8_STAGE(PG8_SB(1, 1), b3 + hstep, voffB); PG8_STA(PG8_SA(1, 0), last, 0, k3);
;             PG8_WAIT_V(8); PG8_WAIT_L(0); PG8_BAR; PG8_MMA(1, 0, At, B0); PG8_MMA(1, 1, At, B1); PG8_BAR; PG8_SCHED;
	s_add_i32 s74, 0, 0x18000
	s_add_i32 s75, 0, 0x1c000
	v_add_u32_e32 v14, s74, v196
	v_add_u32_e32 v30, s75, v196
	ds_read_b128 v[2:5], v14
	ds_read_b128 v[6:9], v14 offset:1024
	ds_read_b128 v[10:13], v14 offset:2048
	ds_read_b128 v[14:17], v14 offset:3072
	ds_read_b128 v[18:21], v30
	ds_read_b128 v[22:25], v30 offset:1024
	ds_read_b128 v[26:29], v30 offset:2048
	ds_read_b128 v[30:33], v30 offset:3072
	s_add_u32 s44, s44, 0x58000
	s_addc_u32 s45, s45, 0
	s_mov_b32 m0, s46
	v_lshl_add_u64 v[234:235], s[44:45], 0, v[166:167]
	ds_read_b128 v[202:205], v200 offset:32768
	ds_read_b128 v[206:209], v200 offset:33792
	ds_read_b128 v[210:213], v200 offset:34816
	ds_read_b128 v[214:217], v200 offset:35840
	ds_read_b128 v[218:221], v200 offset:36864
	ds_read_b128 v[222:225], v200 offset:37888
	ds_read_b128 v[226:229], v200 offset:38912
	ds_read_b128 v[230:233], v200 offset:39936
	global_load_lds_dwordx4 v[234:235], off
	v_lshl_add_u64 v[234:235], s[44:45], 0, v[168:169]
	s_mov_b32 m0, s47
	s_nop 0
	global_load_lds_dwordx4 v[234:235], off
	s_waitcnt vmcnt(8)
	s_waitcnt lgkmcnt(0)
	s_barrier
	s_setprio 1
	s_waitcnt lgkmcnt(0)
	v_mfma_scale_f32_16x16x128_f8f6f4 v[158:161], v[2:9], v[202:209], v[158:161], v1, v1 op_sel_hi:[0,0,0]
	v_mfma_scale_f32_16x16x128_f8f6f4 v[154:157], v[10:17], v[202:209], v[154:157], v1, v1 op_sel_hi:[0,0,0]
	v_mfma_scale_f32_16x16x128_f8f6f4 v[150:153], v[2:9], v[210:217], v[150:153], v1, v1 op_sel_hi:[0,0,0]
	v_mfma_scale_f32_16x16x128_f8f6f4 v[142:145], v[10:17], v[210:217], v[142:145], v1, v1 op_sel_hi:[0,0,0]
	v_mfma_scale_f32_16x16x128_f8f6f4 v[134:137], v[2:9], v[218:225], v[134:137], v1, v1 op_sel_hi:[0,0,0]
	v_mfma_scale_f32_16x16x128_f8f6f4 v[126:129], v[10:17], v[218:225], v[126:129], v1, v1 op_sel_hi:[0,0,0]
	v_mfma_scale_f32_16x16x128_f8f6f4 v[118:121], v[2:9], v[226:233], v[118:121], v1, v1 op_sel_hi:[0,0,0]
	v_mfma_scale_f32_16x16x128_f8f6f4 v[110:113], v[10:17], v[226:233], v[110:113], v1, v1 op_sel_hi:[0,0,0]
	s_setprio 0
	s_setprio 1
	v_mfma_scale_f32_16x16x128_f8f6f4 v[146:149], v[18:25], v[202:209], v[146:149], v1, v1 op_sel_hi:[0,0,0]
	v_mfma_scale_f32_16x16x128_f8f6f4 v[138:141], v[26:33], v[202:209], v[138:141], v1, v1 op_sel_hi:[0,0,0]
	v_mfma_scale_f32_16x16x128_f8f6f4 v[130:133], v[18:25], v[210:217], v[130:133], v1, v1 op_sel_hi:[0,0,0]
	v_mfma_scale_f32_16x16x128_f8f6f4 v[122:125], v[26:33], v[210:217], v[122:125], v1, v1 op_sel_hi:[0,0,0]
	v_mfma_scale_f32_16x16x128_f8f6f4 v[114:117], v[18:25], v[218:225], v[114:117], v1, v1 op_sel_hi:[0,0,0]
	v_mfma_scale_f32_16x16x128_f8f6f4 v[106:109], v[26:33], v[218:225], v[106:109], v1, v1 op_sel_hi:[0,0,0]
	v_mfma_scale_f32_16x16x128_f8f6f4 v[102:105], v[18:25], v[226:233], v[102:105], v1, v1 op_sel_hi:[0,0,0]
	v_mfma_scale_f32_16x16x128_f8f6f4 v[98:101], v[26:33], v[226:233], v[98:101], v1, v1 op_sel_hi:[0,0,0]
	s_setprio 0
	s_barrier
	s_add_i32 s44, s74, s4
	v_lshl_add_u64 v[188:189], v[188:189], 0, s[16:17]
	s_mov_b32 m0, s44
	ds_read_b128 v[202:205], v200 offset:49152
	ds_read_b128 v[206:209], v200 offset:50176
	ds_read_b128 v[210:213], v200 offset:51200
	ds_read_b128 v[214:217], v200 offset:52224
	ds_read_b128 v[218:221], v200 offset:53248
	ds_read_b128 v[222:225], v200 offset:54272
	ds_read_b128 v[226:229], v200 offset:55296
	ds_read_b128 v[230:233], v200 offset:56320
	global_load_lds_dwordx4 v[188:189], off
	v_lshl_add_u64 v[186:187], v[186:187], 0, s[16:17]
	s_add_i32 m0, s44, 0x2000
	v_lshl_add_u64 v[184:185], v[184:185], 0, s[18:19]
	s_add_i32 s44, s75, s4
	global_load_lds_dwordx4 v[186:187], off
	v_lshl_add_u64 v[186:187], v[184:185], 0, v[170:171]
	s_mov_b32 m0, s44
	v_lshl_add_u64 v[184:185], v[184:185], 0, v[164:165]
	global_load_lds_dwordx4 v[186:187], off
	s_add_i32 m0, s44, 0x2000
	s_nop 0
	global_load_lds_dwordx4 v[184:185], off
	v_lshl_add_u64 v[184:185], v[190:191], 0, s[16:17]
	s_mov_b32 m0, s52
	s_nop 0
	global_load_lds_dwordx4 v[184:185], off
	v_lshl_add_u64 v[184:185], v[192:193], 0, s[16:17]
	s_mov_b32 m0, s53
	s_nop 0
	global_load_lds_dwordx4 v[184:185], off
	s_waitcnt vmcnt(8)
	s_waitcnt lgkmcnt(0)
	s_barrier
	s_setprio 1
	s_waitcnt lgkmcnt(0)
	v_mfma_scale_f32_16x16x128_f8f6f4 v[94:97], v[2:9], v[202:209], v[94:97], v1, v1 op_sel_hi:[0,0,0]
	v_mfma_scale_f32_16x16x128_f8f6f4 v[90:93], v[10:17], v[202:209], v[90:93], v1, v1 op_sel_hi:[0,0,0]
	v_mfma_scale_f32_16x16x128_f8f6f4 v[86:89], v[2:9], v[210:217], v[86:89], v1, v1 op_sel_hi:[0,0,0]
	v_mfma_scale_f32_16x16x128_f8f6f4 v[78:81], v[10:17], v[210:217], v[78:81], v1, v1 op_sel_hi:[0,0,0]
	v_mfma_scale_f32_16x16x128_f8f6f4 v[62:65], v[2:9], v[218:225], v[62:65], v1, v1 op_sel_hi:[0,0,0]
	v_mfma_scale_f32_16x16x128_f8f6f4 v[54:57], v[10:17], v[218:225], v[54:57], v1, v1 op_sel_hi:[0,0,0]
	v_mfma_scale_f32_16x16x128_f8f6f4 v[46:49], v[2:9], v[226:233], v[46:49], v1, v1 op_sel_hi:[0,0,0]
	v_mfma_scale_f32_16x16x128_f8f6f4 v[38:41], v[10:17], v[226:233], v[38:41], v1, v1 op_sel_hi:[0,0,0]
	s_setprio 0
	s_setprio 1
	v_mfma_scale_f32_16x16x128_f8f6f4 v[82:85], v[18:25], v[202:209], v[82:85], v1, v1 op_sel_hi:[0,0,0]
	v_mfma_scale_f32_16x16x128_f8f6f4 v[74:77], v[26:33], v[202:209], v[74:77], v1, v1 op_sel_hi:[0,0,0]
	v_mfma_scale_f32_16x16x128_f8f6f4 v[58:61], v[18:25], v[210:217], v[58:61], v1, v1 op_sel_hi:[0,0,0]
	v_mfma_scale_f32_16x16x128_f8f6f4 v[50:53], v[26:33], v[210:217], v[50:53], v1, v1 op_sel_hi:[0,0,0]
	v_mfma_scale_f32_16x16x128_f8f6f4 v[42:45], v[18:25], v[218:225], v[42:45], v1, v1 op_sel_hi:[0,0,0]
	v_mfma_scale_f32_16x16x128_f8f6f4 v[34:37], v[26:33], v[218:225], v[34:37], v1, v1 op_sel_hi:[0,0,0]
	v_mfma_scale_f32_16x16x128_f8f6f4 v[70:73], v[18:25], v[226:233], v[70:73], v1, v1 op_sel_hi:[0,0,0]
	v_mfma_scale_f32_16x16x128_f8f6f4 v[66:69], v[26:33], v[226:233], v[66:69], v1, v1 op_sel_hi:[0,0,0]
	s_setprio 0
	s_add_i32 s71, s71, 2
	s_cmp_gt_u32 s71, 19
	s_mov_b64 s[44:45], s[42:43]
	s_barrier
	s_cbranch_scc0 .LBB0_2387
	s_and_b64 vcc, exec, s[20:21]
	s_cbranch_vccz .LBB0_2390
	s_barrier
